# speedup vs baseline: 1.0319x; 1.0257x over previous
.LBB0_3:
	v_and_b32_e32 v2, 63, v0
	v_bfe_u32 v77, v0, 5, 1
	v_lshrrev_b32_e32 v126, 6, v0
	s_cmpk_lt_i32 s2, 0x100
	v_lshlrev_b32_e32 v78, 4, v0
	v_lshlrev_b32_e32 v74, 4, v2
	v_lshlrev_b32_e32 v76, 3, v77
	s_cbranch_scc0 .LBB0_5
	s_load_dwordx2 s[12:13], s[0:1], 0x0
	s_load_dwordx2 s[10:11], s[0:1], 0x10
	s_load_dwordx2 s[6:7], s[0:1], 0x20
	s_ashr_i32 s4, s2, 1
	s_ashr_i32 s5, s4, 31
	s_lshl_b32 s3, s2, 9
	s_lshl_b64 s[14:15], s[4:5], 13
	s_waitcnt lgkmcnt(0)
	s_add_u32 s12, s12, s14
	s_addc_u32 s13, s13, s15
	v_mov_b32_e32 v79, 0
	v_lshl_add_u64 v[2:3], s[12:13], 0, v[78:79]
	s_movk_i32 s5, 0x1000
	v_add_co_u32_e32 v2, vcc, s5, v2
	s_and_b32 s3, s3, 0x200
	s_nop 0
	v_addc_co_u32_e32 v3, vcc, 0, v3, vcc
	v_lshl_or_b32 v108, v126, 7, s3
	global_load_dwordx4 v[6:9], v78, s[12:13]
	global_load_dwordx4 v[10:13], v[2:3], off
	v_lshlrev_b32_e32 v2, 8, v108
	v_mov_b32_e32 v3, v79
	v_lshl_add_u64 v[2:3], s[8:9], 0, v[2:3]
	v_mov_b32_e32 v75, v79
	v_lshl_add_u64 v[2:3], v[2:3], 0, v[74:75]
	global_load_dwordx4 v[84:87], v[2:3], off
	global_load_dwordx4 v[88:91], v[2:3], off offset:1024
	global_load_dwordx4 v[92:95], v[2:3], off offset:2048
	global_load_dwordx4 v[96:99], v[2:3], off offset:3072
	v_add_co_u32_e32 v4, vcc, s5, v2
	s_movk_i32 s3, 0x2000
	s_nop 0
	v_addc_co_u32_e32 v5, vcc, 0, v3, vcc
	v_add_co_u32_e32 v14, vcc, s3, v2
	s_movk_i32 s3, 0x3000
	s_nop 0
	v_addc_co_u32_e32 v15, vcc, 0, v3, vcc
	global_load_dwordx4 v[100:103], v[4:5], off offset:1024
	global_load_dwordx4 v[104:107], v[4:5], off offset:2048
	global_load_dwordx4 v[118:121], v[14:15], off offset:-4096
	global_load_dwordx4 v[128:131], v[14:15], off
	global_load_dwordx4 v[132:135], v[14:15], off offset:1024
	global_load_dwordx4 v[136:139], v[14:15], off offset:2048
	v_add_co_u32_e32 v16, vcc, s3, v2
	s_movk_i32 s3, 0x4000
	s_nop 0
	v_addc_co_u32_e32 v17, vcc, 0, v3, vcc
	v_add_co_u32_e32 v18, vcc, s3, v2
	s_movk_i32 s3, 0x5000
	s_nop 0
	v_addc_co_u32_e32 v19, vcc, 0, v3, vcc
	global_load_dwordx4 v[140:143], v[14:15], off offset:3072
	global_load_dwordx4 v[144:147], v[18:19], off offset:-4096
	global_load_dwordx4 v[148:151], v[4:5], off offset:3072
	global_load_dwordx4 v[152:155], v[16:17], off offset:1024
	global_load_dwordx4 v[156:159], v[16:17], off offset:2048
	global_load_dwordx4 v[160:163], v[16:17], off offset:3072
	global_load_dwordx4 v[70:73], v[18:19], off
	global_load_dwordx4 v[66:69], v[18:19], off offset:1024
	global_load_dwordx4 v[62:65], v[18:19], off offset:2048
	global_load_dwordx4 v[54:57], v[18:19], off offset:3072
	v_add_co_u32_e32 v4, vcc, s3, v2
	s_movk_i32 s3, 0x6000
	s_nop 0
	v_addc_co_u32_e32 v5, vcc, 0, v3, vcc
	v_add_co_u32_e32 v14, vcc, s3, v2
	s_movk_i32 s3, 0x7000
	s_nop 0
	v_addc_co_u32_e32 v15, vcc, 0, v3, vcc
	global_load_dwordx4 v[50:53], v[4:5], off offset:1024
	global_load_dwordx4 v[42:45], v[4:5], off offset:2048
	global_load_dwordx4 v[58:61], v[14:15], off offset:-4096
	global_load_dwordx4 v[38:41], v[14:15], off
	global_load_dwordx4 v[34:37], v[14:15], off offset:1024
	global_load_dwordx4 v[30:33], v[14:15], off offset:2048
	global_load_dwordx4 v[26:29], v[14:15], off offset:3072
	v_add_co_u32_e32 v2, vcc, s3, v2
	v_lshlrev_b32_e32 v75, 3, v0
	s_nop 0
	v_addc_co_u32_e32 v3, vcc, 0, v3, vcc
	global_load_dwordx4 v[46:49], v[4:5], off offset:3072
	global_load_dwordx4 v[22:25], v[2:3], off
	global_load_dwordx4 v[18:21], v[2:3], off offset:1024
	global_load_dwordx4 v[14:17], v[2:3], off offset:2048
	s_nop 0
	global_load_dwordx4 v[2:5], v[2:3], off offset:3072
	v_bfe_u32 v80, v0, 1, 3
	v_and_b32_e32 v110, 8, v75
	v_mul_u32_u24_e32 v111, 0x210, v80
	v_or_b32_e32 v75, v111, v110
	v_and_b32_e32 v80, 0xf0, v0
	v_add_u32_e32 v164, v75, v80
	s_movk_i32 s5, 0x1f0
	v_mov_b32_e32 v80, 0x100
	v_bitop3_b32 v80, v0, s5, v80 bitop3:0xc8
	s_movk_i32 s3, 0x210
	v_add_u32_e32 v165, v75, v80
	v_lshlrev_b32_e32 v75, 4, v1
	v_mul_u32_u24_e32 v109, 0x1080, v126
	v_mul_u32_u24_e32 v166, 0x210, v77
	v_mad_u32_u24 v167, v77, s3, v75
	v_lshlrev_b32_e32 v82, 4, v77
	v_and_b32_e32 v77, 48, v0
	v_add3_u32 v77, v109, v111, v77
	v_mov_b32_e32 v81, v79
	v_mov_b32_e32 v83, v79
	v_or_b32_e32 v127, v77, v110
	v_mov_b32_e32 v77, v79
	v_lshlrev_b32_e32 v80, 2, v108
	v_lshl_add_u64 v[80:81], s[10:11], 0, v[80:81]
	v_lshl_add_u64 v[82:83], v[80:81], 0, v[82:83]
	v_lshl_add_u64 v[80:81], s[6:7], 0, v[76:77]
	s_waitcnt vmcnt(33)
	v_cvt_f16_f32_e32 v6, v6
	v_cvt_f16_f32_e32 v9, v9
	s_waitcnt vmcnt(32)
	v_cvt_f16_f32_e32 v10, v10
	v_cvt_f16_f32_e32 v13, v13
	s_waitcnt vmcnt(31)
	v_cvt_f16_f32_e32 v79, v84
	v_cvt_f16_f32_e32 v77, v87
	v_cvt_pk_f16_f32 v84, v85, v86
	v_pack_b32_f16 v110, v79, v84
	s_waitcnt vmcnt(30)
	v_cvt_f16_f32_e32 v79, v88
	v_alignbit_b32 v111, v77, v84, 16
	v_cvt_f16_f32_e32 v77, v91
	v_cvt_pk_f16_f32 v84, v89, v90
	v_pack_b32_f16 v112, v79, v84
	s_waitcnt vmcnt(29)
	v_cvt_f16_f32_e32 v79, v92
	v_alignbit_b32 v113, v77, v84, 16
	v_cvt_f16_f32_e32 v77, v95
	v_cvt_pk_f16_f32 v84, v93, v94
	v_pack_b32_f16 v114, v79, v84
	s_waitcnt vmcnt(28)
	v_cvt_f16_f32_e32 v79, v96
	v_alignbit_b32 v115, v77, v84, 16
	v_cvt_f16_f32_e32 v77, v99
	v_cvt_pk_f16_f32 v84, v97, v98
	v_pack_b32_f16 v116, v79, v84
	s_waitcnt vmcnt(25)
	v_cvt_f16_f32_e32 v79, v118
	v_alignbit_b32 v117, v77, v84, 16
	v_cvt_f16_f32_e32 v77, v121
	v_cvt_pk_f16_f32 v84, v119, v120
	v_pack_b32_f16 v118, v79, v84
	v_cvt_f16_f32_e32 v79, v100
	v_alignbit_b32 v119, v77, v84, 16
	v_cvt_f16_f32_e32 v77, v103
	v_cvt_pk_f16_f32 v84, v101, v102
	v_pack_b32_f16 v120, v79, v84
	v_cvt_f16_f32_e32 v79, v104
	v_alignbit_b32 v121, v77, v84, 16
	v_cvt_pk_f16_f32 v77, v105, v106
	v_cvt_f16_f32_e32 v84, v107
	v_pack_b32_f16 v122, v79, v77
	s_waitcnt vmcnt(19)
	v_cvt_f16_f32_e32 v79, v148
	v_cvt_f16_f32_e32 v85, v151
	v_alignbit_b32 v123, v84, v77, 16
	v_cvt_pk_f16_f32 v77, v149, v150
	v_pack_b32_f16 v124, v79, v77
	v_lshrrev_b32_e32 v79, 4, v108
	v_lshl_or_b32 v84, s4, 6, v79
	v_alignbit_b32 v125, v85, v77, 16
	v_ashrrev_i32_e32 v85, 31, v84
	v_lshlrev_b64 v[86:87], 10, v[84:85]
	v_or_b32_e32 v86, v86, v75
	v_lshl_add_u64 v[92:93], v[80:81], 0, v[86:87]
	v_or_b32_e32 v86, 1, v84
	v_ashrrev_i32_e32 v87, 31, v86
	v_cvt_f16_f32_e32 v79, v128
	v_cvt_f16_f32_e32 v85, v131
	v_lshlrev_b64 v[86:87], 10, v[86:87]
	v_or_b32_e32 v86, v86, v75
	v_lshl_add_u64 v[90:91], v[80:81], 0, v[86:87]
	v_cvt_pk_f16_f32 v86, v129, v130
	v_pack_b32_f16 v96, v79, v86
	v_cvt_f16_f32_e32 v79, v132
	v_alignbit_b32 v97, v85, v86, 16
	v_cvt_f16_f32_e32 v85, v135
	v_cvt_pk_f16_f32 v86, v133, v134
	v_pack_b32_f16 v100, v79, v86
	v_cvt_f16_f32_e32 v79, v136
	v_alignbit_b32 v101, v85, v86, 16
	v_cvt_f16_f32_e32 v85, v139
	v_cvt_pk_f16_f32 v86, v137, v138
	v_pack_b32_f16 v106, v79, v86
	v_cvt_f16_f32_e32 v79, v140
	v_alignbit_b32 v107, v85, v86, 16
	v_cvt_f16_f32_e32 v85, v143
	v_cvt_pk_f16_f32 v86, v141, v142
	v_pack_b32_f16 v94, v79, v86
	v_cvt_f16_f32_e32 v79, v144
	v_alignbit_b32 v95, v85, v86, 16
	v_cvt_f16_f32_e32 v85, v147
	v_cvt_pk_f16_f32 v86, v145, v146
	v_pack_b32_f16 v98, v79, v86
	s_waitcnt vmcnt(18)
	v_cvt_f16_f32_e32 v79, v152
	v_alignbit_b32 v99, v85, v86, 16
	v_cvt_f16_f32_e32 v85, v155
	s_waitcnt vmcnt(10)
	v_cvt_f16_f32_e32 v42, v42
	v_cvt_pk_f16_f32 v86, v153, v154
	v_cvt_f16_f32_e32 v50, v50
	v_cvt_f16_f32_e32 v53, v53
	v_cvt_pk_f16_f32 v43, v43, v44
	v_cvt_f16_f32_e32 v44, v45
	v_pack_b32_f16 v102, v79, v86
	v_cvt_f16_f32_e32 v79, v156
	v_alignbit_b32 v103, v85, v86, 16
	v_cvt_f16_f32_e32 v86, v159
	v_cvt_pk_f16_f32 v51, v51, v52
	v_pack_b32_f16 v52, v42, v43
	s_waitcnt vmcnt(4)
	v_cvt_f16_f32_e32 v42, v46
	v_cvt_f16_f32_e32 v87, v163
	v_cvt_f16_f32_e32 v45, v49
	v_cvt_pk_f16_f32 v85, v157, v158
	v_pack_b32_f16 v50, v50, v51
	v_alignbit_b32 v51, v53, v51, 16
	v_alignbit_b32 v53, v44, v43, 16
	v_cvt_pk_f16_f32 v43, v47, v48
	v_pack_b32_f16 v104, v79, v85
	v_alignbit_b32 v105, v86, v85, 16
	v_cvt_pk_f16_f32 v85, v161, v162
	v_or_b32_e32 v86, 2, v84
	v_cvt_f16_f32_e32 v54, v54
	v_cvt_f16_f32_e32 v57, v57
	v_pack_b32_f16 v46, v42, v43
	v_or_b32_e32 v42, 4, v84
	v_add3_u32 v77, v109, v75, v166
	v_alignbit_b32 v109, v87, v85, 16
	v_ashrrev_i32_e32 v87, 31, v86
	v_alignbit_b32 v47, v45, v43, 16
	v_ashrrev_i32_e32 v43, 31, v42
	v_lshlrev_b64 v[86:87], 10, v[86:87]
	v_lshlrev_b64 v[42:43], 10, v[42:43]
	v_or_b32_e32 v86, v86, v75
	v_cvt_pk_f16_f32 v55, v55, v56
	v_or_b32_e32 v42, v42, v75
	v_cvt_f16_f32_e32 v79, v160
	v_lshl_add_u64 v[88:89], v[80:81], 0, v[86:87]
	v_or_b32_e32 v86, 3, v84
	v_cvt_f16_f32_e32 v70, v70
	v_cvt_f16_f32_e32 v73, v73
	v_cvt_f16_f32_e32 v66, v66
	v_cvt_f16_f32_e32 v69, v69
	v_cvt_f16_f32_e32 v62, v62
	v_cvt_f16_f32_e32 v65, v65
	v_pack_b32_f16 v54, v54, v55
	v_cvt_f16_f32_e32 v56, v58
	v_alignbit_b32 v55, v57, v55, 16
	v_cvt_f16_f32_e32 v57, v61
	v_lshl_add_u64 v[44:45], v[80:81], 0, v[42:43]
	v_or_b32_e32 v42, 5, v84
	v_cvt_f16_f32_e32 v38, v38
	v_cvt_f16_f32_e32 v41, v41
	v_cvt_f16_f32_e32 v34, v34
	v_cvt_f16_f32_e32 v37, v37
	v_cvt_f16_f32_e32 v30, v30
	v_cvt_f16_f32_e32 v33, v33
	v_cvt_f16_f32_e32 v26, v26
	v_cvt_f16_f32_e32 v29, v29
	s_waitcnt vmcnt(3)
	v_cvt_f16_f32_e32 v22, v22
	v_cvt_pk_f16_f32 v23, v23, v24
	v_cvt_f16_f32_e32 v24, v25
	s_waitcnt vmcnt(2)
	v_cvt_f16_f32_e32 v18, v18
	v_cvt_f16_f32_e32 v21, v21
	s_waitcnt vmcnt(1)
	v_cvt_f16_f32_e32 v14, v14
	v_cvt_f16_f32_e32 v17, v17
	v_ashrrev_i32_e32 v87, 31, v86
	v_ashrrev_i32_e32 v43, 31, v42
	v_lshlrev_b64 v[86:87], 10, v[86:87]
	v_lshlrev_b64 v[42:43], 10, v[42:43]
	v_or_b32_e32 v86, v86, v75
	v_cvt_pk_f16_f32 v71, v71, v72
	v_cvt_pk_f16_f32 v67, v67, v68
	v_cvt_pk_f16_f32 v63, v63, v64
	v_cvt_pk_f16_f32 v58, v59, v60
	v_or_b32_e32 v42, v42, v75
	v_cvt_pk_f16_f32 v39, v39, v40
	v_cvt_pk_f16_f32 v35, v35, v36
	v_cvt_pk_f16_f32 v31, v31, v32
	v_cvt_pk_f16_f32 v27, v27, v28
	v_cvt_pk_f16_f32 v19, v19, v20
	v_cvt_pk_f16_f32 v15, v15, v16
	v_pack_b32_f16 v108, v79, v85
	v_lshl_add_u64 v[86:87], v[80:81], 0, v[86:87]
	v_pack_b32_f16 v70, v70, v71
	v_alignbit_b32 v71, v73, v71, 16
	v_pack_b32_f16 v66, v66, v67
	v_alignbit_b32 v67, v69, v67, 16
	v_pack_b32_f16 v62, v62, v63
	v_alignbit_b32 v63, v65, v63, 16
	v_pack_b32_f16 v56, v56, v58
	v_alignbit_b32 v57, v57, v58, 16
	v_lshl_add_u64 v[42:43], v[80:81], 0, v[42:43]
	v_pack_b32_f16 v38, v38, v39
	v_alignbit_b32 v39, v41, v39, 16
	v_pack_b32_f16 v34, v34, v35
	v_alignbit_b32 v35, v37, v35, 16
	v_pack_b32_f16 v30, v30, v31
	v_alignbit_b32 v31, v33, v31, 16
	v_pack_b32_f16 v26, v26, v27
	v_alignbit_b32 v27, v29, v27, 16
	v_pack_b32_f16 v22, v22, v23
	v_alignbit_b32 v23, v24, v23, 16
	v_pack_b32_f16 v24, v18, v19
	v_alignbit_b32 v25, v21, v19, 16
	s_waitcnt vmcnt(0)
	v_cvt_f16_f32_e32 v2, v2
	v_pack_b32_f16 v28, v14, v15
	v_alignbit_b32 v29, v17, v15, 16
	v_cvt_pk_f16_f32 v7, v7, v8
	v_pack_b32_f16 v6, v6, v7
	v_alignbit_b32 v7, v9, v7, 16
	ds_write_b64 v164, v[6:7]
	v_cvt_pk_f16_f32 v7, v11, v12
	v_pack_b32_f16 v6, v10, v7
	v_alignbit_b32 v7, v13, v7, 16
	ds_write_b64 v165, v[6:7]
	s_waitcnt lgkmcnt(0)
	s_barrier
	ds_read_b128 v[18:21], v167
	ds_read_b128 v[14:17], v167 offset:1056
	ds_read_b128 v[10:13], v167 offset:2112
	ds_read_b128 v[6:9], v167 offset:3168
	ds_write_b64 v127, v[110:111] offset:4224
	ds_write_b64 v127, v[112:113] offset:4288
	ds_write_b64 v127, v[114:115] offset:4352
	ds_write_b64 v127, v[116:117] offset:4416
	ds_write_b64 v127, v[118:119] offset:4480
	ds_write_b64 v127, v[120:121] offset:4544
	ds_write_b64 v127, v[122:123] offset:4608
	ds_write_b64 v127, v[124:125] offset:4672
	ds_read_b128 v[58:61], v77 offset:4224
	ds_read_b128 v[110:113], v77 offset:5280
	s_waitcnt lgkmcnt(1)
	v_mfma_f32_32x32x16_f16 a[0:15], v[58:61], v[18:21], 0
	ds_read_b128 v[58:61], v77 offset:6336
	s_mov_b32 s4, 0x4038aa3b
	v_cvt_f16_f32_e32 v5, v5
	v_cvt_pk_f16_f32 v3, v3, v4
	v_pack_b32_f16 v2, v2, v3
	v_alignbit_b32 v3, v5, v3, 16
	s_waitcnt lgkmcnt(1)
	v_mfma_f32_32x32x16_f16 a[0:15], v[110:113], v[14:17], a[0:15]
	global_load_dwordx4 v[110:113], v[82:83], off
	global_load_dwordx4 v[114:117], v[82:83], off offset:32
	ds_read_b128 v[118:121], v77 offset:7392
	s_waitcnt lgkmcnt(1)
	v_mfma_f32_32x32x16_f16 a[0:15], v[58:61], v[10:13], a[0:15]
	global_load_dwordx4 v[58:61], v[82:83], off offset:64
	global_load_dwordx4 v[122:125], v[82:83], off offset:96
	global_load_dwordx4 v[128:131], v[82:83], off offset:128
	s_waitcnt lgkmcnt(0)
	v_mfma_f32_32x32x16_f16 a[0:15], v[118:121], v[6:9], a[0:15]
	s_nop 11
	v_accvgpr_read_b32 v49, a1
	v_accvgpr_read_b32 v41, a3
	v_accvgpr_read_b32 v40, a2
	v_accvgpr_read_b32 v48, a0
	v_accvgpr_read_b32 v65, a7
	v_accvgpr_read_b32 v64, a6
	v_accvgpr_read_b32 v73, a11
	v_accvgpr_read_b32 v72, a10
	v_accvgpr_read_b32 v119, a9
	v_accvgpr_read_b32 v118, a8
	v_accvgpr_read_b32 v69, a5
	v_accvgpr_read_b32 v68, a4
	v_accvgpr_read_b32 v33, a15
	v_accvgpr_read_b32 v32, a14
	v_accvgpr_read_b32 v37, a13
	v_accvgpr_read_b32 v36, a12
	s_waitcnt vmcnt(4)
	v_pk_add_f32 v[48:49], v[48:49], v[110:111]
	v_pk_add_f32 v[40:41], v[40:41], v[112:113]
	v_pk_mul_f32 v[48:49], v[48:49], s[4:5] op_sel_hi:[1,0]
	v_pk_mul_f32 v[40:41], v[40:41], s[4:5] op_sel_hi:[1,0]
	s_waitcnt vmcnt(3)
	v_pk_add_f32 v[64:65], v[64:65], v[116:117]
	v_exp_f32_e32 v48, v48
	v_exp_f32_e32 v49, v49
	v_exp_f32_e32 v40, v40
	v_exp_f32_e32 v41, v41
	v_pk_mul_f32 v[64:65], v[64:65], s[4:5] op_sel_hi:[1,0]
	v_pk_add_f32 v[48:49], v[48:49], 1.0 op_sel_hi:[1,0]
	v_exp_f32_e32 v64, v64
	v_exp_f32_e32 v65, v65
	v_pk_add_f32 v[40:41], v[40:41], 1.0 op_sel_hi:[1,0]
	s_waitcnt vmcnt(2)
	v_pk_add_f32 v[58:59], v[118:119], v[58:59]
	v_pk_add_f32 v[60:61], v[72:73], v[60:61]
	v_rcp_f32_e32 v48, v48
	v_rcp_f32_e32 v49, v49
	v_rcp_f32_e32 v40, v40
	v_rcp_f32_e32 v41, v41
	v_pk_mul_f32 v[58:59], v[58:59], s[4:5] op_sel_hi:[1,0]
	v_pk_mul_f32 v[60:61], v[60:61], s[4:5] op_sel_hi:[1,0]
	v_pk_add_f32 v[64:65], v[64:65], 1.0 op_sel_hi:[1,0]
	v_exp_f32_e32 v58, v58
	v_exp_f32_e32 v59, v59
	v_exp_f32_e32 v60, v60
	v_rcp_f32_e32 v64, v64
	v_rcp_f32_e32 v65, v65
	v_exp_f32_e32 v61, v61
	v_pk_add_f32 v[68:69], v[68:69], v[114:115]
	v_pk_fma_f32 v[48:49], v[48:49], 2.0, 1.0 op_sel_hi:[1,0,0] neg_lo:[1,0,0] neg_hi:[1,0,0]
	v_pk_fma_f32 v[40:41], v[40:41], 2.0, 1.0 op_sel_hi:[1,0,0] neg_lo:[1,0,0] neg_hi:[1,0,0]
	v_pk_mul_f32 v[68:69], v[68:69], s[4:5] op_sel_hi:[1,0]
	v_cvt_pk_f16_f32 v41, v40, v41
	v_cvt_pk_f16_f32 v40, v48, v49
	v_exp_f32_e32 v68, v68
	v_exp_f32_e32 v69, v69
	v_pk_fma_f32 v[64:65], v[64:65], 2.0, 1.0 op_sel_hi:[1,0,0] neg_lo:[1,0,0] neg_hi:[1,0,0]
	global_store_dwordx2 v[92:93], v[40:41], off sc1
	v_pk_add_f32 v[40:41], v[58:59], 1.0 op_sel_hi:[1,0]
	v_pk_add_f32 v[58:59], v[60:61], 1.0 op_sel_hi:[1,0]
	ds_write_b64 v127, v[96:97] offset:4224
	ds_write_b64 v127, v[100:101] offset:4288
	ds_write_b64 v127, v[106:107] offset:4352
	v_cvt_pk_f16_f32 v49, v64, v65
	v_rcp_f32_e32 v64, v58
	v_rcp_f32_e32 v65, v59
	global_load_dwordx4 v[58:61], v[82:83], off offset:160
	ds_write_b64 v127, v[94:95] offset:4416
	ds_write_b64 v127, v[98:99] offset:4480
	ds_write_b64 v127, v[102:103] offset:4544
	ds_write_b64 v127, v[104:105] offset:4608
	ds_write_b64 v127, v[108:109] offset:4672
	ds_read_b128 v[94:97], v77 offset:4224
	ds_read_b128 v[98:101], v77 offset:5280
	v_pk_add_f32 v[68:69], v[68:69], 1.0 op_sel_hi:[1,0]
	s_waitcnt lgkmcnt(1)
	v_mfma_f32_32x32x16_f16 a[0:15], v[94:97], v[18:21], 0
	v_rcp_f32_e32 v68, v68
	v_rcp_f32_e32 v69, v69
	ds_read_b128 v[102:105], v77 offset:6336
	s_waitcnt vmcnt(3)
	v_pk_add_f32 v[36:37], v[36:37], v[122:123]
	v_pk_add_f32 v[32:33], v[32:33], v[124:125]
	v_pk_fma_f32 v[68:69], v[68:69], 2.0, 1.0 op_sel_hi:[1,0,0] neg_lo:[1,0,0] neg_hi:[1,0,0]
	v_pk_mul_f32 v[36:37], v[36:37], s[4:5] op_sel_hi:[1,0]
	v_cvt_pk_f16_f32 v48, v68, v69
	global_store_dwordx2 v[92:93], v[48:49], off offset:512 sc1
	global_load_dwordx4 v[92:95], v[82:83], off offset:192
	s_waitcnt lgkmcnt(1)
	v_mfma_f32_32x32x16_f16 a[0:15], v[98:101], v[14:17], a[0:15]
	ds_read_b128 v[96:99], v77 offset:7392
	v_mul_f32_e64 v32, v32, s4
	v_mul_f32_e64 v33, v33, s4
	v_exp_f32_e32 v36, v36
	v_exp_f32_e32 v37, v37
	v_exp_f32_e32 v32, v32
	v_exp_f32_e32 v33, v33
	v_rcp_f32_e32 v40, v40
	s_waitcnt lgkmcnt(1)
	v_mfma_f32_32x32x16_f16 a[0:15], v[102:105], v[10:13], a[0:15]
	v_add_f32_e64 v36, v36, 1.0
	v_add_f32_e64 v37, v37, 1.0
	v_add_f32_e64 v32, v32, 1.0
	v_add_f32_e64 v33, v33, 1.0
	v_rcp_f32_e32 v41, v41
	v_rcp_f32_e32 v36, v36
	v_rcp_f32_e32 v37, v37
	v_rcp_f32_e32 v32, v32
	v_rcp_f32_e32 v33, v33
	s_waitcnt lgkmcnt(0)
	v_mfma_f32_32x32x16_f16 a[0:15], v[96:99], v[6:9], a[0:15]
	v_fma_f32 v40, -v40, 2.0, 1.0
	v_fma_f32 v41, -v41, 2.0, 1.0
	v_fma_f32 v48, -v64, 2.0, 1.0
	v_fma_f32 v49, -v65, 2.0, 1.0
	v_fma_f32 v36, -v36, 2.0, 1.0
	v_fma_f32 v37, -v37, 2.0, 1.0
	v_pk_fma_f32 v[32:33], v[32:33], 2.0, 1.0 op_sel_hi:[1,0,0] neg_lo:[1,0,0] neg_hi:[1,0,0]
	v_cvt_pk_f16_f32 v40, v40, v41
	v_cvt_pk_f16_f32 v41, v48, v49
	v_cvt_pk_f16_f32 v36, v36, v37
	v_cvt_pk_f16_f32 v37, v32, v33
	global_store_dwordx2 v[90:91], v[40:41], off sc1
	global_store_dwordx2 v[90:91], v[36:37], off offset:512 sc1
	global_load_dwordx4 v[96:99], v[82:83], off offset:224
	v_accvgpr_read_b32 v73, a1
	v_accvgpr_read_b32 v69, a3
	v_accvgpr_read_b32 v68, a2
	v_accvgpr_read_b32 v72, a0
	s_waitcnt vmcnt(7)
	v_pk_add_f32 v[72:73], v[72:73], v[128:129]
	v_pk_add_f32 v[68:69], v[68:69], v[130:131]
	v_accvgpr_read_b32 v91, a5
	v_accvgpr_read_b32 v90, a4
	v_accvgpr_read_b32 v65, a7
	v_accvgpr_read_b32 v64, a6
	v_pk_mul_f32 v[72:73], v[72:73], s[4:5] op_sel_hi:[1,0]
	v_pk_mul_f32 v[68:69], v[68:69], s[4:5] op_sel_hi:[1,0]
	v_exp_f32_e32 v72, v72
	v_exp_f32_e32 v73, v73
	v_exp_f32_e32 v68, v68
	v_exp_f32_e32 v69, v69
	v_accvgpr_read_b32 v49, a9
	v_pk_add_f32 v[72:73], v[72:73], 1.0 op_sel_hi:[1,0]
	v_accvgpr_read_b32 v48, a8
	v_pk_add_f32 v[68:69], v[68:69], 1.0 op_sel_hi:[1,0]
	v_rcp_f32_e32 v72, v72
	v_rcp_f32_e32 v73, v73
	v_rcp_f32_e32 v68, v68
	v_rcp_f32_e32 v69, v69
	v_accvgpr_read_b32 v33, a15
	v_pk_fma_f32 v[72:73], v[72:73], 2.0, 1.0 op_sel_hi:[1,0,0] neg_lo:[1,0,0] neg_hi:[1,0,0]
	v_accvgpr_read_b32 v32, a14
	v_pk_fma_f32 v[68:69], v[68:69], 2.0, 1.0 op_sel_hi:[1,0,0] neg_lo:[1,0,0] neg_hi:[1,0,0]
	v_accvgpr_read_b32 v37, a13
	s_waitcnt vmcnt(5)
	v_pk_add_f32 v[58:59], v[90:91], v[58:59]
	v_pk_add_f32 v[60:61], v[64:65], v[60:61]
	v_pk_mul_f32 v[58:59], v[58:59], s[4:5] op_sel_hi:[1,0]
	v_pk_mul_f32 v[60:61], v[60:61], s[4:5] op_sel_hi:[1,0]
	v_exp_f32_e32 v58, v58
	v_exp_f32_e32 v59, v59
	v_exp_f32_e32 v60, v60
	v_exp_f32_e32 v61, v61
	v_cvt_pk_f16_f32 v69, v68, v69
	v_pk_add_f32 v[58:59], v[58:59], 1.0 op_sel_hi:[1,0]
	v_cvt_pk_f16_f32 v68, v72, v73
	v_rcp_f32_e32 v58, v58
	v_rcp_f32_e32 v59, v59
	v_pk_add_f32 v[60:61], v[60:61], 1.0 op_sel_hi:[1,0]
	global_store_dwordx2 v[88:89], v[68:69], off sc1
	v_rcp_f32_e32 v60, v60
	v_rcp_f32_e32 v61, v61
	v_pk_fma_f32 v[58:59], v[58:59], 2.0, 1.0 op_sel_hi:[1,0,0] neg_lo:[1,0,0] neg_hi:[1,0,0]
	v_accvgpr_read_b32 v36, a12
	v_cvt_pk_f16_f32 v68, v58, v59
	v_pk_fma_f32 v[64:65], v[60:61], 2.0, 1.0 op_sel_hi:[1,0,0] neg_lo:[1,0,0] neg_hi:[1,0,0]
	s_waitcnt vmcnt(4)
	v_pk_add_f32 v[48:49], v[48:49], v[92:93]
	global_load_dwordx4 v[58:61], v[82:83], off offset:256
	v_pk_mul_f32 v[48:49], v[48:49], s[4:5] op_sel_hi:[1,0]
	ds_write_b64 v127, v[70:71] offset:4224
	ds_write_b64 v127, v[66:67] offset:4288
	ds_write_b64 v127, v[62:63] offset:4352
	v_exp_f32_e32 v48, v48
	v_exp_f32_e32 v49, v49
	v_cvt_pk_f16_f32 v69, v64, v65
	global_load_dwordx4 v[62:65], v[82:83], off offset:288
	ds_write_b64 v127, v[54:55] offset:4416
	ds_write_b64 v127, v[56:57] offset:4480
	ds_write_b64 v127, v[50:51] offset:4544
	ds_write_b64 v127, v[52:53] offset:4608
	ds_write_b64 v127, v[46:47] offset:4672
	v_pk_add_f32 v[48:49], v[48:49], 1.0 op_sel_hi:[1,0]
	v_accvgpr_read_b32 v41, a11
	v_rcp_f32_e32 v72, v48
	v_rcp_f32_e32 v73, v49
	ds_read_b128 v[46:49], v77 offset:4224
	v_accvgpr_read_b32 v40, a10
	ds_read_b128 v[54:57], v77 offset:6336
	v_pk_fma_f32 v[50:51], v[72:73], 2.0, 1.0 op_sel_hi:[1,0,0] neg_lo:[1,0,0] neg_hi:[1,0,0]
	v_pk_add_f32 v[40:41], v[40:41], v[94:95]
	v_cvt_pk_f16_f32 v66, v50, v51
	ds_read_b128 v[50:53], v77 offset:5280
	s_waitcnt lgkmcnt(2)
	v_mfma_f32_32x32x16_f16 a[0:15], v[46:49], v[18:21], 0
	global_load_dwordx4 v[46:49], v[82:83], off offset:320
	v_mul_f32_e64 v40, v40, s4
	v_mul_f32_e64 v41, v41, s4
	global_store_dwordx2 v[88:89], v[68:69], off offset:512 sc1
	v_exp_f32_e32 v40, v40
	v_exp_f32_e32 v41, v41
	s_waitcnt vmcnt(5)
	v_pk_add_f32 v[36:37], v[36:37], v[96:97]
	v_pk_add_f32 v[32:33], v[32:33], v[98:99]
	s_waitcnt lgkmcnt(0)
	v_mfma_f32_32x32x16_f16 a[0:15], v[50:53], v[14:17], a[0:15]
	ds_read_b128 v[50:53], v77 offset:7392
	v_add_f32_e64 v40, v40, 1.0
	v_add_f32_e64 v41, v41, 1.0
	v_mul_f32_e64 v36, v36, s4
	v_mul_f32_e64 v37, v37, s4
	v_rcp_f32_e32 v40, v40
	v_rcp_f32_e32 v41, v41
	v_pk_mul_f32 v[32:33], v[32:33], s[4:5] op_sel_hi:[1,0]
	v_exp_f32_e32 v36, v36
	v_mfma_f32_32x32x16_f16 a[0:15], v[54:57], v[10:13], a[0:15]
	v_fma_f32 v40, -v40, 2.0, 1.0
	v_fma_f32 v41, -v41, 2.0, 1.0
	v_exp_f32_e32 v37, v37
	v_cvt_pk_f16_f32 v67, v40, v41
	global_store_dwordx2 v[86:87], v[66:67], off sc1
	v_exp_f32_e32 v32, v32
	v_exp_f32_e32 v33, v33
	v_pk_add_f32 v[36:37], v[36:37], 1.0 op_sel_hi:[1,0]
	s_waitcnt lgkmcnt(0)
	v_mfma_f32_32x32x16_f16 a[0:15], v[50:53], v[6:9], a[0:15]
	global_load_dwordx4 v[50:53], v[82:83], off offset:352
	v_add_f32_e64 v32, v32, 1.0
	v_add_f32_e64 v33, v33, 1.0
	v_rcp_f32_e32 v36, v36
	v_rcp_f32_e32 v37, v37
	v_rcp_f32_e32 v32, v32
	v_rcp_f32_e32 v33, v33
	v_pk_fma_f32 v[36:37], v[36:37], 2.0, 1.0 op_sel_hi:[1,0,0] neg_lo:[1,0,0] neg_hi:[1,0,0]
	s_nop 0
	v_cvt_pk_f16_f32 v36, v36, v37
	v_pk_fma_f32 v[32:33], v[32:33], 2.0, 1.0 op_sel_hi:[1,0,0] neg_lo:[1,0,0] neg_hi:[1,0,0]
	s_nop 0
	v_cvt_pk_f16_f32 v37, v32, v33
	v_accvgpr_read_b32 v69, a1
	v_accvgpr_read_b32 v67, a3
	v_accvgpr_read_b32 v66, a2
	v_accvgpr_read_b32 v68, a0
	v_accvgpr_read_b32 v55, a9
	v_accvgpr_read_b32 v54, a8
	v_accvgpr_read_b32 v41, a11
	v_accvgpr_read_b32 v40, a10
	global_store_dwordx2 v[86:87], v[36:37], off offset:512 sc1
	v_accvgpr_read_b32 v37, a13
	v_accvgpr_read_b32 v36, a12
	v_accvgpr_read_b32 v33, a15
	v_accvgpr_read_b32 v32, a14
	v_accvgpr_read_b32 v57, a7
	v_accvgpr_read_b32 v56, a6
	s_waitcnt vmcnt(6)
	v_pk_add_f32 v[58:59], v[68:69], v[58:59]
	v_pk_add_f32 v[60:61], v[66:67], v[60:61]
	v_pk_mul_f32 v[58:59], v[58:59], s[4:5] op_sel_hi:[1,0]
	v_pk_mul_f32 v[60:61], v[60:61], s[4:5] op_sel_hi:[1,0]
	v_exp_f32_e32 v58, v58
	v_exp_f32_e32 v59, v59
	v_exp_f32_e32 v60, v60
	v_exp_f32_e32 v61, v61
	v_accvgpr_read_b32 v67, a5
	v_pk_add_f32 v[58:59], v[58:59], 1.0 op_sel_hi:[1,0]
	v_accvgpr_read_b32 v66, a4
	v_pk_add_f32 v[60:61], v[60:61], 1.0 op_sel_hi:[1,0]
	v_rcp_f32_e32 v58, v58
	v_rcp_f32_e32 v59, v59
	v_rcp_f32_e32 v60, v60
	v_rcp_f32_e32 v61, v61
	s_waitcnt vmcnt(5)
	v_pk_add_f32 v[62:63], v[66:67], v[62:63]
	v_pk_fma_f32 v[58:59], v[58:59], 2.0, 1.0 op_sel_hi:[1,0,0] neg_lo:[1,0,0] neg_hi:[1,0,0]
	v_pk_add_f32 v[56:57], v[56:57], v[64:65]
	v_pk_fma_f32 v[60:61], v[60:61], 2.0, 1.0 op_sel_hi:[1,0,0] neg_lo:[1,0,0] neg_hi:[1,0,0]
	v_pk_mul_f32 v[62:63], v[62:63], s[4:5] op_sel_hi:[1,0]
	v_cvt_pk_f16_f32 v61, v60, v61
	v_cvt_pk_f16_f32 v60, v58, v59
	s_waitcnt vmcnt(4)
	v_pk_add_f32 v[46:47], v[54:55], v[46:47]
	global_store_dwordx2 v[44:45], v[60:61], off sc1
	v_pk_mul_f32 v[54:55], v[46:47], s[4:5] op_sel_hi:[1,0]
	v_pk_add_f32 v[40:41], v[40:41], v[48:49]
	global_load_dwordx4 v[46:49], v[82:83], off offset:384
	ds_write_b64 v127, v[38:39] offset:4224
	ds_write_b64 v127, v[34:35] offset:4288
	ds_write_b64 v127, v[30:31] offset:4352
	ds_write_b64 v127, v[26:27] offset:4416
	ds_write_b64 v127, v[22:23] offset:4480
	ds_write_b64 v127, v[24:25] offset:4544
	ds_write_b64 v127, v[28:29] offset:4608
	ds_write_b64 v127, v[2:3] offset:4672
	ds_read_b128 v[22:25], v77 offset:4224
	global_load_dwordx4 v[2:5], v[82:83], off offset:416
	v_pk_mul_f32 v[56:57], v[56:57], s[4:5] op_sel_hi:[1,0]
	v_pk_mul_f32 v[40:41], v[40:41], s[4:5] op_sel_hi:[1,0]
	v_exp_f32_e32 v62, v62
	v_exp_f32_e32 v63, v63
	v_exp_f32_e32 v56, v56
	v_exp_f32_e32 v57, v57
	v_exp_f32_e32 v54, v54
	v_exp_f32_e32 v55, v55
	v_exp_f32_e32 v40, v40
	v_exp_f32_e32 v41, v41
	v_pk_add_f32 v[62:63], v[62:63], 1.0 op_sel_hi:[1,0]
	v_pk_add_f32 v[56:57], v[56:57], 1.0 op_sel_hi:[1,0]
	v_pk_add_f32 v[54:55], v[54:55], 1.0 op_sel_hi:[1,0]
	s_waitcnt vmcnt(4)
	v_pk_add_f32 v[26:27], v[36:37], v[50:51]
	v_pk_add_f32 v[40:41], v[40:41], 1.0 op_sel_hi:[1,0]
	v_pk_mul_f32 v[26:27], v[26:27], s[4:5] op_sel_hi:[1,0]
	v_rcp_f32_e32 v62, v62
	v_exp_f32_e32 v36, v26
	v_exp_f32_e32 v37, v27
	ds_read_b128 v[26:29], v77 offset:5280
	s_waitcnt lgkmcnt(1)
	v_mfma_f32_32x32x16_f16 a[0:15], v[22:25], v[18:21], 0
	v_add_f32_e64 v18, v32, v52
	v_add_f32_e64 v19, v33, v53
	v_add_f32_e64 v22, v36, 1.0
	v_add_f32_e64 v23, v37, 1.0
	v_mul_f32_e64 v18, v18, s4
	v_mul_f32_e64 v19, v19, s4
	v_rcp_f32_e32 v63, v63
	v_exp_f32_e32 v24, v18
	v_exp_f32_e32 v25, v19
	ds_read_b128 v[18:21], v77 offset:6336
	s_waitcnt lgkmcnt(1)
	v_mfma_f32_32x32x16_f16 a[0:15], v[26:29], v[14:17], a[0:15]
	v_rcp_f32_e32 v26, v22
	v_rcp_f32_e32 v27, v23
	v_pk_add_f32 v[22:23], v[24:25], 1.0 op_sel_hi:[1,0]
	global_load_dwordx4 v[14:17], v[82:83], off offset:448
	v_rcp_f32_e32 v28, v22
	v_rcp_f32_e32 v29, v23
	ds_read_b128 v[22:25], v77 offset:7392
	s_waitcnt lgkmcnt(1)
	v_mfma_f32_32x32x16_f16 a[0:15], v[18:21], v[10:13], a[0:15]
	v_fma_f32 v10, -v26, 2.0, 1.0
	v_fma_f32 v11, -v27, 2.0, 1.0
	v_fma_f32 v12, -v28, 2.0, 1.0
	v_fma_f32 v13, -v29, 2.0, 1.0
	v_rcp_f32_e32 v56, v56
	v_rcp_f32_e32 v57, v57
	v_rcp_f32_e32 v54, v54
	v_rcp_f32_e32 v55, v55
	v_rcp_f32_e32 v40, v40
	s_waitcnt lgkmcnt(0)
	v_mfma_f32_32x32x16_f16 a[0:15], v[22:25], v[6:9], a[0:15]
	global_load_dwordx4 v[6:9], v[82:83], off offset:480
	v_rcp_f32_e32 v41, v41
	v_pk_fma_f32 v[58:59], v[62:63], 2.0, 1.0 op_sel_hi:[1,0,0] neg_lo:[1,0,0] neg_hi:[1,0,0]
	v_pk_fma_f32 v[56:57], v[56:57], 2.0, 1.0 op_sel_hi:[1,0,0] neg_lo:[1,0,0] neg_hi:[1,0,0]
	v_pk_fma_f32 v[30:31], v[54:55], 2.0, 1.0 op_sel_hi:[1,0,0] neg_lo:[1,0,0] neg_hi:[1,0,0]
	v_pk_fma_f32 v[34:35], v[40:41], 2.0, 1.0 op_sel_hi:[1,0,0] neg_lo:[1,0,0] neg_hi:[1,0,0]
	v_cvt_pk_f16_f32 v10, v10, v11
	v_cvt_pk_f16_f32 v11, v12, v13
	v_cvt_pk_f16_f32 v58, v58, v59
	v_cvt_pk_f16_f32 v59, v56, v57
	v_cvt_pk_f16_f32 v30, v30, v31
	v_cvt_pk_f16_f32 v31, v34, v35
	v_accvgpr_read_b32 v29, a1
	v_accvgpr_read_b32 v27, a3
	v_accvgpr_read_b32 v26, a2
	v_accvgpr_read_b32 v28, a0
	v_accvgpr_read_b32 v23, a7
	v_accvgpr_read_b32 v22, a6
	v_accvgpr_read_b32 v25, a5
	v_accvgpr_read_b32 v24, a4
	v_accvgpr_read_b32 v19, a11
	v_accvgpr_read_b32 v18, a10
	v_accvgpr_read_b32 v21, a9
	v_accvgpr_read_b32 v20, a8
	global_store_dwordx2 v[42:43], v[10:11], off offset:512 sc1
	v_accvgpr_read_b32 v11, a15
	v_accvgpr_read_b32 v10, a14
	v_accvgpr_read_b32 v13, a13
	v_accvgpr_read_b32 v12, a12
	s_waitcnt vmcnt(4)
	v_pk_add_f32 v[28:29], v[28:29], v[46:47]
	v_pk_add_f32 v[26:27], v[26:27], v[48:49]
	v_pk_mul_f32 v[28:29], v[28:29], s[4:5] op_sel_hi:[1,0]
	v_pk_mul_f32 v[26:27], v[26:27], s[4:5] op_sel_hi:[1,0]
	v_exp_f32_e32 v28, v28
	v_exp_f32_e32 v29, v29
	v_exp_f32_e32 v26, v26
	v_exp_f32_e32 v27, v27
	s_waitcnt vmcnt(3)
	v_pk_add_f32 v[2:3], v[24:25], v[2:3]
	v_pk_add_f32 v[4:5], v[22:23], v[4:5]
	v_pk_mul_f32 v[2:3], v[2:3], s[4:5] op_sel_hi:[1,0]
	v_pk_mul_f32 v[4:5], v[4:5], s[4:5] op_sel_hi:[1,0]
	v_exp_f32_e32 v2, v2
	v_exp_f32_e32 v3, v3
	v_exp_f32_e32 v4, v4
	v_exp_f32_e32 v5, v5
	v_pk_add_f32 v[28:29], v[28:29], 1.0 op_sel_hi:[1,0]
	v_pk_add_f32 v[26:27], v[26:27], 1.0 op_sel_hi:[1,0]
	v_rcp_f32_e32 v28, v28
	v_rcp_f32_e32 v29, v29
	v_rcp_f32_e32 v26, v26
	v_rcp_f32_e32 v27, v27
	v_pk_add_f32 v[2:3], v[2:3], 1.0 op_sel_hi:[1,0]
	v_pk_add_f32 v[4:5], v[4:5], 1.0 op_sel_hi:[1,0]
	v_rcp_f32_e32 v2, v2
	v_rcp_f32_e32 v3, v3
	v_rcp_f32_e32 v4, v4
	v_rcp_f32_e32 v5, v5
	global_store_dwordx2 v[44:45], v[58:59], off offset:512 sc1
	global_store_dwordx2 v[42:43], v[30:31], off sc1
	v_or_b32_e32 v30, 6, v84
	v_pk_fma_f32 v[28:29], v[28:29], 2.0, 1.0 op_sel_hi:[1,0,0] neg_lo:[1,0,0] neg_hi:[1,0,0]
	v_pk_fma_f32 v[26:27], v[26:27], 2.0, 1.0 op_sel_hi:[1,0,0] neg_lo:[1,0,0] neg_hi:[1,0,0]
	v_ashrrev_i32_e32 v31, 31, v30
	v_cvt_pk_f16_f32 v27, v26, v27
	v_cvt_pk_f16_f32 v26, v28, v29
	v_lshlrev_b64 v[28:29], 10, v[30:31]
	v_or_b32_e32 v28, v28, v75
	s_waitcnt vmcnt(4)
	v_pk_add_f32 v[14:15], v[20:21], v[14:15]
	v_pk_add_f32 v[16:17], v[18:19], v[16:17]
	v_pk_mul_f32 v[14:15], v[14:15], s[4:5] op_sel_hi:[1,0]
	v_pk_mul_f32 v[16:17], v[16:17], s[4:5] op_sel_hi:[1,0]
	v_exp_f32_e32 v14, v14
	v_exp_f32_e32 v15, v15
	v_exp_f32_e32 v16, v16
	v_exp_f32_e32 v17, v17
	v_pk_fma_f32 v[2:3], v[2:3], 2.0, 1.0 op_sel_hi:[1,0,0] neg_lo:[1,0,0] neg_hi:[1,0,0]
	v_pk_add_f32 v[14:15], v[14:15], 1.0 op_sel_hi:[1,0]
	v_pk_fma_f32 v[4:5], v[4:5], 2.0, 1.0 op_sel_hi:[1,0,0] neg_lo:[1,0,0] neg_hi:[1,0,0]
	v_pk_add_f32 v[16:17], v[16:17], 1.0 op_sel_hi:[1,0]
	v_rcp_f32_e32 v14, v14
	s_waitcnt vmcnt(3)
	v_pk_add_f32 v[6:7], v[12:13], v[6:7]
	v_pk_add_f32 v[8:9], v[10:11], v[8:9]
	v_rcp_f32_e32 v15, v15
	v_rcp_f32_e32 v16, v16
	v_rcp_f32_e32 v17, v17
	v_pk_mul_f32 v[6:7], v[6:7], s[4:5] op_sel_hi:[1,0]
	v_pk_mul_f32 v[8:9], v[8:9], s[4:5] op_sel_hi:[1,0]
	v_exp_f32_e32 v6, v6
	v_exp_f32_e32 v7, v7
	v_exp_f32_e32 v8, v8
	v_exp_f32_e32 v9, v9
	v_lshl_add_u64 v[22:23], v[80:81], 0, v[28:29]
	v_cvt_pk_f16_f32 v2, v2, v3
	v_cvt_pk_f16_f32 v3, v4, v5
	global_store_dwordx2 v[22:23], v[2:3], off offset:512 sc1
	v_pk_fma_f32 v[2:3], v[14:15], 2.0, 1.0 op_sel_hi:[1,0,0] neg_lo:[1,0,0] neg_hi:[1,0,0]
	v_pk_fma_f32 v[4:5], v[16:17], 2.0, 1.0 op_sel_hi:[1,0,0] neg_lo:[1,0,0] neg_hi:[1,0,0]
	v_cvt_pk_f16_f32 v2, v2, v3
	v_cvt_pk_f16_f32 v3, v4, v5
	v_or_b32_e32 v4, 7, v84
	v_pk_add_f32 v[6:7], v[6:7], 1.0 op_sel_hi:[1,0]
	v_pk_add_f32 v[8:9], v[8:9], 1.0 op_sel_hi:[1,0]
	v_ashrrev_i32_e32 v5, 31, v4
	v_rcp_f32_e32 v6, v6
	v_rcp_f32_e32 v7, v7
	v_rcp_f32_e32 v8, v8
	v_rcp_f32_e32 v9, v9
	v_lshlrev_b64 v[4:5], 10, v[4:5]
	v_or_b32_e32 v4, v4, v75
	v_lshl_add_u64 v[4:5], v[80:81], 0, v[4:5]
	global_store_dwordx2 v[4:5], v[2:3], off sc1
	v_pk_fma_f32 v[2:3], v[6:7], 2.0, 1.0 op_sel_hi:[1,0,0] neg_lo:[1,0,0] neg_hi:[1,0,0]
	v_pk_fma_f32 v[6:7], v[8:9], 2.0, 1.0 op_sel_hi:[1,0,0] neg_lo:[1,0,0] neg_hi:[1,0,0]
	v_cvt_pk_f16_f32 v2, v2, v3
	v_cvt_pk_f16_f32 v3, v6, v7
	global_store_dwordx2 v[22:23], v[26:27], off sc1
	global_store_dwordx2 v[4:5], v[2:3], off offset:512 sc1
	s_mov_b64 s[4:5], 0
.LBB0_5:
	s_andn2_b64 vcc, exec, s[4:5]
	s_cbranch_vccnz .LBB0_7
	s_load_dwordx2 s[12:13], s[0:1], 0x18
	s_load_dwordx4 s[4:7], s[0:1], 0x28
	s_add_i32 s3, s2, 0xffffff00
	s_lshr_b32 s11, s3, 1
	s_and_b32 s10, s2, 1
	s_lshl_b32 s14, s11, 5
	s_lshl_b32 s15, s10, 11
	s_waitcnt lgkmcnt(0)
	s_add_u32 s12, s12, s15
	v_lshlrev_b32_e32 v2, 5, v0
	s_addc_u32 s13, s13, 0
	v_and_b32_e32 v2, 0x7e0, v2
	v_mov_b32_e32 v3, 0
	v_lshl_add_u64 v[4:5], s[12:13], 0, v[2:3]
	v_or_b32_e32 v2, s14, v126
	v_or_b32_e32 v70, 0x100, v0
	v_lshlrev_b64 v[6:7], 12, v[2:3]
	v_lshrrev_b32_e32 v71, 6, v70
	v_lshl_add_u64 v[14:15], v[4:5], 0, v[6:7]
	v_or_b32_e32 v2, s14, v71
	v_or_b32_e32 v72, 0x200, v0
	global_load_dwordx4 v[6:9], v[14:15], off
	global_load_dwordx4 v[10:13], v[14:15], off offset:16
	v_lshlrev_b64 v[14:15], 12, v[2:3]
	v_lshrrev_b32_e32 v73, 6, v72
	v_lshl_add_u64 v[22:23], v[4:5], 0, v[14:15]
	v_or_b32_e32 v2, s14, v73
	global_load_dwordx4 v[14:17], v[22:23], off
	global_load_dwordx4 v[18:21], v[22:23], off offset:16
	v_lshlrev_b64 v[22:23], 12, v[2:3]
	v_lshl_add_u64 v[30:31], v[4:5], 0, v[22:23]
	global_load_dwordx4 v[22:25], v[30:31], off
	global_load_dwordx4 v[26:29], v[30:31], off offset:16
	v_or_b32_e32 v75, 0x300, v0
	v_lshrrev_b32_e32 v77, 6, v75
	v_or_b32_e32 v2, s14, v77
	v_lshlrev_b64 v[30:31], 12, v[2:3]
	v_lshl_add_u64 v[38:39], v[4:5], 0, v[30:31]
	global_load_dwordx4 v[30:33], v[38:39], off
	global_load_dwordx4 v[34:37], v[38:39], off offset:16
	v_or_b32_e32 v79, 0x400, v0
	v_lshrrev_b32_e32 v80, 6, v79
	v_or_b32_e32 v2, s14, v80
	v_lshlrev_b64 v[38:39], 12, v[2:3]
	v_lshl_add_u64 v[46:47], v[4:5], 0, v[38:39]
	global_load_dwordx4 v[38:41], v[46:47], off
	global_load_dwordx4 v[42:45], v[46:47], off offset:16
	v_or_b32_e32 v81, 0x500, v0
	v_lshrrev_b32_e32 v82, 6, v81
	v_or_b32_e32 v2, s14, v82
	v_lshlrev_b64 v[46:47], 12, v[2:3]
	v_lshl_add_u64 v[54:55], v[4:5], 0, v[46:47]
	global_load_dwordx4 v[46:49], v[54:55], off
	global_load_dwordx4 v[50:53], v[54:55], off offset:16
	v_or_b32_e32 v83, 0x600, v0
	v_lshrrev_b32_e32 v84, 6, v83
	v_or_b32_e32 v2, s14, v84
	v_lshlrev_b64 v[54:55], 12, v[2:3]
	v_lshl_add_u64 v[62:63], v[4:5], 0, v[54:55]
	global_load_dwordx4 v[54:57], v[62:63], off
	global_load_dwordx4 v[58:61], v[62:63], off offset:16
	v_or_b32_e32 v85, 0x700, v0
	v_lshrrev_b32_e32 v86, 6, v85
	v_or_b32_e32 v2, s14, v86
	v_lshlrev_b64 v[62:63], 12, v[2:3]
	v_lshl_add_u64 v[4:5], v[4:5], 0, v[62:63]
	global_load_dwordx4 v[62:65], v[4:5], off
	global_load_dwordx4 v[66:69], v[4:5], off offset:16
	v_and_b32_e32 v4, 0x3f0, v78
	s_movk_i32 s12, 0x410
	v_mad_u32_u24 v2, v126, s12, v4
	v_mad_u32_u24 v5, v71, s12, v4
	s_lshl_b32 s11, s11, 6
	s_lshl_b32 s13, s10, 5
	s_or_b32 s11, s11, s13
	s_and_b32 s3, s3, -2
	s_waitcnt vmcnt(15)
	v_cvt_f16_f32_e32 v6, v6
	v_cvt_pk_f16_f32 v78, v7, v8
	s_waitcnt vmcnt(14)
	v_cvt_pk_f16_f32 v8, v9, v10
	v_cvt_f16_f32_e32 v10, v13
	v_cvt_pk_f16_f32 v9, v11, v12
	s_waitcnt vmcnt(13)
	v_cvt_f16_f32_e32 v13, v14
	s_waitcnt vmcnt(12)
	v_cvt_pk_f16_f32 v12, v17, v18
	v_cvt_f16_f32_e32 v17, v21
	v_alignbit_b32 v7, v8, v78, 16
	s_waitcnt vmcnt(10)
	v_cvt_f16_f32_e32 v21, v29
	v_alignbit_b32 v8, v9, v8, 16
	v_cvt_f16_f32_e32 v18, v22
	v_pack_b32_f16 v6, v6, v78
	v_alignbit_b32 v9, v10, v9, 16
	v_cvt_pk_f16_f32 v14, v15, v16
	v_cvt_pk_f16_f32 v16, v19, v20
	v_cvt_pk_f16_f32 v20, v25, v26
	ds_write_b128 v2, v[6:9]
	v_cvt_pk_f16_f32 v2, v27, v28
	v_alignbit_b32 v11, v12, v14, 16
	v_alignbit_b32 v12, v16, v12, 16
	v_pack_b32_f16 v10, v13, v14
	v_alignbit_b32 v13, v17, v16, 16
	v_alignbit_b32 v16, v2, v20, 16
	v_alignbit_b32 v17, v21, v2, 16
	s_waitcnt vmcnt(9)
	v_cvt_f16_f32_e32 v2, v30
	v_cvt_pk_f16_f32 v19, v23, v24
	v_alignbit_b32 v15, v20, v19, 16
	ds_write_b128 v5, v[10:13]
	v_pack_b32_f16 v14, v18, v19
	v_mad_u32_u24 v5, v73, s12, v4
	ds_write_b128 v5, v[14:17]
	v_cvt_pk_f16_f32 v5, v31, v32
	v_pack_b32_f16 v6, v2, v5
	s_waitcnt vmcnt(8)
	v_cvt_pk_f16_f32 v2, v33, v34
	v_cvt_f16_f32_e32 v9, v37
	v_alignbit_b32 v7, v2, v5, 16
	v_cvt_pk_f16_f32 v5, v35, v36
	v_alignbit_b32 v8, v5, v2, 16
	s_waitcnt vmcnt(7)
	v_cvt_f16_f32_e32 v2, v38
	v_alignbit_b32 v9, v9, v5, 16
	v_mad_u32_u24 v5, v77, s12, v4
	ds_write_b128 v5, v[6:9]
	v_cvt_pk_f16_f32 v5, v39, v40
	v_pack_b32_f16 v6, v2, v5
	s_waitcnt vmcnt(6)
	v_cvt_pk_f16_f32 v2, v41, v42
	v_cvt_f16_f32_e32 v9, v45
	v_alignbit_b32 v7, v2, v5, 16
	v_cvt_pk_f16_f32 v5, v43, v44
	v_alignbit_b32 v8, v5, v2, 16
	s_waitcnt vmcnt(5)
	v_cvt_f16_f32_e32 v2, v46
	v_alignbit_b32 v9, v9, v5, 16
	v_mad_u32_u24 v5, v80, s12, v4
	ds_write_b128 v5, v[6:9]
	v_cvt_pk_f16_f32 v5, v47, v48
	v_pack_b32_f16 v6, v2, v5
	s_waitcnt vmcnt(4)
	v_cvt_pk_f16_f32 v2, v49, v50
	v_cvt_f16_f32_e32 v9, v53
	v_alignbit_b32 v7, v2, v5, 16
	v_cvt_pk_f16_f32 v5, v51, v52
	v_alignbit_b32 v8, v5, v2, 16
	s_waitcnt vmcnt(3)
	v_cvt_f16_f32_e32 v2, v54
	v_alignbit_b32 v9, v9, v5, 16
	v_mad_u32_u24 v5, v82, s12, v4
	ds_write_b128 v5, v[6:9]
	v_cvt_pk_f16_f32 v5, v55, v56
	s_waitcnt vmcnt(2)
	v_cvt_f16_f32_e32 v9, v61
	v_pack_b32_f16 v6, v2, v5
	v_cvt_pk_f16_f32 v2, v57, v58
	v_alignbit_b32 v7, v2, v5, 16
	v_cvt_pk_f16_f32 v5, v59, v60
	v_alignbit_b32 v8, v5, v2, 16
	s_waitcnt vmcnt(1)
	v_cvt_f16_f32_e32 v2, v62
	v_alignbit_b32 v9, v9, v5, 16
	v_mad_u32_u24 v5, v84, s12, v4
	ds_write_b128 v5, v[6:9]
	s_waitcnt vmcnt(0)
	v_cvt_f16_f32_e32 v9, v69
	v_cvt_pk_f16_f32 v5, v63, v64
	v_pack_b32_f16 v6, v2, v5
	v_cvt_pk_f16_f32 v2, v65, v66
	v_alignbit_b32 v7, v2, v5, 16
	v_cvt_pk_f16_f32 v5, v67, v68
	v_alignbit_b32 v8, v5, v2, 16
	v_alignbit_b32 v9, v9, v5, 16
	v_mad_u32_u24 v2, v86, s12, v4
	v_lshrrev_b32_e32 v16, 1, v0
	ds_write_b128 v2, v[6:9]
	v_and_b32_e32 v2, 0x70, v16
	v_mad_u32_u24 v2, v1, s12, v2
	s_waitcnt lgkmcnt(0)
	s_barrier
	ds_read_b128 v[6:9], v2
	v_or_b32_e32 v2, s11, v126
	v_lshlrev_b64 v[10:11], 10, v[2:3]
	v_lshrrev_b32_e32 v2, 1, v70
	v_and_b32_e32 v2, 0xf0, v2
	v_mov_b32_e32 v5, v3
	v_lshl_add_u64 v[10:11], s[4:5], 0, v[10:11]
	v_mad_u32_u24 v2, v1, s12, v2
	v_lshl_add_u64 v[14:15], v[10:11], 0, v[4:5]
	ds_read_b128 v[10:13], v2
	v_or_b32_e32 v2, s11, v71
	s_waitcnt lgkmcnt(1)
	global_store_dwordx4 v[14:15], v[6:9], off sc1
	s_nop 1
	v_lshlrev_b64 v[6:7], 10, v[2:3]
	v_lshrrev_b32_e32 v2, 1, v72
	v_lshl_add_u64 v[6:7], s[4:5], 0, v[6:7]
	v_and_b32_e32 v2, 0x170, v2
	v_lshl_add_u64 v[6:7], v[6:7], 0, v[4:5]
	v_mad_u32_u24 v2, v1, s12, v2
	s_waitcnt lgkmcnt(0)
	global_store_dwordx4 v[6:7], v[10:13], off sc1
	ds_read_b128 v[6:9], v2
	v_or_b32_e32 v2, s11, v73
	v_lshlrev_b64 v[10:11], 10, v[2:3]
	v_lshrrev_b32_e32 v2, 1, v75
	v_and_b32_e32 v2, 0x1f0, v2
	v_lshl_add_u64 v[10:11], s[4:5], 0, v[10:11]
	v_mad_u32_u24 v2, v1, s12, v2
	v_lshl_add_u64 v[14:15], v[10:11], 0, v[4:5]
	ds_read_b128 v[10:13], v2
	v_or_b32_e32 v2, s11, v77
	s_waitcnt lgkmcnt(1)
	global_store_dwordx4 v[14:15], v[6:9], off sc1
	v_mov_b32_e32 v75, v3
	s_nop 0
	v_lshlrev_b64 v[6:7], 10, v[2:3]
	v_lshrrev_b32_e32 v2, 1, v79
	v_lshl_add_u64 v[6:7], s[4:5], 0, v[6:7]
	v_and_b32_e32 v2, 0x270, v2
	v_lshl_add_u64 v[6:7], v[6:7], 0, v[4:5]
	v_mad_u32_u24 v2, v1, s12, v2
	s_waitcnt lgkmcnt(0)
	global_store_dwordx4 v[6:7], v[10:13], off sc1
	ds_read_b128 v[6:9], v2
	v_or_b32_e32 v2, s11, v80
	v_lshlrev_b64 v[10:11], 10, v[2:3]
	v_lshrrev_b32_e32 v2, 1, v81
	v_and_b32_e32 v2, 0x2f0, v2
	v_lshl_add_u64 v[10:11], s[4:5], 0, v[10:11]
	v_mad_u32_u24 v2, v1, s12, v2
	v_lshl_add_u64 v[14:15], v[10:11], 0, v[4:5]
	ds_read_b128 v[10:13], v2
	v_or_b32_e32 v2, s11, v82
	s_waitcnt lgkmcnt(1)
	global_store_dwordx4 v[14:15], v[6:9], off sc1
	s_nop 1
	v_lshlrev_b64 v[6:7], 10, v[2:3]
	v_lshrrev_b32_e32 v2, 1, v83
	v_lshl_add_u64 v[6:7], s[4:5], 0, v[6:7]
	v_and_b32_e32 v2, 0x370, v2
	v_lshl_add_u64 v[6:7], v[6:7], 0, v[4:5]
	v_mad_u32_u24 v2, v1, s12, v2
	s_waitcnt lgkmcnt(0)
	global_store_dwordx4 v[6:7], v[10:13], off sc1
	ds_read_b128 v[6:9], v2
	v_or_b32_e32 v2, s11, v84
	v_lshlrev_b64 v[10:11], 10, v[2:3]
	v_lshrrev_b32_e32 v2, 1, v85
	v_and_b32_e32 v2, 0x3f0, v2
	v_lshl_add_u64 v[10:11], s[4:5], 0, v[10:11]
	v_mad_u32_u24 v2, v1, s12, v2
	v_lshl_add_u64 v[14:15], v[10:11], 0, v[4:5]
	ds_read_b128 v[10:13], v2
	v_or_b32_e32 v2, s11, v86
	s_waitcnt lgkmcnt(1)
	global_store_dwordx4 v[14:15], v[6:9], off sc1
	s_nop 1
	v_lshlrev_b64 v[6:7], 10, v[2:3]
	v_lshl_add_u64 v[6:7], s[4:5], 0, v[6:7]
	v_lshl_add_u64 v[4:5], v[6:7], 0, v[4:5]
	v_bfe_u32 v2, v0, 6, 1
	s_lshl_b32 s4, s10, 10
	s_waitcnt lgkmcnt(0)
	global_store_dwordx4 v[4:5], v[10:13], off sc1
	v_lshl_or_b32 v6, v2, 4, v76
	v_mul_i32_i24_e32 v4, 0xfffffbf2, v1
	s_add_i32 s3, s3, s4
	v_mad_u32_u24 v12, v1, s12, v4
	v_or_b32_e32 v13, s3, v2
	v_mul_u32_u24_e32 v14, 0x410, v6
	v_and_b32_e32 v2, 64, v16
	v_add3_u32 v6, v12, v2, v14
	ds_read_u16 v7, v6 offset:4160
	ds_read_u16 v8, v6 offset:6240
	ds_read_u16 v9, v6 offset:7280
	ds_read_u16 v10, v6 offset:5200
	ds_read_u16 v15, v6 offset:7792
	ds_read_u16 v16, v6 offset:6752
	ds_read_u16 v17, v6 offset:5712
	s_mov_b32 s3, 0x5040100
	s_waitcnt lgkmcnt(4)
	v_perm_b32 v9, v9, v8, s3
	ds_read_u16 v18, v6 offset:4672
	s_waitcnt lgkmcnt(4)
	v_perm_b32 v8, v10, v7, s3
	ds_read_u16 v10, v6
	ds_read_u16 v7, v6 offset:2080
	ds_read_u16 v11, v6 offset:3120
	ds_read_u16 v19, v6 offset:1040
	ds_read_u16 v20, v6 offset:3632
	ds_read_u16 v21, v6 offset:2592
	ds_read_u16 v22, v6 offset:1552
	ds_read_u16 v23, v6 offset:512
	s_waitcnt lgkmcnt(4)
	v_perm_b32 v6, v19, v10, s3
	v_lshlrev_b32_e32 v19, 5, v126
	s_movk_i32 s4, 0xc0
	v_mov_b32_e32 v10, 0x80
	v_bitop3_b32 v24, v19, s4, v10 bitop3:0xc8
	v_add3_u32 v10, v12, v24, v14
	v_add_u32_e32 v2, v13, v2
	v_lshl_add_u64 v[4:5], s[6:7], 0, v[74:75]
	v_perm_b32 v7, v11, v7, s3
	ds_read_u16 v25, v10
	ds_read_u16 v26, v10 offset:1040
	ds_read_u16 v27, v10 offset:2080
	ds_read_u16 v28, v10 offset:3120
	ds_read_u16 v29, v10 offset:4160
	ds_read_u16 v30, v10 offset:5200
	ds_read_u16 v31, v10 offset:6240
	ds_read_u16 v32, v10 offset:7280
	v_lshlrev_b64 v[10:11], 10, v[2:3]
	v_lshl_add_u64 v[10:11], v[4:5], 0, v[10:11]
	global_store_dwordx4 v[10:11], v[6:9], off sc1
	s_movk_i32 s4, 0x140
	v_mov_b32_e32 v11, 0x100
	v_add_u32_e32 v10, v13, v24
	v_bitop3_b32 v24, v19, s4, v11 bitop3:0xc8
	v_add3_u32 v11, v12, v24, v14
	s_waitcnt lgkmcnt(0)
	v_perm_b32 v9, v32, v31, s3
	v_perm_b32 v8, v30, v29, s3
	v_perm_b32 v7, v28, v27, s3
	v_perm_b32 v6, v26, v25, s3
	ds_read_u16 v25, v11
	ds_read_u16 v26, v11 offset:1040
	ds_read_u16 v27, v11 offset:2080
	ds_read_u16 v28, v11 offset:3120
	ds_read_u16 v29, v11 offset:4160
	ds_read_u16 v30, v11 offset:5200
	ds_read_u16 v31, v11 offset:6240
	ds_read_u16 v32, v11 offset:7280
	v_mov_b32_e32 v11, v3
	v_lshlrev_b64 v[10:11], 10, v[10:11]
	v_lshl_add_u64 v[10:11], v[4:5], 0, v[10:11]
	global_store_dwordx4 v[10:11], v[6:9], off sc1
	s_movk_i32 s4, 0x1c0
	v_mov_b32_e32 v11, 0x180
	v_add_u32_e32 v10, v13, v24
	v_bitop3_b32 v24, v19, s4, v11 bitop3:0xc8
	v_add3_u32 v11, v12, v24, v14
	s_waitcnt lgkmcnt(0)
	v_perm_b32 v9, v32, v31, s3
	v_perm_b32 v8, v30, v29, s3
	v_perm_b32 v7, v28, v27, s3
	v_perm_b32 v6, v26, v25, s3
	ds_read_u16 v25, v11
	ds_read_u16 v26, v11 offset:1040
	ds_read_u16 v27, v11 offset:2080
	ds_read_u16 v28, v11 offset:3120
	ds_read_u16 v29, v11 offset:4160
	ds_read_u16 v30, v11 offset:5200
	ds_read_u16 v31, v11 offset:6240
	ds_read_u16 v32, v11 offset:7280
	v_mov_b32_e32 v11, v3
	v_lshlrev_b64 v[10:11], 10, v[10:11]
	v_lshl_add_u64 v[10:11], v[4:5], 0, v[10:11]
	global_store_dwordx4 v[10:11], v[6:9], off sc1
	v_add_u32_e32 v10, v13, v24
	v_mov_b32_e32 v11, v3
	v_lshlrev_b64 v[10:11], 10, v[10:11]
	s_waitcnt lgkmcnt(0)
	v_perm_b32 v9, v32, v31, s3
	v_perm_b32 v8, v30, v29, s3
	v_perm_b32 v7, v28, v27, s3
	v_perm_b32 v6, v26, v25, s3
	v_lshl_add_u64 v[10:11], v[4:5], 0, v[10:11]
	global_store_dwordx4 v[10:11], v[6:9], off sc1
	s_movk_i32 s4, 0x2c0
	v_mov_b32_e32 v10, 0x280
	v_perm_b32 v9, v15, v16, s3
	v_bitop3_b32 v15, v19, s4, v10 bitop3:0xc8
	v_add3_u32 v10, v12, v15, v14
	v_perm_b32 v8, v17, v18, s3
	v_perm_b32 v7, v20, v21, s3
	v_perm_b32 v6, v22, v23, s3
	ds_read_u16 v16, v10
	ds_read_u16 v17, v10 offset:1040
	ds_read_u16 v18, v10 offset:2080
	ds_read_u16 v20, v10 offset:3120
	ds_read_u16 v21, v10 offset:4160
	ds_read_u16 v22, v10 offset:5200
	ds_read_u16 v23, v10 offset:6240
	ds_read_u16 v24, v10 offset:7280
	v_add_u32_e32 v2, 0x200, v2
	v_lshlrev_b64 v[10:11], 10, v[2:3]
	v_lshl_add_u64 v[10:11], v[4:5], 0, v[10:11]
	s_movk_i32 s4, 0x340
	v_mov_b32_e32 v2, 0x300
	global_store_dwordx4 v[10:11], v[6:9], off sc1
	s_waitcnt lgkmcnt(6)
	s_nop 0
	v_perm_b32 v6, v17, v16, s3
	v_bitop3_b32 v16, v19, s4, v2 bitop3:0xc8
	v_add3_u32 v2, v12, v16, v14
	s_waitcnt lgkmcnt(0)
	v_perm_b32 v9, v24, v23, s3
	v_perm_b32 v8, v22, v21, s3
	v_perm_b32 v7, v20, v18, s3
	ds_read_u16 v17, v2
	ds_read_u16 v18, v2 offset:1040
	ds_read_u16 v20, v2 offset:2080
	ds_read_u16 v21, v2 offset:3120
	ds_read_u16 v22, v2 offset:4160
	ds_read_u16 v23, v2 offset:5200
	ds_read_u16 v24, v2 offset:6240
	ds_read_u16 v25, v2 offset:7280
	v_add_u32_e32 v2, v13, v15
	v_lshlrev_b64 v[10:11], 10, v[2:3]
	s_movk_i32 s4, 0x3c0
	v_mov_b32_e32 v2, 0x380
	v_lshl_add_u64 v[10:11], v[4:5], 0, v[10:11]
	v_bitop3_b32 v15, v19, s4, v2 bitop3:0xc8
	global_store_dwordx4 v[10:11], v[6:9], off sc1
	v_add3_u32 v2, v12, v15, v14
	s_waitcnt lgkmcnt(2)
	v_perm_b32 v8, v23, v22, s3
	v_perm_b32 v7, v21, v20, s3
	v_perm_b32 v6, v18, v17, s3
	ds_read_u16 v12, v2
	ds_read_u16 v14, v2 offset:1040
	ds_read_u16 v17, v2 offset:2080
	ds_read_u16 v18, v2 offset:3120
	ds_read_u16 v19, v2 offset:4160
	ds_read_u16 v20, v2 offset:5200
	ds_read_u16 v21, v2 offset:6240
	ds_read_u16 v22, v2 offset:7280
	v_add_u32_e32 v2, v13, v16
	v_lshlrev_b64 v[10:11], 10, v[2:3]
	v_add_u32_e32 v2, v13, v15
	s_waitcnt lgkmcnt(8)
	v_perm_b32 v9, v25, v24, s3
	v_lshl_add_u64 v[10:11], v[4:5], 0, v[10:11]
	v_lshlrev_b64 v[2:3], 10, v[2:3]
	global_store_dwordx4 v[10:11], v[6:9], off sc1
	v_lshl_add_u64 v[2:3], v[4:5], 0, v[2:3]
	s_waitcnt lgkmcnt(0)
	v_perm_b32 v9, v22, v21, s3
	v_perm_b32 v8, v20, v19, s3
	v_perm_b32 v7, v18, v17, s3
	v_perm_b32 v6, v14, v12, s3
	global_store_dwordx4 v[2:3], v[6:9], off sc1

.LBB0_18:
	s_or_b64 exec, exec, s[4:5]
	v_lshrrev_b32_e32 v4, 3, v2
	v_lshrrev_b32_e32 v5, 3, v0
	v_lshlrev_b32_e32 v0, 1, v0
	v_and_b32_e32 v4, 0x1fffffe0, v4
	v_and_b32_e32 v6, 0x80, v0
	v_mov_b32_e32 v7, 0
	v_and_or_b32 v4, v5, 20, v4
	v_lshl_add_u64 v[8:9], s[8:9], 0, v[6:7]
	v_lshlrev_b32_e32 v6, 2, v1
	v_lshl_add_u64 v[0:1], v[8:9], 0, v[6:7]
	v_or_b32_e32 v6, 1, v4
	v_lshlrev_b64 v[10:11], 8, v[6:7]
	v_or_b32_e32 v6, 2, v4
	v_lshlrev_b64 v[12:13], 8, v[6:7]
	v_or_b32_e32 v6, 3, v4
	v_lshlrev_b64 v[14:15], 8, v[6:7]
	v_or_b32_e32 v6, 8, v4
	v_lshlrev_b64 v[16:17], 8, v[6:7]
	v_or_b32_e32 v6, 9, v4
	v_mov_b32_e32 v5, v7
	v_lshlrev_b64 v[18:19], 8, v[6:7]
	v_or_b32_e32 v6, 10, v4
	v_lshlrev_b64 v[8:9], 8, v[4:5]
	v_lshlrev_b64 v[20:21], 8, v[6:7]
	v_or_b32_e32 v6, 11, v4
	v_lshl_add_u64 v[8:9], v[0:1], 0, v[8:9]
	v_lshlrev_b64 v[4:5], 8, v[6:7]
	v_lshl_add_u64 v[10:11], v[0:1], 0, v[10:11]
	v_lshl_add_u64 v[12:13], v[0:1], 0, v[12:13]
	v_lshl_add_u64 v[14:15], v[0:1], 0, v[14:15]
	v_lshl_add_u64 v[16:17], v[0:1], 0, v[16:17]
	v_lshl_add_u64 v[18:19], v[0:1], 0, v[18:19]
	v_lshl_add_u64 v[20:21], v[0:1], 0, v[20:21]
	v_lshl_add_u64 v[0:1], v[0:1], 0, v[4:5]
	global_load_dword v4, v[8:9], off
	global_load_dword v5, v[10:11], off
	global_load_dword v6, v[12:13], off
	global_load_dword v7, v[14:15], off
	global_load_dword v22, v[16:17], off
	global_load_dword v23, v[18:19], off
	global_load_dword v24, v[20:21], off
	global_load_dword v25, v[0:1], off
	v_lshl_add_u64 v[0:1], v[2:3], 4, s[2:3]
	s_waitcnt vmcnt(6)
	v_cvt_pk_f16_f32 v4, v4, v5
	s_waitcnt vmcnt(4)
	v_cvt_pk_f16_f32 v5, v6, v7
	s_waitcnt vmcnt(2)
	v_cvt_pk_f16_f32 v6, v22, v23
	s_waitcnt vmcnt(0)
	v_cvt_pk_f16_f32 v7, v24, v25
	global_store_dwordx4 v[0:1], v[4:7], off sc1
	s_endpgm

_Z7k_finalPKfS0_S0_Pf:
	s_load_dwordx8 s[4:11], s[0:1], 0x0
	s_lshl_b32 s2, s2, 4
	v_lshrrev_b32_e32 v1, 3, v0
	v_or_b32_e32 v34, s2, v1
	v_bfe_u32 v1, v0, 2, 1
	s_ashr_i32 s0, s2, 3
	v_bfe_u32 v35, v0, 1, 1
	s_and_b32 s0, s0, -4
	v_lshlrev_b32_e32 v2, 1, v1
	v_lshlrev_b32_e32 v3, 4, v34
	v_and_b32_e32 v50, 1, v0
	v_or3_b32 v2, s0, v2, v35
	v_and_b32_e32 v3, 0x1f0, v3
	v_lshl_or_b32 v36, v50, 9, v3
	v_mov_b32_e32 v37, 0
	v_ashrrev_i32_e32 v3, 31, v2
	s_waitcnt lgkmcnt(0)
	v_lshl_add_u64 v[4:5], s[4:5], 0, v[36:37]
	v_lshlrev_b64 v[2:3], 10, v[2:3]
	v_lshl_add_u64 v[30:31], v[4:5], 0, v[2:3]
	s_mov_b32 s0, 0x80000
	v_add_co_u32_e32 v6, vcc, s0, v30
	s_mov_b32 s0, 0x100000
	s_nop 0
	v_addc_co_u32_e32 v7, vcc, 0, v31, vcc
	v_add_co_u32_e32 v14, vcc, s0, v30
	s_mov_b32 s0, 0x180000
	s_nop 0
	v_addc_co_u32_e32 v15, vcc, 0, v31, vcc
	v_add_co_u32_e32 v16, vcc, s0, v30
	s_mov_b32 s0, 0x200000
	s_nop 0
	v_addc_co_u32_e32 v17, vcc, 0, v31, vcc
	global_load_dwordx4 v[22:25], v[30:31], off
	global_load_dwordx4 v[2:5], v[6:7], off
	global_load_dwordx4 v[10:13], v[14:15], off
	s_nop 0
	global_load_dwordx4 v[6:9], v[16:17], off
	v_add_co_u32_e32 v26, vcc, s0, v30
	s_mov_b32 s0, 0x280000
	s_nop 0
	v_addc_co_u32_e32 v27, vcc, 0, v31, vcc
	v_add_co_u32_e32 v28, vcc, s0, v30
	s_mov_b32 s0, 0x300000
	s_nop 0
	v_addc_co_u32_e32 v29, vcc, 0, v31, vcc
	global_load_dwordx4 v[18:21], v[26:27], off
	global_load_dwordx4 v[14:17], v[28:29], off
	v_add_co_u32_e32 v26, vcc, s0, v30
	s_mov_b32 s0, 0x380000
	s_nop 0
	v_addc_co_u32_e32 v27, vcc, 0, v31, vcc
	v_add_co_u32_e32 v30, vcc, s0, v30
	global_load_dwordx4 v[26:29], v[26:27], off
	s_nop 0
	v_addc_co_u32_e32 v31, vcc, 0, v31, vcc
	global_load_dwordx4 v[30:33], v[30:31], off
	v_lshlrev_b32_e32 v36, 6, v35
	v_and_or_b32 v44, v0, 15, s2
	v_mov_b32_e32 v45, v37
	v_mov_b32_e32 v49, v37
	v_lshl_or_b32 v1, v1, 7, v36
	v_add_u32_e32 v48, 0x6000, v44
	v_mov_b32_e32 v39, v37
	v_mov_b32_e32 v41, v37
	v_mov_b32_e32 v43, v37
	v_mov_b32_e32 v47, v37
	v_add_u32_e32 v38, 0x1000, v44
	v_add_u32_e32 v40, 0x2000, v44
	v_add_u32_e32 v42, 0x4000, v44
	v_add_u32_e32 v46, 0x5000, v44
	v_lshl_or_b32 v36, v50, 4, v1
	v_lshl_add_u64 v[50:51], v[44:45], 2, s[8:9]
	v_lshl_add_u64 v[48:49], v[48:49], 2, s[8:9]
	v_lshl_add_u64 v[52:53], v[38:39], 2, s[8:9]
	v_lshl_add_u64 v[54:55], v[40:41], 2, s[8:9]
	v_lshl_add_u64 v[56:57], v[42:43], 2, s[8:9]
	v_lshl_add_u64 v[46:47], v[46:47], 2, s[8:9]
	global_load_dword v40, v[50:51], off
	global_load_dword v42, v[52:53], off
	global_load_dword v38, v[54:55], off
	global_load_dword v41, v[56:57], off
	global_load_dword v43, v[46:47], off
	global_load_dword v39, v[48:49], off
	v_ashrrev_i32_e32 v35, 31, v34
	s_mov_b64 s[0:1], 0x8000
	s_waitcnt vmcnt(13)
	v_cvt_f32_f16_e32 v58, v22
	s_waitcnt vmcnt(11)
	v_cvt_f32_f16_e32 v48, v10
	v_cvt_f32_f16_sdwa v49, v10 dst_sel:DWORD dst_unused:UNUSED_PAD src0_sel:WORD_1
	s_waitcnt vmcnt(10)
	v_cvt_f32_f16_e32 v50, v6
	v_cvt_f32_f16_sdwa v51, v6 dst_sel:DWORD dst_unused:UNUSED_PAD src0_sel:WORD_1
	v_cvt_f32_f16_e32 v10, v11
	v_cvt_f32_f16_sdwa v11, v11 dst_sel:DWORD dst_unused:UNUSED_PAD src0_sel:WORD_1
	v_cvt_f32_f16_e32 v6, v7
	v_cvt_f32_f16_sdwa v7, v7 dst_sel:DWORD dst_unused:UNUSED_PAD src0_sel:WORD_1
	v_cvt_f32_f16_sdwa v59, v22 dst_sel:DWORD dst_unused:UNUSED_PAD src0_sel:WORD_1
	v_cvt_f32_f16_e32 v60, v2
	v_cvt_f32_f16_sdwa v61, v2 dst_sel:DWORD dst_unused:UNUSED_PAD src0_sel:WORD_1
	v_cvt_f32_f16_e32 v22, v23
	v_cvt_f32_f16_sdwa v23, v23 dst_sel:DWORD dst_unused:UNUSED_PAD src0_sel:WORD_1
	v_cvt_f32_f16_e32 v2, v3
	v_cvt_f32_f16_sdwa v3, v3 dst_sel:DWORD dst_unused:UNUSED_PAD src0_sel:WORD_1
	s_waitcnt vmcnt(8)
	v_cvt_f32_f16_e32 v54, v14
	v_cvt_f32_f16_sdwa v55, v14 dst_sel:DWORD dst_unused:UNUSED_PAD src0_sel:WORD_1
	v_pk_add_f32 v[6:7], v[10:11], v[6:7]
	v_cvt_f32_f16_e32 v10, v19
	v_cvt_f32_f16_sdwa v11, v19 dst_sel:DWORD dst_unused:UNUSED_PAD src0_sel:WORD_1
	v_cvt_f32_f16_e32 v14, v15
	v_cvt_f32_f16_sdwa v15, v15 dst_sel:DWORD dst_unused:UNUSED_PAD src0_sel:WORD_1
	v_pk_add_f32 v[2:3], v[22:23], v[2:3]
	v_pk_add_f32 v[46:47], v[58:59], v[60:61]
	v_cvt_f32_f16_e32 v52, v18
	v_cvt_f32_f16_sdwa v53, v18 dst_sel:DWORD dst_unused:UNUSED_PAD src0_sel:WORD_1
	s_waitcnt vmcnt(7)
	v_cvt_f32_f16_e32 v56, v26
	v_cvt_f32_f16_sdwa v57, v26 dst_sel:DWORD dst_unused:UNUSED_PAD src0_sel:WORD_1
	s_waitcnt vmcnt(6)
	v_cvt_f32_f16_e32 v58, v30
	v_cvt_f32_f16_sdwa v59, v30 dst_sel:DWORD dst_unused:UNUSED_PAD src0_sel:WORD_1
	v_pk_add_f32 v[2:3], v[2:3], v[6:7]
	v_pk_add_f32 v[6:7], v[10:11], v[14:15]
	v_cvt_f32_f16_e32 v10, v27
	v_cvt_f32_f16_sdwa v11, v27 dst_sel:DWORD dst_unused:UNUSED_PAD src0_sel:WORD_1
	v_cvt_f32_f16_e32 v14, v31
	v_cvt_f32_f16_sdwa v15, v31 dst_sel:DWORD dst_unused:UNUSED_PAD src0_sel:WORD_1
	v_pk_add_f32 v[48:49], v[48:49], v[50:51]
	v_pk_add_f32 v[50:51], v[56:57], v[58:59]
	v_pk_add_f32 v[46:47], v[46:47], v[48:49]
	v_pk_add_f32 v[48:49], v[52:53], v[54:55]
	v_pk_add_f32 v[10:11], v[10:11], v[14:15]
	v_pk_add_f32 v[48:49], v[48:49], v[50:51]
	v_pk_add_f32 v[6:7], v[6:7], v[10:11]
	v_add_u32_e32 v50, 0x3000, v44
	v_add_u32_e32 v22, 0x7000, v44
	v_pk_add_f32 v[44:45], v[46:47], v[48:49]
	v_pk_add_f32 v[46:47], v[2:3], v[6:7]
	v_cvt_f32_f16_e32 v6, v24
	v_cvt_f32_f16_sdwa v7, v24 dst_sel:DWORD dst_unused:UNUSED_PAD src0_sel:WORD_1
	v_cvt_f32_f16_e32 v10, v4
	v_cvt_f32_f16_sdwa v11, v4 dst_sel:DWORD dst_unused:UNUSED_PAD src0_sel:WORD_1
	v_cvt_f32_f16_e32 v14, v12
	v_cvt_f32_f16_sdwa v15, v12 dst_sel:DWORD dst_unused:UNUSED_PAD src0_sel:WORD_1
	v_cvt_f32_f16_e32 v26, v8
	v_cvt_f32_f16_sdwa v27, v8 dst_sel:DWORD dst_unused:UNUSED_PAD src0_sel:WORD_1
	v_pk_add_f32 v[6:7], v[6:7], v[10:11]
	v_mov_b32_e32 v51, v37
	v_lshl_add_u64 v[18:19], v[50:51], 2, s[8:9]
	v_pk_add_f32 v[10:11], v[14:15], v[26:27]
	v_cvt_f32_f16_e32 v14, v16
	v_pk_add_f32 v[10:11], v[6:7], v[10:11]
	v_cvt_f32_f16_e32 v6, v20
	v_cvt_f32_f16_sdwa v7, v20 dst_sel:DWORD dst_unused:UNUSED_PAD src0_sel:WORD_1
	v_cvt_f32_f16_sdwa v15, v16 dst_sel:DWORD dst_unused:UNUSED_PAD src0_sel:WORD_1
	v_mov_b32_e32 v23, v37
	v_lshl_add_u64 v[22:23], v[22:23], 2, s[8:9]
	global_load_dword v2, v[18:19], off
	global_load_dword v3, v[22:23], off
	v_lshlrev_b64 v[18:19], 8, v[34:35]
	v_pk_add_f32 v[14:15], v[6:7], v[14:15]
	v_lshl_add_u64 v[6:7], s[6:7], 0, v[18:19]
	v_cvt_f32_f16_e32 v26, v25
	v_cvt_f32_f16_sdwa v27, v25 dst_sel:DWORD dst_unused:UNUSED_PAD src0_sel:WORD_1
	v_cvt_f32_f16_e32 v22, v28
	v_cvt_f32_f16_sdwa v23, v28 dst_sel:DWORD dst_unused:UNUSED_PAD src0_sel:WORD_1
	v_cvt_f32_f16_e32 v24, v32
	v_cvt_f32_f16_sdwa v25, v32 dst_sel:DWORD dst_unused:UNUSED_PAD src0_sel:WORD_1
	v_lshl_add_u64 v[30:31], v[6:7], 0, v[36:37]
	v_cvt_f32_f16_e32 v48, v5
	v_cvt_f32_f16_sdwa v49, v5 dst_sel:DWORD dst_unused:UNUSED_PAD src0_sel:WORD_1
	global_load_dwordx4 v[4:7], v[30:31], off
	v_pk_add_f32 v[22:23], v[22:23], v[24:25]
	v_cvt_f32_f16_e32 v12, v13
	v_pk_add_f32 v[14:15], v[14:15], v[22:23]
	global_load_dwordx4 v[22:25], v[30:31], off offset:32
	v_cvt_f32_f16_sdwa v13, v13 dst_sel:DWORD dst_unused:UNUSED_PAD src0_sel:WORD_1
	v_cvt_f32_f16_e32 v8, v9
	v_cvt_f32_f16_sdwa v9, v9 dst_sel:DWORD dst_unused:UNUSED_PAD src0_sel:WORD_1
	v_pk_add_f32 v[10:11], v[10:11], v[14:15]
	v_pk_add_f32 v[14:15], v[26:27], v[48:49]
	v_cvt_f32_f16_e32 v20, v21
	v_cvt_f32_f16_sdwa v21, v21 dst_sel:DWORD dst_unused:UNUSED_PAD src0_sel:WORD_1
	v_cvt_f32_f16_e32 v16, v17
	v_cvt_f32_f16_sdwa v17, v17 dst_sel:DWORD dst_unused:UNUSED_PAD src0_sel:WORD_1
	v_cvt_f32_f16_e32 v26, v29
	v_cvt_f32_f16_sdwa v27, v29 dst_sel:DWORD dst_unused:UNUSED_PAD src0_sel:WORD_1
	v_cvt_f32_f16_e32 v28, v33
	v_cvt_f32_f16_sdwa v29, v33 dst_sel:DWORD dst_unused:UNUSED_PAD src0_sel:WORD_1
	v_pk_add_f32 v[8:9], v[12:13], v[8:9]
	v_pk_add_f32 v[12:13], v[20:21], v[16:17]
	v_pk_add_f32 v[8:9], v[14:15], v[8:9]
	v_pk_add_f32 v[14:15], v[26:27], v[28:29]
	v_and_b32_e32 v16, 7, v0
	v_pk_add_f32 v[12:13], v[12:13], v[14:15]
	s_waitcnt vmcnt(1)
	v_mul_f32_e32 v1, v5, v45
	v_fmac_f32_e32 v1, v4, v44
	v_mbcnt_lo_u32_b32 v4, -1, 0
	v_fmac_f32_e32 v1, v6, v46
	v_mbcnt_hi_u32_b32 v14, -1, v4
	v_fmac_f32_e32 v1, v7, v47
	v_and_b32_e32 v5, 64, v14
	s_waitcnt vmcnt(0)
	v_fmac_f32_e32 v1, v22, v10
	v_xor_b32_e32 v4, 1, v14
	v_add_u32_e32 v15, 64, v5
	v_pk_add_f32 v[12:13], v[8:9], v[12:13]
	v_fmac_f32_e32 v1, v23, v11
	v_cmp_lt_i32_e32 vcc, v4, v15
	v_fmac_f32_e32 v1, v24, v12
	v_fmac_f32_e32 v1, v25, v13
	v_cndmask_b32_e32 v4, v14, v4, vcc
	v_lshlrev_b32_e32 v4, 2, v4
	ds_bpermute_b32 v8, v4, v1
	v_lshl_add_u64 v[4:5], s[10:11], 0, v[18:19]
	v_lshl_add_u64 v[6:7], v[4:5], 0, v[36:37]
	v_xor_b32_e32 v4, 2, v14
	v_cmp_lt_i32_e32 vcc, v4, v15
	s_waitcnt lgkmcnt(0)
	v_add_f32_e32 v1, v1, v8
	v_lshl_add_u64 v[8:9], v[6:7], 0, s[0:1]
	v_cndmask_b32_e32 v4, v14, v4, vcc
	v_lshlrev_b32_e32 v4, 2, v4
	ds_bpermute_b32 v4, v4, v1
	s_mov_b32 s0, 0x8000
	s_waitcnt lgkmcnt(0)
	v_add_f32_e32 v1, v1, v4
	v_xor_b32_e32 v4, 4, v14
	v_cmp_lt_i32_e32 vcc, v4, v15
	s_nop 1
	v_cndmask_b32_e32 v4, v14, v4, vcc
	v_lshlrev_b32_e32 v4, 2, v4
	ds_bpermute_b32 v4, v4, v1
	v_add_co_u32_e32 v6, vcc, s0, v6
	s_nop 1
	v_addc_co_u32_e32 v7, vcc, 0, v7, vcc
	v_cmp_eq_u32_e32 vcc, 0, v16
	global_store_dwordx4 v[6:7], v[44:47], off sc1
	global_store_dwordx4 v[8:9], v[10:13], off offset:32 sc1
	s_and_saveexec_b64 s[0:1], vcc
	s_cbranch_execnz .LBB1_3
	s_or_b64 exec, exec, s[0:1]
	v_cmp_gt_u32_e32 vcc, 16, v0
	s_and_saveexec_b64 s[0:1], vcc
	s_cbranch_execnz .LBB1_4

.LBB1_3:
	v_lshl_add_u64 v[6:7], v[34:35], 2, s[10:11]
	s_waitcnt lgkmcnt(0)
	v_add_f32_e32 v1, v1, v4
	v_add_co_u32_e32 v4, vcc, 0x4000, v6
	s_nop 1
	v_addc_co_u32_e32 v5, vcc, 0, v7, vcc
	global_store_dword v[4:5], v1, off sc1
	s_or_b64 exec, exec, s[0:1]
	v_cmp_gt_u32_e32 vcc, 16, v0
	s_and_saveexec_b64 s[0:1], vcc
	s_cbranch_execz .LBB1_2
.LBB1_4:
	s_waitcnt lgkmcnt(0)
	v_pk_add_f32 v[4:5], v[40:41], v[42:43]
	v_pk_add_f32 v[2:3], v[38:39], v[2:3]
	v_or_b32_e32 v0, s2, v0
	v_pk_add_f32 v[2:3], v[4:5], v[2:3]
	v_mov_b32_e32 v1, 0
	v_add_f32_e32 v2, v2, v3
	v_lshl_add_u64 v[0:1], v[0:1], 2, s[10:11]
	global_store_dword v[0:1], v2, off sc1
	s_endpgm
	s_nop 0
	s_nop 0
	s_nop 0
	s_nop 0
	s_nop 0
	s_nop 0
	s_nop 0
	s_nop 0
	s_nop 0
	s_nop 0
	s_nop 0
	s_nop 0
	s_nop 0
	s_nop 0
	s_nop 0
	s_nop 0
	s_nop 0
	s_nop 0
	s_nop 0
	s_nop 0
	s_nop 0
	s_nop 0
	s_nop 0
	s_nop 0
	s_nop 0
	s_nop 0
	s_nop 0
	s_nop 0
	s_nop 0
	s_nop 0
	s_nop 0
	s_endpgm

.LBB2_3:
	s_lshl_b32 s3, s2, 2
	s_and_b32 s3, s3, 28
	s_bfe_u32 s2, s2, 0x20003
	s_load_dwordx2 s[12:13], s[0:1], 0x8
	s_load_dwordx2 s[4:5], s[0:1], 0x28
	s_or_b32 s6, s3, s2
	s_lshl_b32 s2, s6, 8
	s_lshl_b32 s3, s9, 6
	s_or_b32 s3, s3, s2
	s_lshl_b32 s2, s3, 10
	s_waitcnt lgkmcnt(0)
	s_add_u32 s12, s12, s2
	s_addc_u32 s13, s13, 0
	v_lshl_add_u64 v[132:133], s[12:13], 0, v[130:131]
	s_movk_i32 s2, 0x1000
	v_add_co_u32_e32 v6, vcc, s2, v132
	s_movk_i32 s2, 0x2000
	s_nop 0
	v_addc_co_u32_e32 v7, vcc, 0, v133, vcc
	v_add_co_u32_e32 v8, vcc, s2, v132
	global_load_dwordx4 v[66:69], v130, s[12:13] offset:1024
	global_load_dwordx4 v[74:77], v130, s[12:13] offset:2048
	v_addc_co_u32_e32 v9, vcc, 0, v133, vcc
	global_load_dwordx4 v[78:81], v130, s[12:13] offset:3072
	global_load_dwordx4 v[82:85], v[8:9], off offset:-4096
	global_load_dwordx4 v[106:109], v[6:7], off offset:1024
	global_load_dwordx4 v[114:117], v[6:7], off offset:2048
	global_load_dwordx4 v[2:5], v130, s[12:13]
	global_load_dwordx4 v[118:121], v[6:7], off offset:3072
	global_load_dwordx4 v[122:125], v[8:9], off
	global_load_dwordx4 v[102:105], v[8:9], off offset:1024
	global_load_dwordx4 v[86:89], v[8:9], off offset:2048
	global_load_dwordx4 v[70:73], v[8:9], off offset:3072
	s_barrier
	ds_read_b128 v[6:9], v130
	ds_read_b128 v[10:13], v130 offset:4096
	ds_read_b128 v[14:17], v130 offset:8192
	ds_read_b128 v[94:97], v130 offset:12288
	ds_read_b128 v[98:101], v130 offset:1024
	s_waitcnt vmcnt(5) lgkmcnt(4)
	v_mfma_f32_32x32x16_f16 v[50:65], v[6:9], v[2:5], 0
	s_movk_i32 s2, 0x4000
	v_add_co_u32_e32 v146, vcc, s2, v132
	ds_read_b128 v[110:113], v130 offset:5120
	s_nop 0
	v_addc_co_u32_e32 v147, vcc, 0, v133, vcc
	global_load_dwordx4 v[90:93], v[146:147], off offset:-4096
	s_movk_i32 s2, 0x3000
	v_add_co_u32_e32 v148, vcc, s2, v132
	s_waitcnt lgkmcnt(4)
	v_mfma_f32_32x32x16_f16 v[34:49], v[10:13], v[2:5], 0
	v_addc_co_u32_e32 v149, vcc, 0, v133, vcc
	ds_read_b128 v[126:129], v130 offset:9216
	s_waitcnt lgkmcnt(4)
	v_mfma_f32_32x32x16_f16 v[18:33], v[14:17], v[2:5], 0
	s_waitcnt lgkmcnt(3)
	v_mfma_f32_32x32x16_f16 v[2:17], v[94:97], v[2:5], 0
	ds_read_b128 v[134:137], v130 offset:13312
	ds_read_b128 v[138:141], v130 offset:2048
	s_waitcnt lgkmcnt(4)
	v_mfma_f32_32x32x16_f16 v[50:65], v[98:101], v[66:69], v[50:65]
	global_load_dwordx4 v[94:97], v[148:149], off offset:1024
	ds_read_b128 v[98:101], v130 offset:6144
	s_waitcnt lgkmcnt(4)
	v_mfma_f32_32x32x16_f16 v[34:49], v[110:113], v[66:69], v[34:49]
	ds_read_b128 v[142:145], v130 offset:10240
	s_waitcnt lgkmcnt(4)
	v_mfma_f32_32x32x16_f16 v[18:33], v[126:129], v[66:69], v[18:33]
	s_waitcnt lgkmcnt(3)
	v_mfma_f32_32x32x16_f16 v[2:17], v[134:137], v[66:69], v[2:17]
	ds_read_b128 v[126:129], v130 offset:14336
	ds_read_b128 v[66:69], v130 offset:3072
	s_waitcnt lgkmcnt(4)
	v_mfma_f32_32x32x16_f16 v[50:65], v[138:141], v[74:77], v[50:65]
	global_load_dwordx4 v[110:113], v[148:149], off offset:2048
	ds_read_b128 v[134:137], v130 offset:7168
	s_waitcnt lgkmcnt(4)
	v_mfma_f32_32x32x16_f16 v[34:49], v[98:101], v[74:77], v[34:49]
	ds_read_b128 v[138:141], v130 offset:11264
	s_waitcnt lgkmcnt(4)
	v_mfma_f32_32x32x16_f16 v[18:33], v[142:145], v[74:77], v[18:33]
	s_waitcnt lgkmcnt(3)
	v_mfma_f32_32x32x16_f16 v[2:17], v[126:129], v[74:77], v[2:17]
	ds_read_b128 v[142:145], v130 offset:15360
	global_load_dwordx4 v[98:101], v[148:149], off offset:3072
	s_waitcnt lgkmcnt(3)
	v_mfma_f32_32x32x16_f16 v[50:65], v[66:69], v[78:81], v[50:65]
	s_waitcnt lgkmcnt(0)
	s_barrier
	ds_read_b128 v[66:69], v130 offset:16384
	ds_read_b128 v[126:129], v130 offset:20480
	v_mfma_f32_32x32x16_f16 v[34:49], v[134:137], v[78:81], v[34:49]
	ds_read_b128 v[134:137], v130 offset:24576
	v_mfma_f32_32x32x16_f16 v[18:33], v[138:141], v[78:81], v[18:33]
	v_mfma_f32_32x32x16_f16 v[2:17], v[142:145], v[78:81], v[2:17]
	ds_read_b128 v[138:141], v130 offset:28672
	ds_read_b128 v[78:81], v130 offset:17408
	s_waitcnt lgkmcnt(4)
	v_mfma_f32_32x32x16_f16 v[50:65], v[66:69], v[82:85], v[50:65]
	global_load_dwordx4 v[74:77], v[146:147], off
	ds_read_b128 v[66:69], v130 offset:21504
	s_waitcnt lgkmcnt(4)
	v_mfma_f32_32x32x16_f16 v[34:49], v[126:129], v[82:85], v[34:49]
	ds_read_b128 v[126:129], v130 offset:25600
	s_waitcnt lgkmcnt(4)
	v_mfma_f32_32x32x16_f16 v[18:33], v[134:137], v[82:85], v[18:33]
	s_waitcnt lgkmcnt(3)
	v_mfma_f32_32x32x16_f16 v[2:17], v[138:141], v[82:85], v[2:17]
	ds_read_b128 v[134:137], v130 offset:29696
	ds_read_b128 v[82:85], v130 offset:18432
	s_waitcnt lgkmcnt(4)
	v_mfma_f32_32x32x16_f16 v[50:65], v[78:81], v[106:109], v[50:65]
	global_load_dwordx4 v[78:81], v[146:147], off offset:1024
	ds_read_b128 v[138:141], v130 offset:22528
	s_waitcnt lgkmcnt(4)
	v_mfma_f32_32x32x16_f16 v[34:49], v[66:69], v[106:109], v[34:49]
	ds_read_b128 v[66:69], v130 offset:26624
	s_waitcnt lgkmcnt(4)
	v_mfma_f32_32x32x16_f16 v[18:33], v[126:129], v[106:109], v[18:33]
	s_waitcnt lgkmcnt(3)
	v_mfma_f32_32x32x16_f16 v[2:17], v[134:137], v[106:109], v[2:17]
	ds_read_b128 v[126:129], v130 offset:30720
	ds_read_b128 v[106:109], v130 offset:19456
	s_waitcnt lgkmcnt(4)
	v_mfma_f32_32x32x16_f16 v[50:65], v[82:85], v[114:117], v[50:65]
	global_load_dwordx4 v[82:85], v[146:147], off offset:2048
	ds_read_b128 v[134:137], v130 offset:23552
	s_waitcnt lgkmcnt(4)
	v_mfma_f32_32x32x16_f16 v[34:49], v[138:141], v[114:117], v[34:49]
	ds_read_b128 v[138:141], v130 offset:27648
	s_waitcnt lgkmcnt(4)
	v_mfma_f32_32x32x16_f16 v[18:33], v[66:69], v[114:117], v[18:33]
	s_waitcnt lgkmcnt(3)
	v_mfma_f32_32x32x16_f16 v[2:17], v[126:129], v[114:117], v[2:17]
	ds_read_b128 v[142:145], v130 offset:31744
	global_load_dwordx4 v[66:69], v[146:147], off offset:3072
	s_waitcnt vmcnt(12) lgkmcnt(3)
	v_mfma_f32_32x32x16_f16 v[50:65], v[106:109], v[118:121], v[50:65]
	s_waitcnt lgkmcnt(0)
	s_barrier
	ds_read_b128 v[106:109], v130
	ds_read_b128 v[114:117], v130 offset:4096
	v_mfma_f32_32x32x16_f16 v[34:49], v[134:137], v[118:121], v[34:49]
	ds_read_b128 v[126:129], v130 offset:8192
	v_mfma_f32_32x32x16_f16 v[18:33], v[138:141], v[118:121], v[18:33]
	v_mfma_f32_32x32x16_f16 v[2:17], v[142:145], v[118:121], v[2:17]
	ds_read_b128 v[134:137], v130 offset:12288
	ds_read_b128 v[118:121], v130 offset:1024
	s_waitcnt vmcnt(11) lgkmcnt(4)
	v_mfma_f32_32x32x16_f16 v[50:65], v[106:109], v[122:125], v[50:65]
	s_movk_i32 s2, 0x6000
	v_add_co_u32_e32 v146, vcc, s2, v132
	ds_read_b128 v[138:141], v130 offset:5120
	s_nop 0
	v_addc_co_u32_e32 v147, vcc, 0, v133, vcc
	global_load_dwordx4 v[106:109], v[146:147], off offset:-4096
	s_movk_i32 s2, 0x5000
	v_add_co_u32_e32 v148, vcc, s2, v132
	s_waitcnt lgkmcnt(4)
	v_mfma_f32_32x32x16_f16 v[34:49], v[114:117], v[122:125], v[34:49]
	v_addc_co_u32_e32 v149, vcc, 0, v133, vcc
	ds_read_b128 v[142:145], v130 offset:9216
	s_waitcnt lgkmcnt(4)
	v_mfma_f32_32x32x16_f16 v[18:33], v[126:129], v[122:125], v[18:33]
	s_waitcnt lgkmcnt(3)
	v_mfma_f32_32x32x16_f16 v[2:17], v[134:137], v[122:125], v[2:17]
	ds_read_b128 v[126:129], v130 offset:13312
	ds_read_b128 v[122:125], v130 offset:2048
	s_waitcnt vmcnt(11) lgkmcnt(4)
	v_mfma_f32_32x32x16_f16 v[50:65], v[118:121], v[102:105], v[50:65]
	global_load_dwordx4 v[114:117], v[148:149], off offset:1024
	ds_read_b128 v[134:137], v130 offset:6144
	s_waitcnt lgkmcnt(4)
	v_mfma_f32_32x32x16_f16 v[34:49], v[138:141], v[102:105], v[34:49]
	ds_read_b128 v[138:141], v130 offset:10240
	s_waitcnt lgkmcnt(4)
	v_mfma_f32_32x32x16_f16 v[18:33], v[142:145], v[102:105], v[18:33]
	s_waitcnt lgkmcnt(3)
	v_mfma_f32_32x32x16_f16 v[2:17], v[126:129], v[102:105], v[2:17]
	ds_read_b128 v[142:145], v130 offset:14336
	ds_read_b128 v[126:129], v130 offset:3072
	s_waitcnt vmcnt(11) lgkmcnt(4)
	v_mfma_f32_32x32x16_f16 v[50:65], v[122:125], v[86:89], v[50:65]
	global_load_dwordx4 v[118:121], v[148:149], off offset:2048
	ds_read_b128 v[122:125], v130 offset:7168
	s_waitcnt lgkmcnt(4)
	v_mfma_f32_32x32x16_f16 v[34:49], v[134:137], v[86:89], v[34:49]
	ds_read_b128 v[134:137], v130 offset:11264
	s_waitcnt lgkmcnt(4)
	v_mfma_f32_32x32x16_f16 v[18:33], v[138:141], v[86:89], v[18:33]
	s_waitcnt lgkmcnt(3)
	v_mfma_f32_32x32x16_f16 v[2:17], v[142:145], v[86:89], v[2:17]
	ds_read_b128 v[138:141], v130 offset:15360
	global_load_dwordx4 v[102:105], v[148:149], off offset:3072
	s_waitcnt vmcnt(12) lgkmcnt(3)
	v_mfma_f32_32x32x16_f16 v[50:65], v[126:129], v[70:73], v[50:65]
	s_waitcnt lgkmcnt(0)
	s_barrier
	ds_read_b128 v[86:89], v130 offset:16384
	ds_read_b128 v[126:129], v130 offset:20480
	v_mfma_f32_32x32x16_f16 v[34:49], v[122:125], v[70:73], v[34:49]
	ds_read_b128 v[122:125], v130 offset:24576
	v_mfma_f32_32x32x16_f16 v[18:33], v[134:137], v[70:73], v[18:33]
	v_mfma_f32_32x32x16_f16 v[2:17], v[138:141], v[70:73], v[2:17]
	ds_read_b128 v[134:137], v130 offset:28672
	ds_read_b128 v[70:73], v130 offset:17408
	s_waitcnt vmcnt(11) lgkmcnt(4)
	v_mfma_f32_32x32x16_f16 v[50:65], v[86:89], v[90:93], v[50:65]
	global_load_dwordx4 v[86:89], v[146:147], off
	ds_read_b128 v[138:141], v130 offset:21504
	s_waitcnt lgkmcnt(4)
	v_mfma_f32_32x32x16_f16 v[34:49], v[126:129], v[90:93], v[34:49]
	ds_read_b128 v[126:129], v130 offset:25600
	s_waitcnt lgkmcnt(4)
	v_mfma_f32_32x32x16_f16 v[18:33], v[122:125], v[90:93], v[18:33]
	s_waitcnt lgkmcnt(3)
	v_mfma_f32_32x32x16_f16 v[2:17], v[134:137], v[90:93], v[2:17]
	ds_read_b128 v[122:125], v130 offset:29696
	ds_read_b128 v[134:137], v130 offset:18432
	s_waitcnt vmcnt(11) lgkmcnt(4)
	v_mfma_f32_32x32x16_f16 v[50:65], v[70:73], v[94:97], v[50:65]
	global_load_dwordx4 v[90:93], v[146:147], off offset:1024
	ds_read_b128 v[70:73], v130 offset:22528
	s_waitcnt lgkmcnt(4)
	v_mfma_f32_32x32x16_f16 v[34:49], v[138:141], v[94:97], v[34:49]
	ds_read_b128 v[138:141], v130 offset:26624
	s_waitcnt lgkmcnt(4)
	v_mfma_f32_32x32x16_f16 v[18:33], v[126:129], v[94:97], v[18:33]
	s_waitcnt lgkmcnt(3)
	v_mfma_f32_32x32x16_f16 v[2:17], v[122:125], v[94:97], v[2:17]
	ds_read_b128 v[126:129], v130 offset:30720
	ds_read_b128 v[122:125], v130 offset:19456
	s_waitcnt vmcnt(11) lgkmcnt(4)
	v_mfma_f32_32x32x16_f16 v[50:65], v[134:137], v[110:113], v[50:65]
	global_load_dwordx4 v[94:97], v[146:147], off offset:2048
	ds_read_b128 v[134:137], v130 offset:23552
	s_waitcnt lgkmcnt(4)
	v_mfma_f32_32x32x16_f16 v[34:49], v[70:73], v[110:113], v[34:49]
	ds_read_b128 v[142:145], v130 offset:27648
	s_waitcnt lgkmcnt(4)
	v_mfma_f32_32x32x16_f16 v[18:33], v[138:141], v[110:113], v[18:33]
	s_waitcnt lgkmcnt(3)
	v_mfma_f32_32x32x16_f16 v[2:17], v[126:129], v[110:113], v[2:17]
	ds_read_b128 v[138:141], v130 offset:31744
	global_load_dwordx4 v[70:73], v[146:147], off offset:3072
	s_waitcnt vmcnt(12) lgkmcnt(3)
	v_mfma_f32_32x32x16_f16 v[50:65], v[122:125], v[98:101], v[50:65]
	s_waitcnt lgkmcnt(0)
	s_barrier
	ds_read_b128 v[110:113], v130
	ds_read_b128 v[122:125], v130 offset:4096
	v_mfma_f32_32x32x16_f16 v[34:49], v[134:137], v[98:101], v[34:49]
	ds_read_b128 v[126:129], v130 offset:8192
	v_mfma_f32_32x32x16_f16 v[18:33], v[142:145], v[98:101], v[18:33]
	v_mfma_f32_32x32x16_f16 v[2:17], v[138:141], v[98:101], v[2:17]
	ds_read_b128 v[134:137], v130 offset:12288
	ds_read_b128 v[98:101], v130 offset:1024
	s_waitcnt vmcnt(11) lgkmcnt(4)
	v_mfma_f32_32x32x16_f16 v[50:65], v[110:113], v[74:77], v[50:65]
	s_mov_b32 s2, 0x8000
	v_add_co_u32_e32 v146, vcc, s2, v132
	ds_read_b128 v[138:141], v130 offset:5120
	s_nop 0
	v_addc_co_u32_e32 v147, vcc, 0, v133, vcc
	global_load_dwordx4 v[110:113], v[146:147], off offset:-4096
	s_movk_i32 s2, 0x7000
	v_add_co_u32_e32 v148, vcc, s2, v132
	s_waitcnt lgkmcnt(4)
	v_mfma_f32_32x32x16_f16 v[34:49], v[122:125], v[74:77], v[34:49]
	v_addc_co_u32_e32 v149, vcc, 0, v133, vcc
	ds_read_b128 v[142:145], v130 offset:9216
	s_waitcnt lgkmcnt(4)
	v_mfma_f32_32x32x16_f16 v[18:33], v[126:129], v[74:77], v[18:33]
	s_waitcnt lgkmcnt(3)
	v_mfma_f32_32x32x16_f16 v[2:17], v[134:137], v[74:77], v[2:17]
	ds_read_b128 v[126:129], v130 offset:13312
	ds_read_b128 v[74:77], v130 offset:2048
	s_waitcnt vmcnt(11) lgkmcnt(4)
	v_mfma_f32_32x32x16_f16 v[50:65], v[98:101], v[78:81], v[50:65]
	global_load_dwordx4 v[122:125], v[148:149], off offset:1024
	ds_read_b128 v[98:101], v130 offset:6144
	s_waitcnt lgkmcnt(4)
	v_mfma_f32_32x32x16_f16 v[34:49], v[138:141], v[78:81], v[34:49]
	ds_read_b128 v[134:137], v130 offset:10240
	s_waitcnt lgkmcnt(4)
	v_mfma_f32_32x32x16_f16 v[18:33], v[142:145], v[78:81], v[18:33]
	s_waitcnt lgkmcnt(3)
	v_mfma_f32_32x32x16_f16 v[2:17], v[126:129], v[78:81], v[2:17]
	ds_read_b128 v[138:141], v130 offset:14336
	ds_read_b128 v[78:81], v130 offset:3072
	s_waitcnt vmcnt(11) lgkmcnt(4)
	v_mfma_f32_32x32x16_f16 v[50:65], v[74:77], v[82:85], v[50:65]
	global_load_dwordx4 v[126:129], v[148:149], off offset:2048
	ds_read_b128 v[74:77], v130 offset:7168
	s_waitcnt lgkmcnt(4)
	v_mfma_f32_32x32x16_f16 v[34:49], v[98:101], v[82:85], v[34:49]
	ds_read_b128 v[142:145], v130 offset:11264
	s_waitcnt lgkmcnt(4)
	v_mfma_f32_32x32x16_f16 v[18:33], v[134:137], v[82:85], v[18:33]
	s_waitcnt lgkmcnt(3)
	v_mfma_f32_32x32x16_f16 v[2:17], v[138:141], v[82:85], v[2:17]
	ds_read_b128 v[134:137], v130 offset:15360
	global_load_dwordx4 v[98:101], v[148:149], off offset:3072
	s_waitcnt vmcnt(12) lgkmcnt(3)
	v_mfma_f32_32x32x16_f16 v[50:65], v[78:81], v[66:69], v[50:65]
	s_waitcnt lgkmcnt(0)
	s_barrier
	ds_read_b128 v[78:81], v130 offset:16384
	ds_read_b128 v[82:85], v130 offset:20480
	v_mfma_f32_32x32x16_f16 v[34:49], v[74:77], v[66:69], v[34:49]
	ds_read_b128 v[138:141], v130 offset:24576
	v_mfma_f32_32x32x16_f16 v[18:33], v[142:145], v[66:69], v[18:33]
	v_mfma_f32_32x32x16_f16 v[2:17], v[134:137], v[66:69], v[2:17]
	ds_read_b128 v[142:145], v130 offset:28672
	ds_read_b128 v[66:69], v130 offset:17408
	s_waitcnt vmcnt(11) lgkmcnt(4)
	v_mfma_f32_32x32x16_f16 v[50:65], v[78:81], v[106:109], v[50:65]
	global_load_dwordx4 v[74:77], v[146:147], off
	ds_read_b128 v[134:137], v130 offset:21504
	s_waitcnt lgkmcnt(4)
	v_mfma_f32_32x32x16_f16 v[34:49], v[82:85], v[106:109], v[34:49]
	ds_read_b128 v[82:85], v130 offset:25600
	s_waitcnt lgkmcnt(4)
	v_mfma_f32_32x32x16_f16 v[18:33], v[138:141], v[106:109], v[18:33]
	s_waitcnt lgkmcnt(3)
	v_mfma_f32_32x32x16_f16 v[2:17], v[142:145], v[106:109], v[2:17]
	ds_read_b128 v[138:141], v130 offset:29696
	ds_read_b128 v[106:109], v130 offset:18432
	s_waitcnt vmcnt(11) lgkmcnt(4)
	v_mfma_f32_32x32x16_f16 v[50:65], v[66:69], v[114:117], v[50:65]
	global_load_dwordx4 v[78:81], v[146:147], off offset:1024
	ds_read_b128 v[66:69], v130 offset:22528
	s_waitcnt lgkmcnt(4)
	v_mfma_f32_32x32x16_f16 v[34:49], v[134:137], v[114:117], v[34:49]
	ds_read_b128 v[134:137], v130 offset:26624
	s_waitcnt lgkmcnt(4)
	v_mfma_f32_32x32x16_f16 v[18:33], v[82:85], v[114:117], v[18:33]
	s_waitcnt lgkmcnt(3)
	v_mfma_f32_32x32x16_f16 v[2:17], v[138:141], v[114:117], v[2:17]
	ds_read_b128 v[142:145], v130 offset:30720
	ds_read_b128 v[114:117], v130 offset:19456
	s_waitcnt vmcnt(11) lgkmcnt(4)
	v_mfma_f32_32x32x16_f16 v[50:65], v[106:109], v[118:121], v[50:65]
	global_load_dwordx4 v[82:85], v[146:147], off offset:2048
	ds_read_b128 v[106:109], v130 offset:23552
	s_waitcnt lgkmcnt(4)
	v_mfma_f32_32x32x16_f16 v[34:49], v[66:69], v[118:121], v[34:49]
	ds_read_b128 v[138:141], v130 offset:27648
	s_waitcnt lgkmcnt(4)
	v_mfma_f32_32x32x16_f16 v[18:33], v[134:137], v[118:121], v[18:33]
	s_waitcnt lgkmcnt(3)
	v_mfma_f32_32x32x16_f16 v[2:17], v[142:145], v[118:121], v[2:17]
	ds_read_b128 v[134:137], v130 offset:31744
	global_load_dwordx4 v[66:69], v[146:147], off offset:3072
	s_waitcnt vmcnt(12) lgkmcnt(3)
	v_mfma_f32_32x32x16_f16 v[50:65], v[114:117], v[102:105], v[50:65]
	s_waitcnt lgkmcnt(0)
	s_barrier
	ds_read_b128 v[114:117], v130
	ds_read_b128 v[118:121], v130 offset:4096
	v_mfma_f32_32x32x16_f16 v[34:49], v[106:109], v[102:105], v[34:49]
	ds_read_b128 v[142:145], v130 offset:8192
	v_mfma_f32_32x32x16_f16 v[18:33], v[138:141], v[102:105], v[18:33]
	v_mfma_f32_32x32x16_f16 v[2:17], v[134:137], v[102:105], v[2:17]
	ds_read_b128 v[138:141], v130 offset:12288
	ds_read_b128 v[102:105], v130 offset:1024
	s_waitcnt vmcnt(11) lgkmcnt(4)
	v_mfma_f32_32x32x16_f16 v[50:65], v[114:117], v[86:89], v[50:65]
	s_mov_b32 s2, 0xa000
	v_add_co_u32_e32 v146, vcc, s2, v132
	s_waitcnt lgkmcnt(3)
	v_mfma_f32_32x32x16_f16 v[34:49], v[118:121], v[86:89], v[34:49]
	v_addc_co_u32_e32 v147, vcc, 0, v133, vcc
	global_load_dwordx4 v[106:109], v[146:147], off offset:-4096
	ds_read_b128 v[118:121], v130 offset:5120
	s_mov_b32 s2, 0x9000
	v_add_co_u32_e32 v148, vcc, s2, v132
	s_nop 1
	v_addc_co_u32_e32 v149, vcc, 0, v133, vcc
	ds_read_b128 v[134:137], v130 offset:9216
	s_waitcnt lgkmcnt(4)
	v_mfma_f32_32x32x16_f16 v[18:33], v[142:145], v[86:89], v[18:33]
	s_waitcnt lgkmcnt(3)
	v_mfma_f32_32x32x16_f16 v[2:17], v[138:141], v[86:89], v[2:17]
	ds_read_b128 v[142:145], v130 offset:13312
	ds_read_b128 v[86:89], v130 offset:2048
	s_waitcnt vmcnt(11) lgkmcnt(4)
	v_mfma_f32_32x32x16_f16 v[50:65], v[102:105], v[90:93], v[50:65]
	global_load_dwordx4 v[114:117], v[148:149], off offset:1024
	ds_read_b128 v[102:105], v130 offset:6144
	s_waitcnt lgkmcnt(4)
	v_mfma_f32_32x32x16_f16 v[34:49], v[118:121], v[90:93], v[34:49]
	ds_read_b128 v[138:141], v130 offset:10240
	s_waitcnt lgkmcnt(4)
	v_mfma_f32_32x32x16_f16 v[18:33], v[134:137], v[90:93], v[18:33]
	s_waitcnt lgkmcnt(3)
	v_mfma_f32_32x32x16_f16 v[2:17], v[142:145], v[90:93], v[2:17]
	ds_read_b128 v[134:137], v130 offset:14336
	ds_read_b128 v[90:93], v130 offset:3072
	s_waitcnt vmcnt(11) lgkmcnt(4)
	v_mfma_f32_32x32x16_f16 v[50:65], v[86:89], v[94:97], v[50:65]
	global_load_dwordx4 v[118:121], v[148:149], off offset:2048
	ds_read_b128 v[86:89], v130 offset:7168
	s_waitcnt lgkmcnt(4)
	v_mfma_f32_32x32x16_f16 v[34:49], v[102:105], v[94:97], v[34:49]
	ds_read_b128 v[142:145], v130 offset:11264
	s_waitcnt lgkmcnt(4)
	v_mfma_f32_32x32x16_f16 v[18:33], v[138:141], v[94:97], v[18:33]
	s_waitcnt lgkmcnt(3)
	v_mfma_f32_32x32x16_f16 v[2:17], v[134:137], v[94:97], v[2:17]
	ds_read_b128 v[138:141], v130 offset:15360
	global_load_dwordx4 v[102:105], v[148:149], off offset:3072
	s_waitcnt vmcnt(12) lgkmcnt(3)
	v_mfma_f32_32x32x16_f16 v[50:65], v[90:93], v[70:73], v[50:65]
	s_waitcnt lgkmcnt(0)
	s_barrier
	ds_read_b128 v[90:93], v130 offset:16384
	ds_read_b128 v[94:97], v130 offset:20480
	v_mfma_f32_32x32x16_f16 v[34:49], v[86:89], v[70:73], v[34:49]
	ds_read_b128 v[134:137], v130 offset:24576
	v_mfma_f32_32x32x16_f16 v[18:33], v[142:145], v[70:73], v[18:33]
	v_mfma_f32_32x32x16_f16 v[2:17], v[138:141], v[70:73], v[2:17]
	ds_read_b128 v[142:145], v130 offset:28672
	ds_read_b128 v[70:73], v130 offset:17408
	s_waitcnt vmcnt(11) lgkmcnt(4)
	v_mfma_f32_32x32x16_f16 v[50:65], v[90:93], v[110:113], v[50:65]
	global_load_dwordx4 v[86:89], v[146:147], off
	ds_read_b128 v[138:141], v130 offset:21504
	s_waitcnt lgkmcnt(4)
	v_mfma_f32_32x32x16_f16 v[34:49], v[94:97], v[110:113], v[34:49]
	ds_read_b128 v[94:97], v130 offset:25600
	s_waitcnt lgkmcnt(4)
	v_mfma_f32_32x32x16_f16 v[18:33], v[134:137], v[110:113], v[18:33]
	s_waitcnt lgkmcnt(3)
	v_mfma_f32_32x32x16_f16 v[2:17], v[142:145], v[110:113], v[2:17]
	ds_read_b128 v[134:137], v130 offset:29696
	ds_read_b128 v[110:113], v130 offset:18432
	s_waitcnt vmcnt(11) lgkmcnt(4)
	v_mfma_f32_32x32x16_f16 v[50:65], v[70:73], v[122:125], v[50:65]
	global_load_dwordx4 v[90:93], v[146:147], off offset:1024
	ds_read_b128 v[70:73], v130 offset:22528
	s_waitcnt lgkmcnt(4)
	v_mfma_f32_32x32x16_f16 v[34:49], v[138:141], v[122:125], v[34:49]
	ds_read_b128 v[138:141], v130 offset:26624
	s_waitcnt lgkmcnt(4)
	v_mfma_f32_32x32x16_f16 v[18:33], v[94:97], v[122:125], v[18:33]
	s_waitcnt lgkmcnt(3)
	v_mfma_f32_32x32x16_f16 v[2:17], v[134:137], v[122:125], v[2:17]
	ds_read_b128 v[142:145], v130 offset:30720
	ds_read_b128 v[122:125], v130 offset:19456
	s_waitcnt vmcnt(11) lgkmcnt(4)
	v_mfma_f32_32x32x16_f16 v[50:65], v[110:113], v[126:129], v[50:65]
	global_load_dwordx4 v[94:97], v[146:147], off offset:2048
	ds_read_b128 v[110:113], v130 offset:23552
	s_waitcnt lgkmcnt(4)
	v_mfma_f32_32x32x16_f16 v[34:49], v[70:73], v[126:129], v[34:49]
	ds_read_b128 v[134:137], v130 offset:27648
	s_waitcnt lgkmcnt(4)
	v_mfma_f32_32x32x16_f16 v[18:33], v[138:141], v[126:129], v[18:33]
	s_waitcnt lgkmcnt(3)
	v_mfma_f32_32x32x16_f16 v[2:17], v[142:145], v[126:129], v[2:17]
	ds_read_b128 v[138:141], v130 offset:31744
	global_load_dwordx4 v[70:73], v[146:147], off offset:3072
	s_waitcnt vmcnt(12) lgkmcnt(3)
	v_mfma_f32_32x32x16_f16 v[50:65], v[122:125], v[98:101], v[50:65]
	s_waitcnt lgkmcnt(0)
	s_barrier
	ds_read_b128 v[122:125], v130
	ds_read_b128 v[126:129], v130 offset:4096
	v_mfma_f32_32x32x16_f16 v[34:49], v[110:113], v[98:101], v[34:49]
	ds_read_b128 v[142:145], v130 offset:8192
	v_mfma_f32_32x32x16_f16 v[18:33], v[134:137], v[98:101], v[18:33]
	v_mfma_f32_32x32x16_f16 v[2:17], v[138:141], v[98:101], v[2:17]
	ds_read_b128 v[134:137], v130 offset:12288
	ds_read_b128 v[98:101], v130 offset:1024
	s_waitcnt vmcnt(11) lgkmcnt(4)
	v_mfma_f32_32x32x16_f16 v[50:65], v[122:125], v[74:77], v[50:65]
	s_mov_b32 s2, 0xc000
	v_add_co_u32_e32 v146, vcc, s2, v132
	s_waitcnt lgkmcnt(3)
	v_mfma_f32_32x32x16_f16 v[34:49], v[126:129], v[74:77], v[34:49]
	v_addc_co_u32_e32 v147, vcc, 0, v133, vcc
	global_load_dwordx4 v[110:113], v[146:147], off offset:-4096
	ds_read_b128 v[126:129], v130 offset:5120
	s_mov_b32 s2, 0xb000
	v_add_co_u32_e32 v148, vcc, s2, v132
	s_nop 1
	v_addc_co_u32_e32 v149, vcc, 0, v133, vcc
	ds_read_b128 v[138:141], v130 offset:9216
	s_waitcnt lgkmcnt(4)
	v_mfma_f32_32x32x16_f16 v[18:33], v[142:145], v[74:77], v[18:33]
	s_waitcnt lgkmcnt(3)
	v_mfma_f32_32x32x16_f16 v[2:17], v[134:137], v[74:77], v[2:17]
	ds_read_b128 v[142:145], v130 offset:13312
	ds_read_b128 v[74:77], v130 offset:2048
	s_waitcnt vmcnt(11) lgkmcnt(4)
	v_mfma_f32_32x32x16_f16 v[50:65], v[98:101], v[78:81], v[50:65]
	global_load_dwordx4 v[122:125], v[148:149], off offset:1024
	ds_read_b128 v[98:101], v130 offset:6144
	s_waitcnt lgkmcnt(4)
	v_mfma_f32_32x32x16_f16 v[34:49], v[126:129], v[78:81], v[34:49]
	ds_read_b128 v[134:137], v130 offset:10240
	s_waitcnt lgkmcnt(4)
	v_mfma_f32_32x32x16_f16 v[18:33], v[138:141], v[78:81], v[18:33]
	s_waitcnt lgkmcnt(3)
	v_mfma_f32_32x32x16_f16 v[2:17], v[142:145], v[78:81], v[2:17]
	ds_read_b128 v[138:141], v130 offset:14336
	ds_read_b128 v[78:81], v130 offset:3072
	s_waitcnt vmcnt(11) lgkmcnt(4)
	v_mfma_f32_32x32x16_f16 v[50:65], v[74:77], v[82:85], v[50:65]
	global_load_dwordx4 v[126:129], v[148:149], off offset:2048
	ds_read_b128 v[142:145], v130 offset:7168
	s_waitcnt lgkmcnt(4)
	v_mfma_f32_32x32x16_f16 v[34:49], v[98:101], v[82:85], v[34:49]
	ds_read_b128 v[98:101], v130 offset:11264
	s_waitcnt lgkmcnt(4)
	v_mfma_f32_32x32x16_f16 v[18:33], v[134:137], v[82:85], v[18:33]
	s_waitcnt lgkmcnt(3)
	v_mfma_f32_32x32x16_f16 v[2:17], v[138:141], v[82:85], v[2:17]
	ds_read_b128 v[134:137], v130 offset:15360
	global_load_dwordx4 v[74:77], v[148:149], off offset:3072
	s_waitcnt vmcnt(12) lgkmcnt(3)
	v_mfma_f32_32x32x16_f16 v[50:65], v[78:81], v[66:69], v[50:65]
	s_waitcnt lgkmcnt(0)
	s_barrier
	ds_read_b128 v[78:81], v130 offset:16384
	ds_read_b128 v[82:85], v130 offset:20480
	v_mfma_f32_32x32x16_f16 v[34:49], v[142:145], v[66:69], v[34:49]
	ds_read_b128 v[138:141], v130 offset:24576
	v_mfma_f32_32x32x16_f16 v[18:33], v[98:101], v[66:69], v[18:33]
	v_mfma_f32_32x32x16_f16 v[2:17], v[134:137], v[66:69], v[2:17]
	ds_read_b128 v[98:101], v130 offset:28672
	ds_read_b128 v[66:69], v130 offset:17408
	s_waitcnt vmcnt(11) lgkmcnt(4)
	v_mfma_f32_32x32x16_f16 v[50:65], v[78:81], v[106:109], v[50:65]
	global_load_dwordx4 v[78:81], v[146:147], off
	ds_read_b128 v[134:137], v130 offset:21504
	s_waitcnt lgkmcnt(4)
	v_mfma_f32_32x32x16_f16 v[34:49], v[82:85], v[106:109], v[34:49]
	ds_read_b128 v[142:145], v130 offset:25600
	s_waitcnt lgkmcnt(4)
	v_mfma_f32_32x32x16_f16 v[18:33], v[138:141], v[106:109], v[18:33]
	s_waitcnt lgkmcnt(3)
	v_mfma_f32_32x32x16_f16 v[2:17], v[98:101], v[106:109], v[2:17]
	ds_read_b128 v[138:141], v130 offset:29696
	ds_read_b128 v[98:101], v130 offset:18432
	s_waitcnt vmcnt(11) lgkmcnt(4)
	v_mfma_f32_32x32x16_f16 v[50:65], v[66:69], v[114:117], v[50:65]
	global_load_dwordx4 v[82:85], v[146:147], off offset:1024
	ds_read_b128 v[66:69], v130 offset:22528
	s_waitcnt lgkmcnt(4)
	v_mfma_f32_32x32x16_f16 v[34:49], v[134:137], v[114:117], v[34:49]
	ds_read_b128 v[106:109], v130 offset:26624
	s_waitcnt lgkmcnt(4)
	v_mfma_f32_32x32x16_f16 v[18:33], v[142:145], v[114:117], v[18:33]
	s_waitcnt lgkmcnt(3)
	v_mfma_f32_32x32x16_f16 v[2:17], v[138:141], v[114:117], v[2:17]
	ds_read_b128 v[134:137], v130 offset:30720
	ds_read_b128 v[114:117], v130 offset:19456
	s_waitcnt vmcnt(11) lgkmcnt(4)
	v_mfma_f32_32x32x16_f16 v[50:65], v[98:101], v[118:121], v[50:65]
	global_load_dwordx4 v[98:101], v[146:147], off offset:2048
	ds_read_b128 v[138:141], v130 offset:23552
	s_waitcnt lgkmcnt(4)
	v_mfma_f32_32x32x16_f16 v[34:49], v[66:69], v[118:121], v[34:49]
	ds_read_b128 v[142:145], v130 offset:27648
	s_waitcnt lgkmcnt(4)
	v_mfma_f32_32x32x16_f16 v[18:33], v[106:109], v[118:121], v[18:33]
	s_waitcnt lgkmcnt(3)
	v_mfma_f32_32x32x16_f16 v[2:17], v[134:137], v[118:121], v[2:17]
	ds_read_b128 v[106:109], v130 offset:31744
	global_load_dwordx4 v[66:69], v[146:147], off offset:3072
	s_waitcnt vmcnt(12) lgkmcnt(3)
	v_mfma_f32_32x32x16_f16 v[50:65], v[114:117], v[102:105], v[50:65]
	s_waitcnt lgkmcnt(0)
	s_barrier
	ds_read_b128 v[114:117], v130
	ds_read_b128 v[118:121], v130 offset:4096
	v_mfma_f32_32x32x16_f16 v[34:49], v[138:141], v[102:105], v[34:49]
	ds_read_b128 v[134:137], v130 offset:8192
	v_mfma_f32_32x32x16_f16 v[18:33], v[142:145], v[102:105], v[18:33]
	v_mfma_f32_32x32x16_f16 v[2:17], v[106:109], v[102:105], v[2:17]
	ds_read_b128 v[138:141], v130 offset:12288
	ds_read_b128 v[106:109], v130 offset:1024
	s_waitcnt vmcnt(11) lgkmcnt(4)
	v_mfma_f32_32x32x16_f16 v[50:65], v[114:117], v[86:89], v[50:65]
	s_mov_b32 s2, 0xe000
	v_add_co_u32_e32 v146, vcc, s2, v132
	ds_read_b128 v[114:117], v130 offset:5120
	s_nop 0
	v_addc_co_u32_e32 v147, vcc, 0, v133, vcc
	global_load_dwordx4 v[102:105], v[146:147], off offset:-4096
	s_mov_b32 s2, 0xd000
	v_add_co_u32_e32 v148, vcc, s2, v132
	s_waitcnt lgkmcnt(4)
	v_mfma_f32_32x32x16_f16 v[34:49], v[118:121], v[86:89], v[34:49]
	v_addc_co_u32_e32 v149, vcc, 0, v133, vcc
	ds_read_b128 v[118:121], v130 offset:9216
	s_waitcnt lgkmcnt(4)
	v_mfma_f32_32x32x16_f16 v[18:33], v[134:137], v[86:89], v[18:33]
	s_waitcnt lgkmcnt(3)
	v_mfma_f32_32x32x16_f16 v[2:17], v[138:141], v[86:89], v[2:17]
	ds_read_b128 v[134:137], v130 offset:13312
	ds_read_b128 v[86:89], v130 offset:2048
	s_waitcnt vmcnt(11) lgkmcnt(4)
	v_mfma_f32_32x32x16_f16 v[50:65], v[106:109], v[90:93], v[50:65]
	global_load_dwordx4 v[106:109], v[148:149], off offset:1024
	ds_read_b128 v[138:141], v130 offset:6144
	s_waitcnt lgkmcnt(4)
	v_mfma_f32_32x32x16_f16 v[34:49], v[114:117], v[90:93], v[34:49]
	ds_read_b128 v[114:117], v130 offset:10240
	s_waitcnt lgkmcnt(4)
	v_mfma_f32_32x32x16_f16 v[18:33], v[118:121], v[90:93], v[18:33]
	s_waitcnt lgkmcnt(3)
	v_mfma_f32_32x32x16_f16 v[2:17], v[134:137], v[90:93], v[2:17]
	ds_read_b128 v[118:121], v130 offset:14336
	ds_read_b128 v[134:137], v130 offset:3072
	s_waitcnt vmcnt(11) lgkmcnt(4)
	v_mfma_f32_32x32x16_f16 v[50:65], v[86:89], v[94:97], v[50:65]
	global_load_dwordx4 v[90:93], v[148:149], off offset:2048
	ds_read_b128 v[142:145], v130 offset:7168
	s_waitcnt lgkmcnt(4)
	v_mfma_f32_32x32x16_f16 v[34:49], v[138:141], v[94:97], v[34:49]
	ds_read_b128 v[138:141], v130 offset:11264
	s_waitcnt lgkmcnt(4)
	v_mfma_f32_32x32x16_f16 v[18:33], v[114:117], v[94:97], v[18:33]
	s_waitcnt lgkmcnt(3)
	v_mfma_f32_32x32x16_f16 v[2:17], v[118:121], v[94:97], v[2:17]
	ds_read_b128 v[114:117], v130 offset:15360
	global_load_dwordx4 v[86:89], v[148:149], off offset:3072
	s_waitcnt vmcnt(12) lgkmcnt(3)
	v_mfma_f32_32x32x16_f16 v[50:65], v[134:137], v[70:73], v[50:65]
	s_waitcnt lgkmcnt(0)
	s_barrier
	ds_read_b128 v[94:97], v130 offset:16384
	ds_read_b128 v[118:121], v130 offset:20480
	v_mfma_f32_32x32x16_f16 v[34:49], v[142:145], v[70:73], v[34:49]
	ds_read_b128 v[134:137], v130 offset:24576
	v_mfma_f32_32x32x16_f16 v[18:33], v[138:141], v[70:73], v[18:33]
	v_mfma_f32_32x32x16_f16 v[2:17], v[114:117], v[70:73], v[2:17]
	ds_read_b128 v[138:141], v130 offset:28672
	ds_read_b128 v[70:73], v130 offset:17408
	s_waitcnt vmcnt(11) lgkmcnt(4)
	v_mfma_f32_32x32x16_f16 v[50:65], v[94:97], v[110:113], v[50:65]
	global_load_dwordx4 v[94:97], v[146:147], off
	ds_read_b128 v[114:117], v130 offset:21504
	s_waitcnt lgkmcnt(4)
	v_mfma_f32_32x32x16_f16 v[34:49], v[118:121], v[110:113], v[34:49]
	ds_read_b128 v[118:121], v130 offset:25600
	s_waitcnt lgkmcnt(4)
	v_mfma_f32_32x32x16_f16 v[18:33], v[134:137], v[110:113], v[18:33]
	s_waitcnt lgkmcnt(3)
	v_mfma_f32_32x32x16_f16 v[2:17], v[138:141], v[110:113], v[2:17]
	ds_read_b128 v[134:137], v130 offset:29696
	ds_read_b128 v[138:141], v130 offset:18432
	s_waitcnt vmcnt(11) lgkmcnt(4)
	v_mfma_f32_32x32x16_f16 v[50:65], v[70:73], v[122:125], v[50:65]
	global_load_dwordx4 v[110:113], v[146:147], off offset:1024
	ds_read_b128 v[70:73], v130 offset:22528
	s_waitcnt lgkmcnt(4)
	v_mfma_f32_32x32x16_f16 v[34:49], v[114:117], v[122:125], v[34:49]
	ds_read_b128 v[142:145], v130 offset:26624
	s_waitcnt lgkmcnt(4)
	v_mfma_f32_32x32x16_f16 v[18:33], v[118:121], v[122:125], v[18:33]
	s_waitcnt lgkmcnt(3)
	v_mfma_f32_32x32x16_f16 v[2:17], v[134:137], v[122:125], v[2:17]
	ds_read_b128 v[118:121], v130 offset:30720
	ds_read_b128 v[122:125], v130 offset:19456
	s_waitcnt vmcnt(11) lgkmcnt(4)
	v_mfma_f32_32x32x16_f16 v[50:65], v[138:141], v[126:129], v[50:65]
	global_load_dwordx4 v[114:117], v[146:147], off offset:2048
	ds_read_b128 v[134:137], v130 offset:23552
	s_waitcnt lgkmcnt(4)
	v_mfma_f32_32x32x16_f16 v[34:49], v[70:73], v[126:129], v[34:49]
	ds_read_b128 v[138:141], v130 offset:27648
	s_waitcnt lgkmcnt(4)
	v_mfma_f32_32x32x16_f16 v[18:33], v[142:145], v[126:129], v[18:33]
	s_waitcnt lgkmcnt(3)
	v_mfma_f32_32x32x16_f16 v[2:17], v[118:121], v[126:129], v[2:17]
	ds_read_b128 v[142:145], v130 offset:31744
	global_load_dwordx4 v[70:73], v[146:147], off offset:3072
	s_waitcnt vmcnt(12) lgkmcnt(3)
	v_mfma_f32_32x32x16_f16 v[50:65], v[122:125], v[74:77], v[50:65]
	s_waitcnt lgkmcnt(0)
	s_barrier
	ds_read_b128 v[118:121], v130
	ds_read_b128 v[122:125], v130 offset:4096
	v_mfma_f32_32x32x16_f16 v[34:49], v[134:137], v[74:77], v[34:49]
	ds_read_b128 v[126:129], v130 offset:8192
	v_mfma_f32_32x32x16_f16 v[18:33], v[138:141], v[74:77], v[18:33]
	v_mfma_f32_32x32x16_f16 v[2:17], v[142:145], v[74:77], v[2:17]
	ds_read_b128 v[134:137], v130 offset:12288
	ds_read_b128 v[138:141], v130 offset:1024
	s_waitcnt vmcnt(11) lgkmcnt(4)
	v_mfma_f32_32x32x16_f16 v[50:65], v[118:121], v[78:81], v[50:65]
	s_mov_b32 s2, 0xf000
	v_add_co_u32_e32 v142, vcc, s2, v132
	ds_read_b128 v[118:121], v130 offset:5120
	s_nop 0
	v_addc_co_u32_e32 v143, vcc, 0, v133, vcc
	global_load_dwordx4 v[74:77], v[142:143], off
	s_waitcnt lgkmcnt(4)
	v_mfma_f32_32x32x16_f16 v[34:49], v[122:125], v[78:81], v[34:49]
	ds_read_b128 v[122:125], v130 offset:9216
	s_waitcnt lgkmcnt(4)
	v_mfma_f32_32x32x16_f16 v[18:33], v[126:129], v[78:81], v[18:33]
	s_waitcnt lgkmcnt(3)
	v_mfma_f32_32x32x16_f16 v[2:17], v[134:137], v[78:81], v[2:17]
	ds_read_b128 v[126:129], v130 offset:13312
	ds_read_b128 v[132:135], v130 offset:2048
	s_waitcnt vmcnt(11) lgkmcnt(4)
	v_mfma_f32_32x32x16_f16 v[50:65], v[138:141], v[82:85], v[50:65]
	global_load_dwordx4 v[78:81], v[142:143], off offset:1024
	ds_read_b128 v[136:139], v130 offset:6144
	s_waitcnt lgkmcnt(4)
	v_mfma_f32_32x32x16_f16 v[34:49], v[118:121], v[82:85], v[34:49]
	ds_read_b128 v[118:121], v130 offset:10240
	s_waitcnt lgkmcnt(4)
	v_mfma_f32_32x32x16_f16 v[18:33], v[122:125], v[82:85], v[18:33]
	s_waitcnt lgkmcnt(3)
	v_mfma_f32_32x32x16_f16 v[2:17], v[126:129], v[82:85], v[2:17]
	ds_read_b128 v[122:125], v130 offset:14336
	ds_read_b128 v[126:129], v130 offset:3072
	s_waitcnt vmcnt(11) lgkmcnt(4)
	v_mfma_f32_32x32x16_f16 v[50:65], v[132:135], v[98:101], v[50:65]
	global_load_dwordx4 v[82:85], v[142:143], off offset:2048
	ds_read_b128 v[132:135], v130 offset:7168
	s_waitcnt lgkmcnt(4)
	v_mfma_f32_32x32x16_f16 v[34:49], v[136:139], v[98:101], v[34:49]
	ds_read_b128 v[136:139], v130 offset:11264
	s_waitcnt lgkmcnt(4)
	v_mfma_f32_32x32x16_f16 v[18:33], v[118:121], v[98:101], v[18:33]
	s_waitcnt lgkmcnt(3)
	v_mfma_f32_32x32x16_f16 v[2:17], v[122:125], v[98:101], v[2:17]
	ds_read_b128 v[118:121], v130 offset:15360
	global_load_dwordx4 v[98:101], v[142:143], off offset:3072
	s_waitcnt vmcnt(12) lgkmcnt(3)
	v_mfma_f32_32x32x16_f16 v[50:65], v[126:129], v[66:69], v[50:65]
	s_waitcnt lgkmcnt(0)
	s_barrier
	ds_read_b128 v[122:125], v130 offset:16384
	ds_read_b128 v[126:129], v130 offset:20480
	v_mfma_f32_32x32x16_f16 v[34:49], v[132:135], v[66:69], v[34:49]
	ds_read_b128 v[132:135], v130 offset:24576
	v_mfma_f32_32x32x16_f16 v[18:33], v[136:139], v[66:69], v[18:33]
	v_mfma_f32_32x32x16_f16 v[2:17], v[118:121], v[66:69], v[2:17]
	ds_read_b128 v[136:139], v130 offset:28672
	ds_read_b128 v[66:69], v130 offset:17408
	s_waitcnt vmcnt(11) lgkmcnt(4)
	v_mfma_f32_32x32x16_f16 v[50:65], v[122:125], v[102:105], v[50:65]
	ds_read_b128 v[118:121], v130 offset:21504
	s_waitcnt lgkmcnt(4)
	v_mfma_f32_32x32x16_f16 v[34:49], v[126:129], v[102:105], v[34:49]
	ds_read_b128 v[122:125], v130 offset:25600
	s_waitcnt lgkmcnt(4)
	v_mfma_f32_32x32x16_f16 v[18:33], v[132:135], v[102:105], v[18:33]
	s_waitcnt lgkmcnt(3)
	v_mfma_f32_32x32x16_f16 v[2:17], v[136:139], v[102:105], v[2:17]
	ds_read_b128 v[126:129], v130 offset:29696
	s_waitcnt vmcnt(10) lgkmcnt(3)
	v_mfma_f32_32x32x16_f16 v[50:65], v[66:69], v[106:109], v[50:65]
	ds_read_b128 v[66:69], v130 offset:18432
	ds_read_b128 v[102:105], v130 offset:22528
	s_waitcnt lgkmcnt(4)
	v_mfma_f32_32x32x16_f16 v[34:49], v[118:121], v[106:109], v[34:49]
	ds_read_b128 v[118:121], v130 offset:26624
	s_waitcnt lgkmcnt(4)
	v_mfma_f32_32x32x16_f16 v[18:33], v[122:125], v[106:109], v[18:33]
	s_waitcnt lgkmcnt(3)
	v_mfma_f32_32x32x16_f16 v[2:17], v[126:129], v[106:109], v[2:17]
	ds_read_b128 v[106:109], v130 offset:30720
	ds_read_b128 v[122:125], v130 offset:19456
	s_waitcnt vmcnt(9) lgkmcnt(4)
	v_mfma_f32_32x32x16_f16 v[50:65], v[66:69], v[90:93], v[50:65]
	ds_read_b128 v[66:69], v130 offset:23552
	s_waitcnt lgkmcnt(4)
	v_mfma_f32_32x32x16_f16 v[34:49], v[102:105], v[90:93], v[34:49]
	ds_read_b128 v[102:105], v130 offset:27648
	s_waitcnt lgkmcnt(4)
	v_mfma_f32_32x32x16_f16 v[18:33], v[118:121], v[90:93], v[18:33]
	s_waitcnt lgkmcnt(3)
	v_mfma_f32_32x32x16_f16 v[2:17], v[106:109], v[90:93], v[2:17]
	ds_read_b128 v[118:121], v130 offset:31744
	s_waitcnt vmcnt(8) lgkmcnt(3)
	v_mfma_f32_32x32x16_f16 v[50:65], v[122:125], v[86:89], v[50:65]
	s_waitcnt lgkmcnt(0)
	s_barrier
	ds_read_b128 v[90:93], v130
	ds_read_b128 v[106:109], v130 offset:4096
	v_mfma_f32_32x32x16_f16 v[34:49], v[66:69], v[86:89], v[34:49]
	ds_read_b128 v[66:69], v130 offset:8192
	v_mfma_f32_32x32x16_f16 v[18:33], v[102:105], v[86:89], v[18:33]
	v_mfma_f32_32x32x16_f16 v[2:17], v[118:121], v[86:89], v[2:17]
	ds_read_b128 v[102:105], v130 offset:12288
	ds_read_b128 v[86:89], v130 offset:1024
	s_waitcnt vmcnt(7) lgkmcnt(4)
	v_mfma_f32_32x32x16_f16 v[50:65], v[90:93], v[94:97], v[50:65]
	ds_read_b128 v[90:93], v130 offset:5120
	s_waitcnt lgkmcnt(4)
	v_mfma_f32_32x32x16_f16 v[34:49], v[106:109], v[94:97], v[34:49]
	ds_read_b128 v[106:109], v130 offset:9216
	s_waitcnt lgkmcnt(4)
	v_mfma_f32_32x32x16_f16 v[18:33], v[66:69], v[94:97], v[18:33]
	s_waitcnt lgkmcnt(3)
	v_mfma_f32_32x32x16_f16 v[2:17], v[102:105], v[94:97], v[2:17]
	ds_read_b128 v[66:69], v130 offset:13312
	ds_read_b128 v[94:97], v130 offset:2048
	s_waitcnt vmcnt(6) lgkmcnt(4)
	v_mfma_f32_32x32x16_f16 v[50:65], v[86:89], v[110:113], v[50:65]
	ds_read_b128 v[86:89], v130 offset:6144
	s_waitcnt lgkmcnt(4)
	v_mfma_f32_32x32x16_f16 v[34:49], v[90:93], v[110:113], v[34:49]
	ds_read_b128 v[90:93], v130 offset:10240
	s_waitcnt lgkmcnt(4)
	v_mfma_f32_32x32x16_f16 v[18:33], v[106:109], v[110:113], v[18:33]
	s_waitcnt lgkmcnt(3)
	v_mfma_f32_32x32x16_f16 v[2:17], v[66:69], v[110:113], v[2:17]
	ds_read_b128 v[102:105], v130 offset:14336
	ds_read_b128 v[66:69], v130 offset:3072
	s_waitcnt vmcnt(5) lgkmcnt(4)
	v_mfma_f32_32x32x16_f16 v[50:65], v[94:97], v[114:117], v[50:65]
	ds_read_b128 v[94:97], v130 offset:7168
	s_waitcnt lgkmcnt(4)
	v_mfma_f32_32x32x16_f16 v[34:49], v[86:89], v[114:117], v[34:49]
	ds_read_b128 v[86:89], v130 offset:11264
	s_waitcnt lgkmcnt(4)
	v_mfma_f32_32x32x16_f16 v[18:33], v[90:93], v[114:117], v[18:33]
	s_waitcnt lgkmcnt(3)
	v_mfma_f32_32x32x16_f16 v[2:17], v[102:105], v[114:117], v[2:17]
	ds_read_b128 v[90:93], v130 offset:15360
	s_waitcnt vmcnt(4) lgkmcnt(3)
	v_mfma_f32_32x32x16_f16 v[50:65], v[66:69], v[70:73], v[50:65]
	s_waitcnt lgkmcnt(0)
	s_barrier
	ds_read_b128 v[66:69], v130 offset:16384
	ds_read_b128 v[102:105], v130 offset:20480
	v_mfma_f32_32x32x16_f16 v[34:49], v[94:97], v[70:73], v[34:49]
	ds_read_b128 v[94:97], v130 offset:24576
	v_mfma_f32_32x32x16_f16 v[18:33], v[86:89], v[70:73], v[18:33]
	v_mfma_f32_32x32x16_f16 v[2:17], v[90:93], v[70:73], v[2:17]
	ds_read_b128 v[86:89], v130 offset:28672
	ds_read_b128 v[70:73], v130 offset:17408
	s_waitcnt vmcnt(3) lgkmcnt(4)
	v_mfma_f32_32x32x16_f16 v[50:65], v[66:69], v[74:77], v[50:65]
	ds_read_b128 v[66:69], v130 offset:21504
	s_waitcnt lgkmcnt(4)
	v_mfma_f32_32x32x16_f16 v[34:49], v[102:105], v[74:77], v[34:49]
	ds_read_b128 v[90:93], v130 offset:25600
	s_waitcnt lgkmcnt(4)
	v_mfma_f32_32x32x16_f16 v[18:33], v[94:97], v[74:77], v[18:33]
	s_waitcnt lgkmcnt(3)
	v_mfma_f32_32x32x16_f16 v[2:17], v[86:89], v[74:77], v[2:17]
	ds_read_b128 v[94:97], v130 offset:29696
	ds_read_b128 v[74:77], v130 offset:18432
	s_waitcnt vmcnt(2) lgkmcnt(4)
	v_mfma_f32_32x32x16_f16 v[50:65], v[70:73], v[78:81], v[50:65]
	ds_read_b128 v[70:73], v130 offset:22528
	s_waitcnt lgkmcnt(4)
	v_mfma_f32_32x32x16_f16 v[34:49], v[66:69], v[78:81], v[34:49]
	ds_read_b128 v[66:69], v130 offset:26624
	s_waitcnt lgkmcnt(4)
	v_mfma_f32_32x32x16_f16 v[18:33], v[90:93], v[78:81], v[18:33]
	s_waitcnt lgkmcnt(3)
	v_mfma_f32_32x32x16_f16 v[2:17], v[94:97], v[78:81], v[2:17]
	ds_read_b128 v[86:89], v130 offset:30720
	ds_read_b128 v[78:81], v130 offset:19456
	s_waitcnt vmcnt(1) lgkmcnt(4)
	v_mfma_f32_32x32x16_f16 v[50:65], v[74:77], v[82:85], v[50:65]
	ds_read_b128 v[74:77], v130 offset:23552
	s_waitcnt lgkmcnt(4)
	v_mfma_f32_32x32x16_f16 v[34:49], v[70:73], v[82:85], v[34:49]
	ds_read_b128 v[70:73], v130 offset:27648
	s_waitcnt lgkmcnt(4)
	v_mfma_f32_32x32x16_f16 v[18:33], v[66:69], v[82:85], v[18:33]
	s_waitcnt lgkmcnt(3)
	v_mfma_f32_32x32x16_f16 v[2:17], v[86:89], v[82:85], v[2:17]
	ds_read_b128 v[66:69], v130 offset:31744
	s_waitcnt vmcnt(0) lgkmcnt(3)
	v_mfma_f32_32x32x16_f16 v[50:65], v[78:81], v[98:101], v[50:65]
	s_waitcnt lgkmcnt(2)
	v_mfma_f32_32x32x16_f16 v[34:49], v[74:77], v[98:101], v[34:49]
	s_waitcnt lgkmcnt(1)
	v_mfma_f32_32x32x16_f16 v[18:33], v[70:73], v[98:101], v[18:33]
	s_waitcnt lgkmcnt(0)
	v_mfma_f32_32x32x16_f16 v[2:17], v[66:69], v[98:101], v[2:17]
	v_lshrrev_b32_e32 v66, 1, v0
	v_and_b32_e32 v66, 16, v66
	ds_read_b128 v[68:71], v66 offset:32768
	ds_read_b128 v[72:75], v66 offset:32800
	ds_read_b128 v[76:79], v66 offset:32832
	s_mov_b32 s2, 0x4038aa3b
	s_waitcnt lgkmcnt(1)
	v_pk_fma_f32 v[72:73], v[54:55], s[2:3], v[72:73] op_sel_hi:[1,0,1]
	v_pk_fma_f32 v[68:69], v[50:51], s[2:3], v[68:69] op_sel_hi:[1,0,1]
	v_pk_fma_f32 v[70:71], v[52:53], s[2:3], v[70:71] op_sel_hi:[1,0,1]
	ds_read_b128 v[50:53], v66 offset:32864
	v_exp_f32_e32 v54, v68
	v_exp_f32_e32 v55, v69
	v_pk_fma_f32 v[74:75], v[56:57], s[2:3], v[74:75] op_sel_hi:[1,0,1]
	v_exp_f32_e32 v56, v70
	v_exp_f32_e32 v57, v71
	v_pk_add_f32 v[54:55], v[54:55], 1.0 op_sel_hi:[1,0]
	s_waitcnt lgkmcnt(1)
	v_pk_fma_f32 v[58:59], v[58:59], s[2:3], v[76:77] op_sel_hi:[1,0,1]
	s_waitcnt lgkmcnt(0)
	v_pk_fma_f32 v[76:77], v[62:63], s[2:3], v[50:51] op_sel_hi:[1,0,1]
	v_pk_fma_f32 v[64:65], v[64:65], s[2:3], v[52:53] op_sel_hi:[1,0,1]
	ds_read_b128 v[50:53], v66 offset:33280
	v_rcp_f32_e32 v62, v54
	v_rcp_f32_e32 v63, v55
	v_pk_add_f32 v[54:55], v[56:57], 1.0 op_sel_hi:[1,0]
	v_pk_fma_f32 v[60:61], v[60:61], s[2:3], v[78:79] op_sel_hi:[1,0,1]
	v_rcp_f32_e32 v68, v54
	v_rcp_f32_e32 v69, v55
	v_pk_fma_f32 v[70:71], v[62:63], 2.0, 1.0 op_sel_hi:[1,0,0] neg_lo:[1,0,0] neg_hi:[1,0,0]
	ds_read_b128 v[54:57], v66 offset:33312
	s_waitcnt lgkmcnt(1)
	v_pk_fma_f32 v[70:71], v[50:51], v[70:71], 0 op_sel_hi:[1,1,0]
	v_pk_fma_f32 v[78:79], v[68:69], 2.0, 1.0 op_sel_hi:[1,0,0] neg_lo:[1,0,0] neg_hi:[1,0,0]
	v_pk_fma_f32 v[62:63], v[62:63], v[62:63], v[62:63] neg_lo:[1,0,0] neg_hi:[1,0,0]
	v_pk_mul_f32 v[50:51], v[50:51], 4.0 op_sel_hi:[1,0]
	v_pk_fma_f32 v[70:71], v[52:53], v[78:79], v[70:71]
	v_pk_mul_f32 v[50:51], v[50:51], v[62:63]
	v_pk_mul_f32 v[52:53], v[52:53], 4.0 op_sel_hi:[1,0]
	v_exp_f32_e32 v62, v72
	v_exp_f32_e32 v63, v73
	v_pk_fma_f32 v[68:69], v[68:69], v[68:69], v[68:69] neg_lo:[1,0,0] neg_hi:[1,0,0]
	v_exp_f32_e32 v60, v60
	v_pk_mul_f32 v[52:53], v[52:53], v[68:69]
	v_exp_f32_e32 v68, v74
	v_exp_f32_e32 v69, v75
	v_pk_add_f32 v[62:63], v[62:63], 1.0 op_sel_hi:[1,0]
	v_cvt_pk_f16_f32 v53, v52, v53
	v_rcp_f32_e32 v62, v62
	v_rcp_f32_e32 v63, v63
	v_pk_add_f32 v[68:69], v[68:69], 1.0 op_sel_hi:[1,0]
	v_cvt_pk_f16_f32 v52, v50, v51
	v_rcp_f32_e32 v68, v68
	v_rcp_f32_e32 v69, v69
	v_pk_fma_f32 v[50:51], v[62:63], 2.0, 1.0 op_sel_hi:[1,0,0] neg_lo:[1,0,0] neg_hi:[1,0,0]
	v_pk_fma_f32 v[62:63], v[62:63], v[62:63], v[62:63] neg_lo:[1,0,0] neg_hi:[1,0,0]
	s_waitcnt lgkmcnt(0)
	v_pk_fma_f32 v[50:51], v[54:55], v[50:51], v[70:71]
	v_pk_fma_f32 v[70:71], v[68:69], 2.0, 1.0 op_sel_hi:[1,0,0] neg_lo:[1,0,0] neg_hi:[1,0,0]
	v_pk_mul_f32 v[54:55], v[54:55], 4.0 op_sel_hi:[1,0]
	v_pk_fma_f32 v[50:51], v[56:57], v[70:71], v[50:51]
	v_pk_mul_f32 v[62:63], v[54:55], v[62:63]
	v_pk_mul_f32 v[54:55], v[56:57], 4.0 op_sel_hi:[1,0]
	v_pk_fma_f32 v[56:57], v[68:69], v[68:69], v[68:69] neg_lo:[1,0,0] neg_hi:[1,0,0]
	v_exp_f32_e32 v61, v61
	v_pk_mul_f32 v[54:55], v[54:55], v[56:57]
	v_pk_add_f32 v[60:61], v[60:61], 1.0 op_sel_hi:[1,0]
	v_cvt_pk_f16_f32 v55, v54, v55
	v_cvt_pk_f16_f32 v54, v62, v63
	v_exp_f32_e32 v62, v58
	v_exp_f32_e32 v63, v59
	ds_read_b128 v[56:59], v66 offset:33344
	v_rcp_f32_e32 v70, v60
	v_rcp_f32_e32 v71, v61
	v_pk_add_f32 v[62:63], v[62:63], 1.0 op_sel_hi:[1,0]
	v_permlane32_swap_b32_e32 v52, v54
	v_rcp_f32_e32 v68, v62
	v_rcp_f32_e32 v69, v63
	ds_read_b128 v[60:63], v66 offset:33376
	v_permlane32_swap_b32_e32 v53, v55
	v_pk_fma_f32 v[72:73], v[68:69], 2.0, 1.0 op_sel_hi:[1,0,0] neg_lo:[1,0,0] neg_hi:[1,0,0]
	s_waitcnt lgkmcnt(1)
	v_pk_fma_f32 v[50:51], v[56:57], v[72:73], v[50:51]
	v_pk_fma_f32 v[72:73], v[70:71], 2.0, 1.0 op_sel_hi:[1,0,0] neg_lo:[1,0,0] neg_hi:[1,0,0]
	v_pk_mul_f32 v[56:57], v[56:57], 4.0 op_sel_hi:[1,0]
	v_pk_fma_f32 v[72:73], v[58:59], v[72:73], v[50:51]
	v_pk_fma_f32 v[50:51], v[68:69], v[68:69], v[68:69] neg_lo:[1,0,0] neg_hi:[1,0,0]
	s_nop 0
	v_pk_mul_f32 v[50:51], v[56:57], v[50:51]
	v_pk_mul_f32 v[56:57], v[58:59], 4.0 op_sel_hi:[1,0]
	v_pk_fma_f32 v[58:59], v[70:71], v[70:71], v[70:71] neg_lo:[1,0,0] neg_hi:[1,0,0]
	s_nop 0
	v_pk_mul_f32 v[56:57], v[56:57], v[58:59]
	v_exp_f32_e32 v58, v76
	v_exp_f32_e32 v59, v77
	v_cvt_pk_f16_f32 v57, v56, v57
	v_cvt_pk_f16_f32 v56, v50, v51
	v_exp_f32_e32 v50, v64
	v_exp_f32_e32 v51, v65
	v_pk_add_f32 v[58:59], v[58:59], 1.0 op_sel_hi:[1,0]
	v_pk_add_f32 v[50:51], v[50:51], 1.0 op_sel_hi:[1,0]
	v_rcp_f32_e32 v64, v58
	v_rcp_f32_e32 v65, v59
	v_rcp_f32_e32 v68, v50
	v_rcp_f32_e32 v69, v51
	s_waitcnt lgkmcnt(0)
	v_pk_mul_f32 v[50:51], v[60:61], 4.0 op_sel_hi:[1,0]
	v_pk_fma_f32 v[58:59], v[64:65], v[64:65], v[64:65] neg_lo:[1,0,0] neg_hi:[1,0,0]
	v_pk_fma_f32 v[64:65], v[64:65], 2.0, 1.0 op_sel_hi:[1,0,0] neg_lo:[1,0,0] neg_hi:[1,0,0]
	v_pk_mul_f32 v[70:71], v[50:51], v[58:59]
	v_pk_mul_f32 v[50:51], v[62:63], 4.0 op_sel_hi:[1,0]
	v_pk_fma_f32 v[58:59], v[68:69], v[68:69], v[68:69] neg_lo:[1,0,0] neg_hi:[1,0,0]
	v_pk_fma_f32 v[68:69], v[68:69], 2.0, 1.0 op_sel_hi:[1,0,0] neg_lo:[1,0,0] neg_hi:[1,0,0]
	v_pk_mul_f32 v[50:51], v[50:51], v[58:59]
	v_cvt_pk_f16_f32 v58, v70, v71
	v_cvt_pk_f16_f32 v59, v50, v51
	v_lshl_add_u64 v[50:51], s[4:5], 0, v[130:131]
	s_lshl_b32 s4, s10, 3
	s_add_i32 s4, s4, s3
	s_ashr_i32 s5, s4, 31
	s_lshl_b64 s[12:13], s[4:5], 10
	v_lshl_add_u64 v[70:71], v[50:51], 0, s[12:13]
	s_or_b32 s12, s4, 1
	s_ashr_i32 s13, s12, 31
	s_lshl_b64 s[12:13], s[12:13], 10
	global_store_dwordx4 v[70:71], v[52:55], off sc1
	v_permlane32_swap_b32_e32 v56, v58
	v_permlane32_swap_b32_e32 v57, v59
	v_lshl_add_u64 v[52:53], v[50:51], 0, s[12:13]
	global_store_dwordx4 v[52:53], v[56:59], off sc1
	ds_read_b128 v[52:55], v66 offset:32896
	s_or_b32 s12, s4, 2
	v_pk_fma_f32 v[56:57], v[60:61], v[64:65], v[72:73]
	s_ashr_i32 s13, s12, 31
	v_pk_fma_f32 v[64:65], v[62:63], v[68:69], v[56:57]
	ds_read_b128 v[56:59], v66 offset:33408
	ds_read_b128 v[60:63], v66 offset:32928
	s_waitcnt lgkmcnt(2)
	v_pk_fma_f32 v[34:35], v[34:35], s[2:3], v[52:53] op_sel_hi:[1,0,1]
	v_pk_fma_f32 v[36:37], v[36:37], s[2:3], v[54:55] op_sel_hi:[1,0,1]
	v_exp_f32_e32 v34, v34
	v_exp_f32_e32 v35, v35
	v_exp_f32_e32 v36, v36
	v_exp_f32_e32 v37, v37
	s_waitcnt lgkmcnt(0)
	v_pk_fma_f32 v[38:39], v[38:39], s[2:3], v[60:61] op_sel_hi:[1,0,1]
	v_pk_fma_f32 v[40:41], v[40:41], s[2:3], v[62:63] op_sel_hi:[1,0,1]
	v_exp_f32_e32 v38, v38
	v_exp_f32_e32 v39, v39
	v_pk_add_f32 v[34:35], v[34:35], 1.0 op_sel_hi:[1,0]
	v_exp_f32_e32 v40, v40
	v_exp_f32_e32 v41, v41
	v_rcp_f32_e32 v52, v34
	v_rcp_f32_e32 v53, v35
	v_pk_add_f32 v[34:35], v[36:37], 1.0 op_sel_hi:[1,0]
	v_pk_add_f32 v[38:39], v[38:39], 1.0 op_sel_hi:[1,0]
	v_rcp_f32_e32 v54, v34
	v_rcp_f32_e32 v55, v35
	ds_read_b128 v[34:37], v66 offset:33440
	v_rcp_f32_e32 v38, v38
	v_rcp_f32_e32 v39, v39
	v_pk_add_f32 v[40:41], v[40:41], 1.0 op_sel_hi:[1,0]
	v_pk_fma_f32 v[68:69], v[52:53], 2.0, 1.0 op_sel_hi:[1,0,0] neg_lo:[1,0,0] neg_hi:[1,0,0]
	v_rcp_f32_e32 v40, v40
	v_rcp_f32_e32 v41, v41
	v_pk_fma_f32 v[64:65], v[56:57], v[68:69], v[64:65]
	v_pk_mul_f32 v[56:57], v[56:57], 4.0 op_sel_hi:[1,0]
	v_pk_fma_f32 v[52:53], v[52:53], v[52:53], v[52:53] neg_lo:[1,0,0] neg_hi:[1,0,0]
	v_pk_fma_f32 v[68:69], v[54:55], 2.0, 1.0 op_sel_hi:[1,0,0] neg_lo:[1,0,0] neg_hi:[1,0,0]
	v_pk_mul_f32 v[56:57], v[56:57], v[52:53]
	v_pk_mul_f32 v[52:53], v[58:59], 4.0 op_sel_hi:[1,0]
	v_pk_fma_f32 v[54:55], v[54:55], v[54:55], v[54:55] neg_lo:[1,0,0] neg_hi:[1,0,0]
	v_pk_fma_f32 v[64:65], v[58:59], v[68:69], v[64:65]
	v_pk_mul_f32 v[52:53], v[52:53], v[54:55]
	v_pk_fma_f32 v[54:55], v[38:39], 2.0, 1.0 op_sel_hi:[1,0,0] neg_lo:[1,0,0] neg_hi:[1,0,0]
	v_cvt_pk_f16_f32 v53, v52, v53
	v_cvt_pk_f16_f32 v52, v56, v57
	s_waitcnt lgkmcnt(0)
	v_pk_fma_f32 v[54:55], v[34:35], v[54:55], v[64:65]
	v_pk_fma_f32 v[56:57], v[40:41], 2.0, 1.0 op_sel_hi:[1,0,0] neg_lo:[1,0,0] neg_hi:[1,0,0]
	v_pk_mul_f32 v[34:35], v[34:35], 4.0 op_sel_hi:[1,0]
	v_pk_fma_f32 v[38:39], v[38:39], v[38:39], v[38:39] neg_lo:[1,0,0] neg_hi:[1,0,0]
	v_pk_fma_f32 v[60:61], v[36:37], v[56:57], v[54:55]
	v_pk_mul_f32 v[38:39], v[34:35], v[38:39]
	v_pk_mul_f32 v[54:55], v[36:37], 4.0 op_sel_hi:[1,0]
	ds_read_b128 v[34:37], v66 offset:32960
	v_pk_fma_f32 v[40:41], v[40:41], v[40:41], v[40:41] neg_lo:[1,0,0] neg_hi:[1,0,0]
	ds_read_b128 v[56:59], v66 offset:33472
	v_pk_mul_f32 v[40:41], v[54:55], v[40:41]
	v_cvt_pk_f16_f32 v54, v38, v39
	v_cvt_pk_f16_f32 v55, v40, v41
	ds_read_b128 v[38:41], v66 offset:32992
	s_waitcnt lgkmcnt(2)
	v_pk_fma_f32 v[34:35], v[42:43], s[2:3], v[34:35] op_sel_hi:[1,0,1]
	v_pk_fma_f32 v[36:37], v[44:45], s[2:3], v[36:37] op_sel_hi:[1,0,1]
	v_exp_f32_e32 v34, v34
	v_exp_f32_e32 v35, v35
	v_exp_f32_e32 v36, v36
	v_exp_f32_e32 v37, v37
	s_waitcnt lgkmcnt(0)
	v_pk_fma_f32 v[38:39], v[46:47], s[2:3], v[38:39] op_sel_hi:[1,0,1]
	v_pk_fma_f32 v[40:41], v[48:49], s[2:3], v[40:41] op_sel_hi:[1,0,1]
	v_exp_f32_e32 v38, v38
	v_exp_f32_e32 v39, v39
	v_pk_add_f32 v[34:35], v[34:35], 1.0 op_sel_hi:[1,0]
	v_exp_f32_e32 v40, v40
	v_exp_f32_e32 v41, v41
	v_rcp_f32_e32 v42, v34
	v_rcp_f32_e32 v43, v35
	v_pk_add_f32 v[34:35], v[36:37], 1.0 op_sel_hi:[1,0]
	v_pk_add_f32 v[38:39], v[38:39], 1.0 op_sel_hi:[1,0]
	v_rcp_f32_e32 v44, v34
	v_rcp_f32_e32 v45, v35
	ds_read_b128 v[34:37], v66 offset:33504
	v_rcp_f32_e32 v46, v38
	v_rcp_f32_e32 v47, v39
	v_pk_add_f32 v[38:39], v[40:41], 1.0 op_sel_hi:[1,0]
	v_pk_fma_f32 v[62:63], v[42:43], 2.0, 1.0 op_sel_hi:[1,0,0] neg_lo:[1,0,0] neg_hi:[1,0,0]
	v_rcp_f32_e32 v40, v38
	v_rcp_f32_e32 v41, v39
	v_pk_fma_f32 v[60:61], v[56:57], v[62:63], v[60:61]
	v_pk_fma_f32 v[42:43], v[42:43], v[42:43], v[42:43] neg_lo:[1,0,0] neg_hi:[1,0,0]
	v_pk_mul_f32 v[56:57], v[56:57], 4.0 op_sel_hi:[1,0]
	v_pk_fma_f32 v[62:63], v[44:45], 2.0, 1.0 op_sel_hi:[1,0,0] neg_lo:[1,0,0] neg_hi:[1,0,0]
	v_pk_mul_f32 v[42:43], v[56:57], v[42:43]
	v_pk_mul_f32 v[56:57], v[58:59], 4.0 op_sel_hi:[1,0]
	v_pk_fma_f32 v[44:45], v[44:45], v[44:45], v[44:45] neg_lo:[1,0,0] neg_hi:[1,0,0]
	v_cvt_pk_f16_f32 v38, v42, v43
	v_pk_mul_f32 v[44:45], v[56:57], v[44:45]
	v_pk_fma_f32 v[42:43], v[46:47], 2.0, 1.0 op_sel_hi:[1,0,0] neg_lo:[1,0,0] neg_hi:[1,0,0]
	s_waitcnt lgkmcnt(0)
	v_pk_mul_f32 v[48:49], v[34:35], 4.0 op_sel_hi:[1,0]
	v_pk_fma_f32 v[46:47], v[46:47], v[46:47], v[46:47] neg_lo:[1,0,0] neg_hi:[1,0,0]
	v_cvt_pk_f16_f32 v39, v44, v45
	v_pk_fma_f32 v[44:45], v[40:41], 2.0, 1.0 op_sel_hi:[1,0,0] neg_lo:[1,0,0] neg_hi:[1,0,0]
	v_pk_mul_f32 v[46:47], v[48:49], v[46:47]
	v_pk_mul_f32 v[48:49], v[36:37], 4.0 op_sel_hi:[1,0]
	v_pk_fma_f32 v[40:41], v[40:41], v[40:41], v[40:41] neg_lo:[1,0,0] neg_hi:[1,0,0]
	s_lshl_b64 s[12:13], s[12:13], 10
	v_pk_mul_f32 v[40:41], v[48:49], v[40:41]
	v_permlane32_swap_b32_e32 v52, v54
	v_cvt_pk_f16_f32 v41, v40, v41
	v_cvt_pk_f16_f32 v40, v46, v47
	v_lshl_add_u64 v[46:47], v[50:51], 0, s[12:13]
	s_or_b32 s12, s4, 3
	s_ashr_i32 s13, s12, 31
	v_permlane32_swap_b32_e32 v53, v55
	s_lshl_b64 s[12:13], s[12:13], 10
	global_store_dwordx4 v[46:47], v[52:55], off sc1
	v_permlane32_swap_b32_e32 v38, v40
	v_permlane32_swap_b32_e32 v39, v41
	v_lshl_add_u64 v[46:47], v[50:51], 0, s[12:13]
	global_store_dwordx4 v[46:47], v[38:41], off sc1
	ds_read_b128 v[38:41], v66 offset:33024
	v_pk_fma_f32 v[60:61], v[58:59], v[62:63], v[60:61]
	s_or_b32 s12, s4, 4
	v_pk_fma_f32 v[34:35], v[34:35], v[42:43], v[60:61]
	s_ashr_i32 s13, s12, 31
	v_pk_fma_f32 v[46:47], v[36:37], v[44:45], v[34:35]
	ds_read_b128 v[34:37], v66 offset:33056
	ds_read_b128 v[42:45], v66 offset:33536
	s_waitcnt lgkmcnt(2)
	v_pk_fma_f32 v[18:19], v[18:19], s[2:3], v[38:39] op_sel_hi:[1,0,1]
	v_pk_fma_f32 v[20:21], v[20:21], s[2:3], v[40:41] op_sel_hi:[1,0,1]
	v_exp_f32_e32 v18, v18
	v_exp_f32_e32 v19, v19
	v_exp_f32_e32 v20, v20
	v_exp_f32_e32 v21, v21
	s_waitcnt lgkmcnt(1)
	v_pk_fma_f32 v[22:23], v[22:23], s[2:3], v[34:35] op_sel_hi:[1,0,1]
	v_pk_fma_f32 v[24:25], v[24:25], s[2:3], v[36:37] op_sel_hi:[1,0,1]
	v_exp_f32_e32 v22, v22
	v_exp_f32_e32 v23, v23
	v_exp_f32_e32 v24, v24
	v_exp_f32_e32 v25, v25
	v_pk_add_f32 v[18:19], v[18:19], 1.0 op_sel_hi:[1,0]
	v_pk_add_f32 v[22:23], v[22:23], 1.0 op_sel_hi:[1,0]
	v_rcp_f32_e32 v38, v18
	v_rcp_f32_e32 v39, v19
	v_pk_add_f32 v[18:19], v[20:21], 1.0 op_sel_hi:[1,0]
	v_rcp_f32_e32 v22, v22
	v_rcp_f32_e32 v40, v18
	v_rcp_f32_e32 v41, v19
	ds_read_b128 v[18:21], v66 offset:33568
	v_rcp_f32_e32 v23, v23
	v_pk_add_f32 v[24:25], v[24:25], 1.0 op_sel_hi:[1,0]
	v_pk_fma_f32 v[48:49], v[38:39], 2.0, 1.0 op_sel_hi:[1,0,0] neg_lo:[1,0,0] neg_hi:[1,0,0]
	v_rcp_f32_e32 v24, v24
	v_rcp_f32_e32 v25, v25
	s_waitcnt lgkmcnt(1)
	v_pk_fma_f32 v[46:47], v[42:43], v[48:49], v[46:47]
	v_pk_fma_f32 v[48:49], v[40:41], 2.0, 1.0 op_sel_hi:[1,0,0] neg_lo:[1,0,0] neg_hi:[1,0,0]
	v_pk_mul_f32 v[42:43], v[42:43], 4.0 op_sel_hi:[1,0]
	v_pk_fma_f32 v[38:39], v[38:39], v[38:39], v[38:39] neg_lo:[1,0,0] neg_hi:[1,0,0]
	v_pk_fma_f32 v[46:47], v[44:45], v[48:49], v[46:47]
	v_pk_mul_f32 v[42:43], v[42:43], v[38:39]
	v_pk_mul_f32 v[38:39], v[44:45], 4.0 op_sel_hi:[1,0]
	v_pk_fma_f32 v[40:41], v[40:41], v[40:41], v[40:41] neg_lo:[1,0,0] neg_hi:[1,0,0]
	v_pk_fma_f32 v[34:35], v[22:23], 2.0, 1.0 op_sel_hi:[1,0,0] neg_lo:[1,0,0] neg_hi:[1,0,0]
	v_pk_mul_f32 v[38:39], v[38:39], v[40:41]
	s_waitcnt lgkmcnt(0)
	v_pk_fma_f32 v[34:35], v[18:19], v[34:35], v[46:47]
	v_pk_fma_f32 v[36:37], v[24:25], 2.0, 1.0 op_sel_hi:[1,0,0] neg_lo:[1,0,0] neg_hi:[1,0,0]
	v_pk_mul_f32 v[18:19], v[18:19], 4.0 op_sel_hi:[1,0]
	v_pk_fma_f32 v[22:23], v[22:23], v[22:23], v[22:23] neg_lo:[1,0,0] neg_hi:[1,0,0]
	v_cvt_pk_f16_f32 v39, v38, v39
	v_cvt_pk_f16_f32 v38, v42, v43
	v_pk_fma_f32 v[42:43], v[20:21], v[36:37], v[34:35]
	v_pk_mul_f32 v[22:23], v[18:19], v[22:23]
	v_pk_mul_f32 v[18:19], v[20:21], 4.0 op_sel_hi:[1,0]
	v_pk_fma_f32 v[20:21], v[24:25], v[24:25], v[24:25] neg_lo:[1,0,0] neg_hi:[1,0,0]
	v_cvt_pk_f16_f32 v40, v22, v23
	v_pk_mul_f32 v[24:25], v[18:19], v[20:21]
	ds_read_b128 v[18:21], v66 offset:33088
	v_cvt_pk_f16_f32 v41, v24, v25
	ds_read_b128 v[22:25], v66 offset:33600
	ds_read_b128 v[34:37], v66 offset:33120
	s_lshl_b64 s[12:13], s[12:13], 10
	v_permlane32_swap_b32_e32 v38, v40
	s_waitcnt lgkmcnt(2)
	v_pk_fma_f32 v[18:19], v[26:27], s[2:3], v[18:19] op_sel_hi:[1,0,1]
	v_pk_fma_f32 v[20:21], v[28:29], s[2:3], v[20:21] op_sel_hi:[1,0,1]
	v_exp_f32_e32 v18, v18
	v_exp_f32_e32 v19, v19
	v_exp_f32_e32 v20, v20
	v_exp_f32_e32 v21, v21
	v_permlane32_swap_b32_e32 v39, v41
	v_pk_add_f32 v[18:19], v[18:19], 1.0 op_sel_hi:[1,0]
	s_nop 0
	v_rcp_f32_e32 v26, v18
	v_rcp_f32_e32 v27, v19
	v_pk_add_f32 v[18:19], v[20:21], 1.0 op_sel_hi:[1,0]
	v_pk_fma_f32 v[44:45], v[26:27], 2.0, 1.0 op_sel_hi:[1,0,0] neg_lo:[1,0,0] neg_hi:[1,0,0]
	v_rcp_f32_e32 v28, v18
	v_rcp_f32_e32 v29, v19
	s_waitcnt lgkmcnt(1)
	v_pk_fma_f32 v[42:43], v[22:23], v[44:45], v[42:43]
	v_pk_mul_f32 v[22:23], v[22:23], 4.0 op_sel_hi:[1,0]
	v_pk_fma_f32 v[26:27], v[26:27], v[26:27], v[26:27] neg_lo:[1,0,0] neg_hi:[1,0,0]
	v_pk_fma_f32 v[44:45], v[28:29], 2.0, 1.0 op_sel_hi:[1,0,0] neg_lo:[1,0,0] neg_hi:[1,0,0]
	v_pk_mul_f32 v[26:27], v[22:23], v[26:27]
	v_pk_fma_f32 v[42:43], v[24:25], v[44:45], v[42:43]
	v_pk_mul_f32 v[22:23], v[24:25], 4.0 op_sel_hi:[1,0]
	v_pk_fma_f32 v[24:25], v[28:29], v[28:29], v[28:29] neg_lo:[1,0,0] neg_hi:[1,0,0]
	s_waitcnt lgkmcnt(0)
	v_pk_fma_f32 v[28:29], v[32:33], s[2:3], v[36:37] op_sel_hi:[1,0,1]
	v_pk_mul_f32 v[22:23], v[22:23], v[24:25]
	v_pk_fma_f32 v[24:25], v[30:31], s[2:3], v[34:35] op_sel_hi:[1,0,1]
	v_exp_f32_e32 v28, v28
	v_exp_f32_e32 v24, v24
	v_exp_f32_e32 v25, v25
	v_exp_f32_e32 v29, v29
	ds_read_b128 v[18:21], v66 offset:33632
	v_cvt_pk_f16_f32 v23, v22, v23
	v_pk_add_f32 v[24:25], v[24:25], 1.0 op_sel_hi:[1,0]
	v_pk_add_f32 v[28:29], v[28:29], 1.0 op_sel_hi:[1,0]
	v_rcp_f32_e32 v24, v24
	v_rcp_f32_e32 v25, v25
	v_rcp_f32_e32 v28, v28
	v_rcp_f32_e32 v29, v29
	v_cvt_pk_f16_f32 v22, v26, v27
	v_pk_fma_f32 v[26:27], v[24:25], 2.0, 1.0 op_sel_hi:[1,0,0] neg_lo:[1,0,0] neg_hi:[1,0,0]
	s_waitcnt lgkmcnt(0)
	v_pk_mul_f32 v[32:33], v[18:19], 4.0 op_sel_hi:[1,0]
	v_pk_fma_f32 v[24:25], v[24:25], v[24:25], v[24:25] neg_lo:[1,0,0] neg_hi:[1,0,0]
	v_pk_fma_f32 v[30:31], v[28:29], 2.0, 1.0 op_sel_hi:[1,0,0] neg_lo:[1,0,0] neg_hi:[1,0,0]
	v_pk_mul_f32 v[32:33], v[32:33], v[24:25]
	v_pk_mul_f32 v[24:25], v[20:21], 4.0 op_sel_hi:[1,0]
	v_pk_fma_f32 v[28:29], v[28:29], v[28:29], v[28:29] neg_lo:[1,0,0] neg_hi:[1,0,0]
	v_pk_fma_f32 v[18:19], v[18:19], v[26:27], v[42:43]
	v_pk_mul_f32 v[24:25], v[24:25], v[28:29]
	v_lshl_add_u64 v[28:29], v[50:51], 0, s[12:13]
	s_or_b32 s12, s4, 5
	s_ashr_i32 s13, s12, 31
	v_cvt_pk_f16_f32 v25, v24, v25
	v_cvt_pk_f16_f32 v24, v32, v33
	s_lshl_b64 s[12:13], s[12:13], 10
	global_store_dwordx4 v[28:29], v[38:41], off sc1
	v_permlane32_swap_b32_e32 v22, v24
	v_permlane32_swap_b32_e32 v23, v25
	v_lshl_add_u64 v[28:29], v[50:51], 0, s[12:13]
	global_store_dwordx4 v[28:29], v[22:25], off sc1
	ds_read_b128 v[22:25], v66 offset:33152
	v_pk_fma_f32 v[30:31], v[20:21], v[30:31], v[18:19]
	ds_read_b128 v[18:21], v66 offset:33184
	ds_read_b128 v[26:29], v66 offset:33664
	s_waitcnt lgkmcnt(2)
	v_pk_fma_f32 v[2:3], v[2:3], s[2:3], v[22:23] op_sel_hi:[1,0,1]
	s_nop 0
	v_exp_f32_e32 v2, v2
	v_exp_f32_e32 v3, v3
	v_pk_fma_f32 v[4:5], v[4:5], s[2:3], v[24:25] op_sel_hi:[1,0,1]
	s_waitcnt lgkmcnt(1)
	v_pk_fma_f32 v[6:7], v[6:7], s[2:3], v[18:19] op_sel_hi:[1,0,1]
	v_exp_f32_e32 v4, v4
	v_exp_f32_e32 v5, v5
	v_exp_f32_e32 v6, v6
	v_exp_f32_e32 v7, v7
	v_pk_fma_f32 v[8:9], v[8:9], s[2:3], v[20:21] op_sel_hi:[1,0,1]
	v_pk_add_f32 v[2:3], v[2:3], 1.0 op_sel_hi:[1,0]
	v_exp_f32_e32 v8, v8
	v_exp_f32_e32 v9, v9
	v_rcp_f32_e32 v22, v2
	v_rcp_f32_e32 v23, v3
	v_pk_add_f32 v[2:3], v[4:5], 1.0 op_sel_hi:[1,0]
	v_pk_add_f32 v[6:7], v[6:7], 1.0 op_sel_hi:[1,0]
	v_rcp_f32_e32 v24, v2
	v_rcp_f32_e32 v25, v3
	ds_read_b128 v[2:5], v66 offset:33696
	v_rcp_f32_e32 v6, v6
	v_rcp_f32_e32 v7, v7
	v_pk_add_f32 v[8:9], v[8:9], 1.0 op_sel_hi:[1,0]
	v_pk_fma_f32 v[32:33], v[22:23], 2.0, 1.0 op_sel_hi:[1,0,0] neg_lo:[1,0,0] neg_hi:[1,0,0]
	v_rcp_f32_e32 v8, v8
	v_rcp_f32_e32 v9, v9
	s_waitcnt lgkmcnt(1)
	v_pk_fma_f32 v[30:31], v[26:27], v[32:33], v[30:31]
	v_pk_fma_f32 v[32:33], v[24:25], 2.0, 1.0 op_sel_hi:[1,0,0] neg_lo:[1,0,0] neg_hi:[1,0,0]
	v_pk_mul_f32 v[26:27], v[26:27], 4.0 op_sel_hi:[1,0]
	v_pk_fma_f32 v[22:23], v[22:23], v[22:23], v[22:23] neg_lo:[1,0,0] neg_hi:[1,0,0]
	v_pk_fma_f32 v[30:31], v[28:29], v[32:33], v[30:31]
	v_pk_mul_f32 v[26:27], v[26:27], v[22:23]
	v_pk_mul_f32 v[22:23], v[28:29], 4.0 op_sel_hi:[1,0]
	v_pk_fma_f32 v[24:25], v[24:25], v[24:25], v[24:25] neg_lo:[1,0,0] neg_hi:[1,0,0]
	v_pk_fma_f32 v[18:19], v[6:7], 2.0, 1.0 op_sel_hi:[1,0,0] neg_lo:[1,0,0] neg_hi:[1,0,0]
	v_pk_mul_f32 v[22:23], v[22:23], v[24:25]
	s_waitcnt lgkmcnt(0)
	v_pk_fma_f32 v[18:19], v[2:3], v[18:19], v[30:31]
	v_pk_fma_f32 v[20:21], v[8:9], 2.0, 1.0 op_sel_hi:[1,0,0] neg_lo:[1,0,0] neg_hi:[1,0,0]
	v_pk_mul_f32 v[2:3], v[2:3], 4.0 op_sel_hi:[1,0]
	v_pk_fma_f32 v[6:7], v[6:7], v[6:7], v[6:7] neg_lo:[1,0,0] neg_hi:[1,0,0]
	v_cvt_pk_f16_f32 v23, v22, v23
	v_cvt_pk_f16_f32 v22, v26, v27
	v_pk_fma_f32 v[26:27], v[4:5], v[20:21], v[18:19]
	v_pk_mul_f32 v[6:7], v[2:3], v[6:7]
	v_pk_mul_f32 v[2:3], v[4:5], 4.0 op_sel_hi:[1,0]
	v_pk_fma_f32 v[4:5], v[8:9], v[8:9], v[8:9] neg_lo:[1,0,0] neg_hi:[1,0,0]
	v_cvt_pk_f16_f32 v24, v6, v7
	v_pk_mul_f32 v[8:9], v[2:3], v[4:5]
	ds_read_b128 v[2:5], v66 offset:33216
	v_cvt_pk_f16_f32 v25, v8, v9
	ds_read_b128 v[6:9], v66 offset:33728
	ds_read_b128 v[18:21], v66 offset:33248
	v_permlane32_swap_b32_e32 v22, v24
	s_waitcnt lgkmcnt(2)
	v_pk_fma_f32 v[2:3], v[10:11], s[2:3], v[2:3] op_sel_hi:[1,0,1]
	v_pk_fma_f32 v[4:5], v[12:13], s[2:3], v[4:5] op_sel_hi:[1,0,1]
	v_exp_f32_e32 v2, v2
	v_exp_f32_e32 v3, v3
	v_exp_f32_e32 v4, v4
	v_exp_f32_e32 v5, v5
	v_permlane32_swap_b32_e32 v23, v25
	v_pk_add_f32 v[2:3], v[2:3], 1.0 op_sel_hi:[1,0]
	s_nop 0
	v_rcp_f32_e32 v10, v2
	v_rcp_f32_e32 v11, v3
	v_pk_add_f32 v[2:3], v[4:5], 1.0 op_sel_hi:[1,0]
	v_pk_fma_f32 v[28:29], v[10:11], 2.0, 1.0 op_sel_hi:[1,0,0] neg_lo:[1,0,0] neg_hi:[1,0,0]
	v_rcp_f32_e32 v12, v2
	v_rcp_f32_e32 v13, v3
	s_waitcnt lgkmcnt(1)
	v_pk_fma_f32 v[26:27], v[6:7], v[28:29], v[26:27]
	v_pk_mul_f32 v[6:7], v[6:7], 4.0 op_sel_hi:[1,0]
	v_pk_fma_f32 v[10:11], v[10:11], v[10:11], v[10:11] neg_lo:[1,0,0] neg_hi:[1,0,0]
	v_pk_fma_f32 v[28:29], v[12:13], 2.0, 1.0 op_sel_hi:[1,0,0] neg_lo:[1,0,0] neg_hi:[1,0,0]
	v_pk_mul_f32 v[10:11], v[6:7], v[10:11]
	v_pk_fma_f32 v[26:27], v[8:9], v[28:29], v[26:27]
	v_pk_mul_f32 v[6:7], v[8:9], 4.0 op_sel_hi:[1,0]
	v_pk_fma_f32 v[8:9], v[12:13], v[12:13], v[12:13] neg_lo:[1,0,0] neg_hi:[1,0,0]
	s_waitcnt lgkmcnt(0)
	v_pk_fma_f32 v[12:13], v[16:17], s[2:3], v[20:21] op_sel_hi:[1,0,1]
	v_pk_mul_f32 v[6:7], v[6:7], v[8:9]
	v_pk_fma_f32 v[8:9], v[14:15], s[2:3], v[18:19] op_sel_hi:[1,0,1]
	v_exp_f32_e32 v12, v12
	v_exp_f32_e32 v8, v8
	v_exp_f32_e32 v9, v9
	v_exp_f32_e32 v13, v13
	ds_read_b128 v[2:5], v66 offset:33760
	v_cvt_pk_f16_f32 v7, v6, v7
	v_pk_add_f32 v[8:9], v[8:9], 1.0 op_sel_hi:[1,0]
	v_pk_add_f32 v[12:13], v[12:13], 1.0 op_sel_hi:[1,0]
	v_rcp_f32_e32 v8, v8
	v_rcp_f32_e32 v9, v9
	v_rcp_f32_e32 v12, v12
	v_rcp_f32_e32 v13, v13
	v_cvt_pk_f16_f32 v6, v10, v11
	v_pk_fma_f32 v[10:11], v[8:9], 2.0, 1.0 op_sel_hi:[1,0,0] neg_lo:[1,0,0] neg_hi:[1,0,0]
	s_waitcnt lgkmcnt(0)
	v_pk_mul_f32 v[16:17], v[2:3], 4.0 op_sel_hi:[1,0]
	v_pk_fma_f32 v[14:15], v[12:13], 2.0, 1.0 op_sel_hi:[1,0,0] neg_lo:[1,0,0] neg_hi:[1,0,0]
	v_pk_fma_f32 v[2:3], v[2:3], v[10:11], v[26:27]
	v_pk_fma_f32 v[8:9], v[8:9], v[8:9], v[8:9] neg_lo:[1,0,0] neg_hi:[1,0,0]
	v_pk_fma_f32 v[2:3], v[4:5], v[14:15], v[2:3]
	v_pk_mul_f32 v[16:17], v[16:17], v[8:9]
	v_add_f32_e32 v2, v2, v3
	v_mbcnt_lo_u32_b32 v3, -1, 0
	v_mbcnt_hi_u32_b32 v3, -1, v3
	v_pk_mul_f32 v[8:9], v[4:5], 4.0 op_sel_hi:[1,0]
	v_and_b32_e32 v5, 64, v3
	v_xor_b32_e32 v4, 32, v3
	v_add_u32_e32 v5, 64, v5
	v_cmp_lt_i32_e32 vcc, v4, v5
	s_or_b32 s2, s4, 6
	s_ashr_i32 s3, s2, 31
	v_cndmask_b32_e32 v3, v3, v4, vcc
	v_lshlrev_b32_e32 v3, 2, v3
	v_pk_fma_f32 v[12:13], v[12:13], v[12:13], v[12:13] neg_lo:[1,0,0] neg_hi:[1,0,0]
	s_lshl_b64 s[2:3], s[2:3], 10
	ds_bpermute_b32 v3, v3, v2
	v_pk_mul_f32 v[8:9], v[8:9], v[12:13]
	v_lshl_add_u64 v[12:13], v[50:51], 0, s[2:3]
	s_or_b32 s2, s4, 7
	s_ashr_i32 s3, s2, 31
	v_cvt_pk_f16_f32 v9, v8, v9
	v_cvt_pk_f16_f32 v8, v16, v17
	s_lshl_b64 s[2:3], s[2:3], 10
	s_nop 0
	v_permlane32_swap_b32_e32 v6, v8
	v_permlane32_swap_b32_e32 v7, v9
	v_lshl_add_u64 v[4:5], v[50:51], 0, s[2:3]
	v_cmp_gt_u32_e32 vcc, 32, v1
	global_store_dwordx4 v[12:13], v[22:25], off sc1
	global_store_dwordx4 v[4:5], v[6:9], off sc1
	s_and_saveexec_b64 s[2:3], vcc
	s_cbranch_execz .LBB2_5
	s_load_dwordx2 s[4:5], s[0:1], 0x30
	s_lshl_b32 s7, s10, 12
	s_lshl_b32 s6, s6, 7
	s_or_b32 s6, s6, s7
	s_lshl_b32 s7, s8, 5
	s_or_b32 s6, s7, s6
	s_waitcnt lgkmcnt(0)
	v_add_f32_e32 v4, v2, v3
	v_or_b32_e32 v2, s6, v1
	v_ashrrev_i32_e32 v3, 31, v2
	v_lshl_add_u64 v[2:3], v[2:3], 2, s[4:5]
	global_store_dword v[2:3], v4, off sc1

.LBB3_3:
	s_lshl_b32 s3, s2, 2
	s_and_b32 s3, s3, 28
	s_bfe_u32 s2, s2, 0x20003
	s_load_dwordx2 s[10:11], s[0:1], 0x8
	s_load_dwordx2 s[12:13], s[0:1], 0x20
	s_or_b32 s2, s3, s2
	s_lshl_b32 s2, s2, 2
	s_or_b32 s6, s5, s2
	s_lshl_b32 s2, s6, 16
	s_waitcnt lgkmcnt(0)
	s_add_u32 s2, s10, s2
	s_addc_u32 s3, s11, 0
	v_lshl_add_u64 v[168:169], s[2:3], 0, v[134:135]
	s_movk_i32 s7, 0x1000
	v_add_co_u32_e32 v6, vcc, s7, v168
	s_movk_i32 s7, 0x2000
	s_nop 0
	v_addc_co_u32_e32 v7, vcc, 0, v169, vcc
	v_add_co_u32_e32 v8, vcc, s7, v168
	global_load_dwordx4 v[90:93], v134, s[2:3] offset:1024
	global_load_dwordx4 v[102:105], v134, s[2:3] offset:2048
	v_addc_co_u32_e32 v9, vcc, 0, v169, vcc
	global_load_dwordx4 v[106:109], v134, s[2:3] offset:3072
	global_load_dwordx4 v[94:97], v[8:9], off offset:-4096
	global_load_dwordx4 v[98:101], v[6:7], off offset:1024
	global_load_dwordx4 v[86:89], v[6:7], off offset:2048
	global_load_dwordx4 v[2:5], v134, s[2:3]
	global_load_dwordx4 v[82:85], v[6:7], off offset:3072
	global_load_dwordx4 v[78:81], v[8:9], off
	global_load_dwordx4 v[74:77], v[8:9], off offset:1024
	global_load_dwordx4 v[70:73], v[8:9], off offset:2048
	global_load_dwordx4 v[66:69], v[8:9], off offset:3072
	s_barrier
	ds_read_b128 v[6:9], v134
	ds_read_b128 v[10:13], v134 offset:4096
	ds_read_b128 v[14:17], v134 offset:8192
	ds_read_b128 v[110:113], v134 offset:12288
	s_load_dwordx2 s[2:3], s[0:1], 0x40
	s_lshl_b32 s7, s6, 6
	v_and_b32_e32 v1, 31, v0
	s_lshl_b32 s9, s4, 3
	v_lshrrev_b32_e32 v18, 2, v0
	s_add_i32 s10, s9, s7
	v_and_b32_e32 v18, 8, v18
	v_mov_b32_e32 v19, v135
	s_ashr_i32 s11, s10, 31
	v_lshl_add_u64 v[18:19], s[12:13], 0, v[18:19]
	s_lshl_b64 s[12:13], s[10:11], 10
	v_lshlrev_b32_e32 v1, 4, v1
	v_or_b32_e32 v20, s12, v1
	s_or_b32 s12, s10, 1
	v_mov_b32_e32 v21, s13
	s_ashr_i32 s13, s12, 31
	s_lshl_b64 s[12:13], s[12:13], 10
	v_or_b32_e32 v22, s12, v1
	s_or_b32 s12, s10, 2
	v_mov_b32_e32 v23, s13
	s_ashr_i32 s13, s12, 31
	v_lshl_add_u64 v[20:21], v[18:19], 0, v[20:21]
	s_lshl_b64 s[12:13], s[12:13], 10
	v_lshl_add_u64 v[22:23], v[18:19], 0, v[22:23]
	global_load_dwordx2 v[166:167], v[20:21], off
	global_load_dwordx2 v[164:165], v[20:21], off offset:512
	global_load_dwordx2 v[162:163], v[22:23], off
	global_load_dwordx2 v[160:161], v[22:23], off offset:512
	v_or_b32_e32 v20, s12, v1
	s_or_b32 s12, s10, 3
	v_mov_b32_e32 v21, s13
	s_ashr_i32 s13, s12, 31
	s_lshl_b64 s[12:13], s[12:13], 10
	v_or_b32_e32 v22, s12, v1
	s_or_b32 s12, s10, 4
	v_mov_b32_e32 v23, s13
	s_ashr_i32 s13, s12, 31
	v_lshl_add_u64 v[20:21], v[18:19], 0, v[20:21]
	s_lshl_b64 s[12:13], s[12:13], 10
	v_lshl_add_u64 v[22:23], v[18:19], 0, v[22:23]
	global_load_dwordx2 v[158:159], v[20:21], off
	global_load_dwordx2 v[156:157], v[20:21], off offset:512
	global_load_dwordx2 v[154:155], v[22:23], off
	global_load_dwordx2 v[152:153], v[22:23], off offset:512
	v_or_b32_e32 v20, s12, v1
	s_or_b32 s12, s10, 5
	v_mov_b32_e32 v21, s13
	s_ashr_i32 s13, s12, 31
	s_lshl_b64 s[12:13], s[12:13], 10
	v_or_b32_e32 v22, s12, v1
	s_or_b32 s12, s10, 6
	v_mov_b32_e32 v23, s13
	s_ashr_i32 s13, s12, 31
	s_or_b32 s10, s10, 7
	v_lshl_add_u64 v[20:21], v[18:19], 0, v[20:21]
	s_lshl_b64 s[12:13], s[12:13], 10
	s_ashr_i32 s11, s10, 31
	v_lshl_add_u64 v[22:23], v[18:19], 0, v[22:23]
	global_load_dwordx2 v[150:151], v[20:21], off
	global_load_dwordx2 v[148:149], v[20:21], off offset:512
	global_load_dwordx2 v[146:147], v[22:23], off
	global_load_dwordx2 v[144:145], v[22:23], off offset:512
	v_or_b32_e32 v20, s12, v1
	v_mov_b32_e32 v21, s13
	s_lshl_b64 s[10:11], s[10:11], 10
	v_lshl_add_u64 v[20:21], v[18:19], 0, v[20:21]
	v_or_b32_e32 v22, s10, v1
	v_mov_b32_e32 v23, s11
	v_lshl_add_u64 v[18:19], v[18:19], 0, v[22:23]
	global_load_dwordx2 v[142:143], v[20:21], off
	global_load_dwordx2 v[140:141], v[20:21], off offset:512
	global_load_dwordx2 v[138:139], v[18:19], off
	global_load_dwordx2 v[136:137], v[18:19], off offset:512
	s_lshl_b32 s7, s4, 7
	ds_read_b128 v[118:121], v134 offset:1024
	s_waitcnt vmcnt(21) lgkmcnt(0)
	v_mfma_f32_32x32x16_f16 v[50:65], v[6:9], v[2:5], 0
	s_movk_i32 s9, 0x4000
	v_add_co_u32_e32 v178, vcc, s9, v168
	ds_read_b128 v[122:125], v134 offset:5120
	s_nop 0
	v_addc_co_u32_e32 v179, vcc, 0, v169, vcc
	global_load_dwordx4 v[114:117], v[178:179], off offset:-4096
	s_movk_i32 s9, 0x3000
	v_add_co_u32_e32 v180, vcc, s9, v168
	v_mfma_f32_32x32x16_f16 v[34:49], v[10:13], v[2:5], 0
	s_nop 0
	v_addc_co_u32_e32 v181, vcc, 0, v169, vcc
	ds_read_b128 v[126:129], v134 offset:9216
	v_mfma_f32_32x32x16_f16 v[18:33], v[14:17], v[2:5], 0
	ds_read_b128 v[130:133], v134 offset:13312
	v_mfma_f32_32x32x16_f16 v[2:17], v[110:113], v[2:5], 0
	ds_read_b128 v[110:113], v134 offset:2048
	v_mfma_f32_32x32x16_f16 v[50:65], v[118:121], v[90:93], v[50:65]
	global_load_dwordx4 v[118:121], v[180:181], off offset:1024
	ds_read_b128 v[170:173], v134 offset:6144
	s_waitcnt lgkmcnt(4)
	v_mfma_f32_32x32x16_f16 v[34:49], v[122:125], v[90:93], v[34:49]
	ds_read_b128 v[174:177], v134 offset:10240
	s_waitcnt lgkmcnt(4)
	v_mfma_f32_32x32x16_f16 v[18:33], v[126:129], v[90:93], v[18:33]
	ds_read_b128 v[126:129], v134 offset:14336
	s_waitcnt lgkmcnt(4)
	v_mfma_f32_32x32x16_f16 v[2:17], v[130:133], v[90:93], v[2:17]
	ds_read_b128 v[90:93], v134 offset:3072
	s_waitcnt lgkmcnt(4)
	v_mfma_f32_32x32x16_f16 v[50:65], v[110:113], v[102:105], v[50:65]
	global_load_dwordx4 v[122:125], v[180:181], off offset:2048
	ds_read_b128 v[110:113], v134 offset:7168
	s_waitcnt lgkmcnt(4)
	v_mfma_f32_32x32x16_f16 v[34:49], v[170:173], v[102:105], v[34:49]
	ds_read_b128 v[130:133], v134 offset:11264
	s_waitcnt lgkmcnt(4)
	v_mfma_f32_32x32x16_f16 v[18:33], v[174:177], v[102:105], v[18:33]
	ds_read_b128 v[170:173], v134 offset:15360
	s_waitcnt lgkmcnt(4)
	v_mfma_f32_32x32x16_f16 v[2:17], v[126:129], v[102:105], v[2:17]
	global_load_dwordx4 v[102:105], v[180:181], off offset:3072
	s_waitcnt lgkmcnt(3)
	v_mfma_f32_32x32x16_f16 v[50:65], v[90:93], v[106:109], v[50:65]
	s_waitcnt lgkmcnt(0)
	s_barrier
	ds_read_b128 v[90:93], v134 offset:16384
	ds_read_b128 v[126:129], v134 offset:20480
	v_mfma_f32_32x32x16_f16 v[34:49], v[110:113], v[106:109], v[34:49]
	ds_read_b128 v[110:113], v134 offset:24576
	v_mfma_f32_32x32x16_f16 v[18:33], v[130:133], v[106:109], v[18:33]
	ds_read_b128 v[130:133], v134 offset:28672
	v_mfma_f32_32x32x16_f16 v[2:17], v[170:173], v[106:109], v[2:17]
	ds_read_b128 v[106:109], v134 offset:17408
	s_waitcnt lgkmcnt(4)
	v_mfma_f32_32x32x16_f16 v[50:65], v[90:93], v[94:97], v[50:65]
	global_load_dwordx4 v[90:93], v[178:179], off
	ds_read_b128 v[170:173], v134 offset:21504
	s_waitcnt lgkmcnt(4)
	v_mfma_f32_32x32x16_f16 v[34:49], v[126:129], v[94:97], v[34:49]
	ds_read_b128 v[126:129], v134 offset:25600
	s_waitcnt lgkmcnt(4)
	v_mfma_f32_32x32x16_f16 v[18:33], v[110:113], v[94:97], v[18:33]
	ds_read_b128 v[110:113], v134 offset:29696
	s_waitcnt lgkmcnt(4)
	v_mfma_f32_32x32x16_f16 v[2:17], v[130:133], v[94:97], v[2:17]
	ds_read_b128 v[130:133], v134 offset:18432
	s_waitcnt lgkmcnt(4)
	v_mfma_f32_32x32x16_f16 v[50:65], v[106:109], v[98:101], v[50:65]
	global_load_dwordx4 v[94:97], v[178:179], off offset:1024
	ds_read_b128 v[106:109], v134 offset:22528
	s_waitcnt lgkmcnt(4)
	v_mfma_f32_32x32x16_f16 v[34:49], v[170:173], v[98:101], v[34:49]
	ds_read_b128 v[170:173], v134 offset:26624
	s_waitcnt lgkmcnt(4)
	v_mfma_f32_32x32x16_f16 v[18:33], v[126:129], v[98:101], v[18:33]
	ds_read_b128 v[126:129], v134 offset:30720
	s_waitcnt lgkmcnt(4)
	v_mfma_f32_32x32x16_f16 v[2:17], v[110:113], v[98:101], v[2:17]
	ds_read_b128 v[110:113], v134 offset:19456
	s_waitcnt lgkmcnt(4)
	v_mfma_f32_32x32x16_f16 v[50:65], v[130:133], v[86:89], v[50:65]
	global_load_dwordx4 v[98:101], v[178:179], off offset:2048
	ds_read_b128 v[130:133], v134 offset:23552
	s_waitcnt lgkmcnt(4)
	v_mfma_f32_32x32x16_f16 v[34:49], v[106:109], v[86:89], v[34:49]
	ds_read_b128 v[106:109], v134 offset:27648
	s_waitcnt lgkmcnt(4)
	v_mfma_f32_32x32x16_f16 v[18:33], v[170:173], v[86:89], v[18:33]
	ds_read_b128 v[170:173], v134 offset:31744
	s_waitcnt lgkmcnt(4)
	v_mfma_f32_32x32x16_f16 v[2:17], v[126:129], v[86:89], v[2:17]
	global_load_dwordx4 v[86:89], v[178:179], off offset:3072
	s_waitcnt vmcnt(28) lgkmcnt(3)
	v_mfma_f32_32x32x16_f16 v[50:65], v[110:113], v[82:85], v[50:65]
	s_waitcnt lgkmcnt(0)
	s_barrier
	ds_read_b128 v[110:113], v134
	ds_read_b128 v[126:129], v134 offset:4096
	v_mfma_f32_32x32x16_f16 v[34:49], v[130:133], v[82:85], v[34:49]
	ds_read_b128 v[130:133], v134 offset:8192
	v_mfma_f32_32x32x16_f16 v[18:33], v[106:109], v[82:85], v[18:33]
	ds_read_b128 v[106:109], v134 offset:12288
	v_mfma_f32_32x32x16_f16 v[2:17], v[170:173], v[82:85], v[2:17]
	ds_read_b128 v[82:85], v134 offset:1024
	s_waitcnt vmcnt(27) lgkmcnt(4)
	v_mfma_f32_32x32x16_f16 v[50:65], v[110:113], v[78:81], v[50:65]
	s_movk_i32 s9, 0x6000
	v_add_co_u32_e32 v178, vcc, s9, v168
	ds_read_b128 v[170:173], v134 offset:5120
	s_nop 0
	v_addc_co_u32_e32 v179, vcc, 0, v169, vcc
	global_load_dwordx4 v[110:113], v[178:179], off offset:-4096
	s_movk_i32 s9, 0x5000
	v_add_co_u32_e32 v180, vcc, s9, v168
	s_waitcnt lgkmcnt(4)
	v_mfma_f32_32x32x16_f16 v[34:49], v[126:129], v[78:81], v[34:49]
	v_addc_co_u32_e32 v181, vcc, 0, v169, vcc
	ds_read_b128 v[174:177], v134 offset:9216
	s_waitcnt lgkmcnt(4)
	v_mfma_f32_32x32x16_f16 v[18:33], v[130:133], v[78:81], v[18:33]
	ds_read_b128 v[130:133], v134 offset:13312
	s_waitcnt lgkmcnt(4)
	v_mfma_f32_32x32x16_f16 v[2:17], v[106:109], v[78:81], v[2:17]
	ds_read_b128 v[78:81], v134 offset:2048
	s_waitcnt vmcnt(27) lgkmcnt(4)
	v_mfma_f32_32x32x16_f16 v[50:65], v[82:85], v[74:77], v[50:65]
	global_load_dwordx4 v[126:129], v[180:181], off offset:1024
	ds_read_b128 v[82:85], v134 offset:6144
	s_waitcnt lgkmcnt(4)
	v_mfma_f32_32x32x16_f16 v[34:49], v[170:173], v[74:77], v[34:49]
	ds_read_b128 v[106:109], v134 offset:10240
	s_waitcnt lgkmcnt(4)
	v_mfma_f32_32x32x16_f16 v[18:33], v[174:177], v[74:77], v[18:33]
	ds_read_b128 v[170:173], v134 offset:14336
	s_waitcnt lgkmcnt(4)
	v_mfma_f32_32x32x16_f16 v[2:17], v[130:133], v[74:77], v[2:17]
	ds_read_b128 v[74:77], v134 offset:3072
	s_waitcnt vmcnt(27) lgkmcnt(4)
	v_mfma_f32_32x32x16_f16 v[50:65], v[78:81], v[70:73], v[50:65]
	global_load_dwordx4 v[130:133], v[180:181], off offset:2048
	ds_read_b128 v[78:81], v134 offset:7168
	s_waitcnt lgkmcnt(4)
	v_mfma_f32_32x32x16_f16 v[34:49], v[82:85], v[70:73], v[34:49]
	ds_read_b128 v[82:85], v134 offset:11264
	s_waitcnt lgkmcnt(4)
	v_mfma_f32_32x32x16_f16 v[18:33], v[106:109], v[70:73], v[18:33]
	ds_read_b128 v[174:177], v134 offset:15360
	s_waitcnt lgkmcnt(4)
	v_mfma_f32_32x32x16_f16 v[2:17], v[170:173], v[70:73], v[2:17]
	global_load_dwordx4 v[106:109], v[180:181], off offset:3072
	s_waitcnt vmcnt(28) lgkmcnt(3)
	v_mfma_f32_32x32x16_f16 v[50:65], v[74:77], v[66:69], v[50:65]
	s_waitcnt lgkmcnt(0)
	s_barrier
	ds_read_b128 v[70:73], v134 offset:16384
	ds_read_b128 v[170:173], v134 offset:20480
	v_mfma_f32_32x32x16_f16 v[34:49], v[78:81], v[66:69], v[34:49]
	ds_read_b128 v[78:81], v134 offset:24576
	v_mfma_f32_32x32x16_f16 v[18:33], v[82:85], v[66:69], v[18:33]
	ds_read_b128 v[82:85], v134 offset:28672
	v_mfma_f32_32x32x16_f16 v[2:17], v[174:177], v[66:69], v[2:17]
	ds_read_b128 v[66:69], v134 offset:17408
	s_waitcnt vmcnt(11) lgkmcnt(4)
	v_mfma_f32_32x32x16_f16 v[50:65], v[70:73], v[114:117], v[50:65]
	global_load_dwordx4 v[74:77], v[178:179], off
	ds_read_b128 v[70:73], v134 offset:21504
	s_waitcnt lgkmcnt(4)
	v_mfma_f32_32x32x16_f16 v[34:49], v[170:173], v[114:117], v[34:49]
	ds_read_b128 v[170:173], v134 offset:25600
	s_waitcnt lgkmcnt(4)
	v_mfma_f32_32x32x16_f16 v[18:33], v[78:81], v[114:117], v[18:33]
	ds_read_b128 v[174:177], v134 offset:29696
	s_waitcnt lgkmcnt(4)
	v_mfma_f32_32x32x16_f16 v[2:17], v[82:85], v[114:117], v[2:17]
	ds_read_b128 v[82:85], v134 offset:18432
	s_waitcnt vmcnt(11) lgkmcnt(4)
	v_mfma_f32_32x32x16_f16 v[50:65], v[66:69], v[118:121], v[50:65]
	global_load_dwordx4 v[78:81], v[178:179], off offset:1024
	ds_read_b128 v[66:69], v134 offset:22528
	s_waitcnt lgkmcnt(4)
	v_mfma_f32_32x32x16_f16 v[34:49], v[70:73], v[118:121], v[34:49]
	ds_read_b128 v[70:73], v134 offset:26624
	s_waitcnt lgkmcnt(4)
	v_mfma_f32_32x32x16_f16 v[18:33], v[170:173], v[118:121], v[18:33]
	ds_read_b128 v[114:117], v134 offset:30720
	s_waitcnt lgkmcnt(4)
	v_mfma_f32_32x32x16_f16 v[2:17], v[174:177], v[118:121], v[2:17]
	ds_read_b128 v[118:121], v134 offset:19456
	s_waitcnt vmcnt(11) lgkmcnt(4)
	v_mfma_f32_32x32x16_f16 v[50:65], v[82:85], v[122:125], v[50:65]
	global_load_dwordx4 v[82:85], v[178:179], off offset:2048
	ds_read_b128 v[170:173], v134 offset:23552
	s_waitcnt lgkmcnt(4)
	v_mfma_f32_32x32x16_f16 v[34:49], v[66:69], v[122:125], v[34:49]
	ds_read_b128 v[174:177], v134 offset:27648
	s_waitcnt lgkmcnt(4)
	v_mfma_f32_32x32x16_f16 v[18:33], v[70:73], v[122:125], v[18:33]
	ds_read_b128 v[70:73], v134 offset:31744
	s_waitcnt lgkmcnt(4)
	v_mfma_f32_32x32x16_f16 v[2:17], v[114:117], v[122:125], v[2:17]
	global_load_dwordx4 v[66:69], v[178:179], off offset:3072
	s_waitcnt vmcnt(12) lgkmcnt(3)
	v_mfma_f32_32x32x16_f16 v[50:65], v[118:121], v[102:105], v[50:65]
	s_waitcnt lgkmcnt(0)
	s_barrier
	ds_read_b128 v[114:117], v134
	ds_read_b128 v[118:121], v134 offset:4096
	v_mfma_f32_32x32x16_f16 v[34:49], v[170:173], v[102:105], v[34:49]
	ds_read_b128 v[122:125], v134 offset:8192
	v_mfma_f32_32x32x16_f16 v[18:33], v[174:177], v[102:105], v[18:33]
	ds_read_b128 v[170:173], v134 offset:12288
	v_mfma_f32_32x32x16_f16 v[2:17], v[70:73], v[102:105], v[2:17]
	ds_read_b128 v[70:73], v134 offset:1024
	s_waitcnt vmcnt(11) lgkmcnt(4)
	v_mfma_f32_32x32x16_f16 v[50:65], v[114:117], v[90:93], v[50:65]
	s_mov_b32 s9, 0x8000
	v_add_co_u32_e32 v178, vcc, s9, v168
	ds_read_b128 v[102:105], v134 offset:5120
	s_nop 0
	v_addc_co_u32_e32 v179, vcc, 0, v169, vcc
	global_load_dwordx4 v[114:117], v[178:179], off offset:-4096
	s_movk_i32 s9, 0x7000
	v_add_co_u32_e32 v180, vcc, s9, v168
	s_waitcnt lgkmcnt(4)
	v_mfma_f32_32x32x16_f16 v[34:49], v[118:121], v[90:93], v[34:49]
	v_addc_co_u32_e32 v181, vcc, 0, v169, vcc
	ds_read_b128 v[174:177], v134 offset:9216
	s_waitcnt lgkmcnt(4)
	v_mfma_f32_32x32x16_f16 v[18:33], v[122:125], v[90:93], v[18:33]
	ds_read_b128 v[122:125], v134 offset:13312
	s_waitcnt lgkmcnt(4)
	v_mfma_f32_32x32x16_f16 v[2:17], v[170:173], v[90:93], v[2:17]
	ds_read_b128 v[90:93], v134 offset:2048
	s_waitcnt vmcnt(11) lgkmcnt(4)
	v_mfma_f32_32x32x16_f16 v[50:65], v[70:73], v[94:97], v[50:65]
	global_load_dwordx4 v[118:121], v[180:181], off offset:1024
	ds_read_b128 v[70:73], v134 offset:6144
	s_waitcnt lgkmcnt(4)
	v_mfma_f32_32x32x16_f16 v[34:49], v[102:105], v[94:97], v[34:49]
	ds_read_b128 v[102:105], v134 offset:10240
	s_waitcnt lgkmcnt(4)
	v_mfma_f32_32x32x16_f16 v[18:33], v[174:177], v[94:97], v[18:33]
	ds_read_b128 v[170:173], v134 offset:14336
	s_waitcnt lgkmcnt(4)
	v_mfma_f32_32x32x16_f16 v[2:17], v[122:125], v[94:97], v[2:17]
	ds_read_b128 v[94:97], v134 offset:3072
	s_waitcnt vmcnt(11) lgkmcnt(4)
	v_mfma_f32_32x32x16_f16 v[50:65], v[90:93], v[98:101], v[50:65]
	global_load_dwordx4 v[122:125], v[180:181], off offset:2048
	ds_read_b128 v[90:93], v134 offset:7168
	s_waitcnt lgkmcnt(4)
	v_mfma_f32_32x32x16_f16 v[34:49], v[70:73], v[98:101], v[34:49]
	ds_read_b128 v[70:73], v134 offset:11264
	s_waitcnt lgkmcnt(4)
	v_mfma_f32_32x32x16_f16 v[18:33], v[102:105], v[98:101], v[18:33]
	ds_read_b128 v[174:177], v134 offset:15360
	s_waitcnt lgkmcnt(4)
	v_mfma_f32_32x32x16_f16 v[2:17], v[170:173], v[98:101], v[2:17]
	global_load_dwordx4 v[102:105], v[180:181], off offset:3072
	s_waitcnt vmcnt(12) lgkmcnt(3)
	v_mfma_f32_32x32x16_f16 v[50:65], v[94:97], v[86:89], v[50:65]
	s_waitcnt lgkmcnt(0)
	s_barrier
	ds_read_b128 v[94:97], v134 offset:16384
	ds_read_b128 v[98:101], v134 offset:20480
	v_mfma_f32_32x32x16_f16 v[34:49], v[90:93], v[86:89], v[34:49]
	ds_read_b128 v[90:93], v134 offset:24576
	v_mfma_f32_32x32x16_f16 v[18:33], v[70:73], v[86:89], v[18:33]
	ds_read_b128 v[70:73], v134 offset:28672
	v_mfma_f32_32x32x16_f16 v[2:17], v[174:177], v[86:89], v[2:17]
	ds_read_b128 v[170:173], v134 offset:17408
	s_waitcnt vmcnt(11) lgkmcnt(4)
	v_mfma_f32_32x32x16_f16 v[50:65], v[94:97], v[110:113], v[50:65]
	global_load_dwordx4 v[86:89], v[178:179], off
	ds_read_b128 v[94:97], v134 offset:21504
	s_waitcnt lgkmcnt(4)
	v_mfma_f32_32x32x16_f16 v[34:49], v[98:101], v[110:113], v[34:49]
	ds_read_b128 v[98:101], v134 offset:25600
	s_waitcnt lgkmcnt(4)
	v_mfma_f32_32x32x16_f16 v[18:33], v[90:93], v[110:113], v[18:33]
	ds_read_b128 v[174:177], v134 offset:29696
	s_waitcnt lgkmcnt(4)
	v_mfma_f32_32x32x16_f16 v[2:17], v[70:73], v[110:113], v[2:17]
	ds_read_b128 v[70:73], v134 offset:18432
	s_waitcnt vmcnt(11) lgkmcnt(4)
	v_mfma_f32_32x32x16_f16 v[50:65], v[170:173], v[126:129], v[50:65]
	global_load_dwordx4 v[90:93], v[178:179], off offset:1024
	ds_read_b128 v[110:113], v134 offset:22528
	s_waitcnt lgkmcnt(4)
	v_mfma_f32_32x32x16_f16 v[34:49], v[94:97], v[126:129], v[34:49]
	ds_read_b128 v[170:173], v134 offset:26624
	s_waitcnt lgkmcnt(4)
	v_mfma_f32_32x32x16_f16 v[18:33], v[98:101], v[126:129], v[18:33]
	ds_read_b128 v[98:101], v134 offset:30720
	s_waitcnt lgkmcnt(4)
	v_mfma_f32_32x32x16_f16 v[2:17], v[174:177], v[126:129], v[2:17]
	ds_read_b128 v[126:129], v134 offset:19456
	s_waitcnt vmcnt(11) lgkmcnt(4)
	v_mfma_f32_32x32x16_f16 v[50:65], v[70:73], v[130:133], v[50:65]
	global_load_dwordx4 v[94:97], v[178:179], off offset:2048
	ds_read_b128 v[174:177], v134 offset:23552
	s_waitcnt lgkmcnt(4)
	v_mfma_f32_32x32x16_f16 v[34:49], v[110:113], v[130:133], v[34:49]
	ds_read_b128 v[110:113], v134 offset:27648
	s_waitcnt lgkmcnt(4)
	v_mfma_f32_32x32x16_f16 v[18:33], v[170:173], v[130:133], v[18:33]
	ds_read_b128 v[170:173], v134 offset:31744
	s_waitcnt lgkmcnt(4)
	v_mfma_f32_32x32x16_f16 v[2:17], v[98:101], v[130:133], v[2:17]
	global_load_dwordx4 v[70:73], v[178:179], off offset:3072
	s_waitcnt vmcnt(12) lgkmcnt(3)
	v_mfma_f32_32x32x16_f16 v[50:65], v[126:129], v[106:109], v[50:65]
	s_waitcnt lgkmcnt(0)
	s_barrier
	ds_read_b128 v[98:101], v134
	ds_read_b128 v[126:129], v134 offset:4096
	v_mfma_f32_32x32x16_f16 v[34:49], v[174:177], v[106:109], v[34:49]
	ds_read_b128 v[130:133], v134 offset:8192
	v_mfma_f32_32x32x16_f16 v[18:33], v[110:113], v[106:109], v[18:33]
	ds_read_b128 v[174:177], v134 offset:12288
	v_mfma_f32_32x32x16_f16 v[2:17], v[170:173], v[106:109], v[2:17]
	ds_read_b128 v[106:109], v134 offset:1024
	s_waitcnt vmcnt(11) lgkmcnt(4)
	v_mfma_f32_32x32x16_f16 v[50:65], v[98:101], v[74:77], v[50:65]
	s_mov_b32 s9, 0xa000
	v_add_co_u32_e32 v178, vcc, s9, v168
	ds_read_b128 v[98:101], v134 offset:5120
	s_nop 0
	v_addc_co_u32_e32 v179, vcc, 0, v169, vcc
	global_load_dwordx4 v[110:113], v[178:179], off offset:-4096
	s_mov_b32 s9, 0x9000
	v_add_co_u32_e32 v180, vcc, s9, v168
	s_waitcnt lgkmcnt(4)
	v_mfma_f32_32x32x16_f16 v[34:49], v[126:129], v[74:77], v[34:49]
	v_addc_co_u32_e32 v181, vcc, 0, v169, vcc
	ds_read_b128 v[170:173], v134 offset:9216
	s_waitcnt lgkmcnt(4)
	v_mfma_f32_32x32x16_f16 v[18:33], v[130:133], v[74:77], v[18:33]
	ds_read_b128 v[130:133], v134 offset:13312
	s_waitcnt lgkmcnt(4)
	v_mfma_f32_32x32x16_f16 v[2:17], v[174:177], v[74:77], v[2:17]
	ds_read_b128 v[74:77], v134 offset:2048
	s_waitcnt vmcnt(11) lgkmcnt(4)
	v_mfma_f32_32x32x16_f16 v[50:65], v[106:109], v[78:81], v[50:65]
	global_load_dwordx4 v[126:129], v[180:181], off offset:1024
	ds_read_b128 v[106:109], v134 offset:6144
	s_waitcnt lgkmcnt(4)
	v_mfma_f32_32x32x16_f16 v[34:49], v[98:101], v[78:81], v[34:49]
	ds_read_b128 v[98:101], v134 offset:10240
	s_waitcnt lgkmcnt(4)
	v_mfma_f32_32x32x16_f16 v[18:33], v[170:173], v[78:81], v[18:33]
	ds_read_b128 v[170:173], v134 offset:14336
	s_waitcnt lgkmcnt(4)
	v_mfma_f32_32x32x16_f16 v[2:17], v[130:133], v[78:81], v[2:17]
	ds_read_b128 v[78:81], v134 offset:3072
	s_waitcnt vmcnt(11) lgkmcnt(4)
	v_mfma_f32_32x32x16_f16 v[50:65], v[74:77], v[82:85], v[50:65]
	global_load_dwordx4 v[130:133], v[180:181], off offset:2048
	ds_read_b128 v[74:77], v134 offset:7168
	s_waitcnt lgkmcnt(4)
	v_mfma_f32_32x32x16_f16 v[34:49], v[106:109], v[82:85], v[34:49]
	ds_read_b128 v[174:177], v134 offset:11264
	s_waitcnt lgkmcnt(4)
	v_mfma_f32_32x32x16_f16 v[18:33], v[98:101], v[82:85], v[18:33]
	ds_read_b128 v[98:101], v134 offset:15360
	s_waitcnt lgkmcnt(4)
	v_mfma_f32_32x32x16_f16 v[2:17], v[170:173], v[82:85], v[2:17]
	global_load_dwordx4 v[106:109], v[180:181], off offset:3072
	s_waitcnt vmcnt(12) lgkmcnt(3)
	v_mfma_f32_32x32x16_f16 v[50:65], v[78:81], v[66:69], v[50:65]
	s_waitcnt lgkmcnt(0)
	s_barrier
	ds_read_b128 v[78:81], v134 offset:16384
	ds_read_b128 v[82:85], v134 offset:20480
	v_mfma_f32_32x32x16_f16 v[34:49], v[74:77], v[66:69], v[34:49]
	ds_read_b128 v[74:77], v134 offset:24576
	v_mfma_f32_32x32x16_f16 v[18:33], v[174:177], v[66:69], v[18:33]
	ds_read_b128 v[170:173], v134 offset:28672
	v_mfma_f32_32x32x16_f16 v[2:17], v[98:101], v[66:69], v[2:17]
	ds_read_b128 v[66:69], v134 offset:17408
	s_waitcnt vmcnt(11) lgkmcnt(4)
	v_mfma_f32_32x32x16_f16 v[50:65], v[78:81], v[114:117], v[50:65]
	global_load_dwordx4 v[78:81], v[178:179], off
	ds_read_b128 v[98:101], v134 offset:21504
	s_waitcnt lgkmcnt(4)
	v_mfma_f32_32x32x16_f16 v[34:49], v[82:85], v[114:117], v[34:49]
	ds_read_b128 v[174:177], v134 offset:25600
	s_waitcnt lgkmcnt(4)
	v_mfma_f32_32x32x16_f16 v[18:33], v[74:77], v[114:117], v[18:33]
	ds_read_b128 v[74:77], v134 offset:29696
	s_waitcnt lgkmcnt(4)
	v_mfma_f32_32x32x16_f16 v[2:17], v[170:173], v[114:117], v[2:17]
	ds_read_b128 v[114:117], v134 offset:18432
	s_waitcnt vmcnt(11) lgkmcnt(4)
	v_mfma_f32_32x32x16_f16 v[50:65], v[66:69], v[118:121], v[50:65]
	global_load_dwordx4 v[82:85], v[178:179], off offset:1024
	ds_read_b128 v[66:69], v134 offset:22528
	s_waitcnt lgkmcnt(4)
	v_mfma_f32_32x32x16_f16 v[34:49], v[98:101], v[118:121], v[34:49]
	ds_read_b128 v[170:173], v134 offset:26624
	s_waitcnt lgkmcnt(4)
	v_mfma_f32_32x32x16_f16 v[18:33], v[174:177], v[118:121], v[18:33]
	ds_read_b128 v[174:177], v134 offset:30720
	s_waitcnt lgkmcnt(4)
	v_mfma_f32_32x32x16_f16 v[2:17], v[74:77], v[118:121], v[2:17]
	ds_read_b128 v[118:121], v134 offset:19456
	s_waitcnt vmcnt(11) lgkmcnt(4)
	v_mfma_f32_32x32x16_f16 v[50:65], v[114:117], v[122:125], v[50:65]
	global_load_dwordx4 v[98:101], v[178:179], off offset:2048
	ds_read_b128 v[114:117], v134 offset:23552
	s_waitcnt lgkmcnt(4)
	v_mfma_f32_32x32x16_f16 v[34:49], v[66:69], v[122:125], v[34:49]
	ds_read_b128 v[66:69], v134 offset:27648
	s_waitcnt lgkmcnt(4)
	v_mfma_f32_32x32x16_f16 v[18:33], v[170:173], v[122:125], v[18:33]
	ds_read_b128 v[170:173], v134 offset:31744
	s_waitcnt lgkmcnt(4)
	v_mfma_f32_32x32x16_f16 v[2:17], v[174:177], v[122:125], v[2:17]
	global_load_dwordx4 v[74:77], v[178:179], off offset:3072
	s_waitcnt vmcnt(12) lgkmcnt(3)
	v_mfma_f32_32x32x16_f16 v[50:65], v[118:121], v[102:105], v[50:65]
	s_waitcnt lgkmcnt(0)
	s_barrier
	ds_read_b128 v[118:121], v134
	ds_read_b128 v[122:125], v134 offset:4096
	v_mfma_f32_32x32x16_f16 v[34:49], v[114:117], v[102:105], v[34:49]
	ds_read_b128 v[174:177], v134 offset:8192
	v_mfma_f32_32x32x16_f16 v[18:33], v[66:69], v[102:105], v[18:33]
	ds_read_b128 v[66:69], v134 offset:12288
	v_mfma_f32_32x32x16_f16 v[2:17], v[170:173], v[102:105], v[2:17]
	ds_read_b128 v[102:105], v134 offset:1024
	s_waitcnt vmcnt(11) lgkmcnt(4)
	v_mfma_f32_32x32x16_f16 v[50:65], v[118:121], v[86:89], v[50:65]
	s_mov_b32 s9, 0xc000
	v_add_co_u32_e32 v178, vcc, s9, v168
	s_waitcnt lgkmcnt(3)
	v_mfma_f32_32x32x16_f16 v[34:49], v[122:125], v[86:89], v[34:49]
	v_addc_co_u32_e32 v179, vcc, 0, v169, vcc
	global_load_dwordx4 v[114:117], v[178:179], off offset:-4096
	ds_read_b128 v[122:125], v134 offset:5120
	s_mov_b32 s9, 0xb000
	v_add_co_u32_e32 v180, vcc, s9, v168
	s_nop 1
	v_addc_co_u32_e32 v181, vcc, 0, v169, vcc
	ds_read_b128 v[170:173], v134 offset:9216
	s_waitcnt lgkmcnt(4)
	v_mfma_f32_32x32x16_f16 v[18:33], v[174:177], v[86:89], v[18:33]
	ds_read_b128 v[174:177], v134 offset:13312
	s_waitcnt lgkmcnt(4)
	v_mfma_f32_32x32x16_f16 v[2:17], v[66:69], v[86:89], v[2:17]
	ds_read_b128 v[66:69], v134 offset:2048
	s_waitcnt vmcnt(11) lgkmcnt(4)
	v_mfma_f32_32x32x16_f16 v[50:65], v[102:105], v[90:93], v[50:65]
	global_load_dwordx4 v[118:121], v[180:181], off offset:1024
	ds_read_b128 v[86:89], v134 offset:6144
	s_waitcnt lgkmcnt(4)
	v_mfma_f32_32x32x16_f16 v[34:49], v[122:125], v[90:93], v[34:49]
	ds_read_b128 v[102:105], v134 offset:10240
	s_waitcnt lgkmcnt(4)
	v_mfma_f32_32x32x16_f16 v[18:33], v[170:173], v[90:93], v[18:33]
	ds_read_b128 v[170:173], v134 offset:14336
	s_waitcnt lgkmcnt(4)
	v_mfma_f32_32x32x16_f16 v[2:17], v[174:177], v[90:93], v[2:17]
	ds_read_b128 v[90:93], v134 offset:3072
	s_waitcnt vmcnt(11) lgkmcnt(4)
	v_mfma_f32_32x32x16_f16 v[50:65], v[66:69], v[94:97], v[50:65]
	global_load_dwordx4 v[122:125], v[180:181], off offset:2048
	ds_read_b128 v[66:69], v134 offset:7168
	s_waitcnt lgkmcnt(4)
	v_mfma_f32_32x32x16_f16 v[34:49], v[86:89], v[94:97], v[34:49]
	ds_read_b128 v[86:89], v134 offset:11264
	s_waitcnt lgkmcnt(4)
	v_mfma_f32_32x32x16_f16 v[18:33], v[102:105], v[94:97], v[18:33]
	ds_read_b128 v[102:105], v134 offset:15360
	s_waitcnt lgkmcnt(4)
	v_mfma_f32_32x32x16_f16 v[2:17], v[170:173], v[94:97], v[2:17]
	global_load_dwordx4 v[94:97], v[180:181], off offset:3072
	s_waitcnt vmcnt(12) lgkmcnt(3)
	v_mfma_f32_32x32x16_f16 v[50:65], v[90:93], v[70:73], v[50:65]
	s_waitcnt lgkmcnt(0)
	s_barrier
	ds_read_b128 v[90:93], v134 offset:16384
	ds_read_b128 v[170:173], v134 offset:20480
	v_mfma_f32_32x32x16_f16 v[34:49], v[66:69], v[70:73], v[34:49]
	ds_read_b128 v[66:69], v134 offset:24576
	v_mfma_f32_32x32x16_f16 v[18:33], v[86:89], v[70:73], v[18:33]
	ds_read_b128 v[86:89], v134 offset:28672
	v_mfma_f32_32x32x16_f16 v[2:17], v[102:105], v[70:73], v[2:17]
	ds_read_b128 v[70:73], v134 offset:17408
	s_waitcnt vmcnt(11) lgkmcnt(4)
	v_mfma_f32_32x32x16_f16 v[50:65], v[90:93], v[110:113], v[50:65]
	global_load_dwordx4 v[102:105], v[178:179], off
	ds_read_b128 v[90:93], v134 offset:21504
	s_waitcnt lgkmcnt(4)
	v_mfma_f32_32x32x16_f16 v[34:49], v[170:173], v[110:113], v[34:49]
	ds_read_b128 v[170:173], v134 offset:25600
	s_waitcnt lgkmcnt(4)
	v_mfma_f32_32x32x16_f16 v[18:33], v[66:69], v[110:113], v[18:33]
	ds_read_b128 v[66:69], v134 offset:29696
	s_waitcnt lgkmcnt(4)
	v_mfma_f32_32x32x16_f16 v[2:17], v[86:89], v[110:113], v[2:17]
	ds_read_b128 v[110:113], v134 offset:18432
	s_waitcnt vmcnt(11) lgkmcnt(4)
	v_mfma_f32_32x32x16_f16 v[50:65], v[70:73], v[126:129], v[50:65]
	global_load_dwordx4 v[86:89], v[178:179], off offset:1024
	ds_read_b128 v[174:177], v134 offset:22528
	s_waitcnt lgkmcnt(4)
	v_mfma_f32_32x32x16_f16 v[34:49], v[90:93], v[126:129], v[34:49]
	ds_read_b128 v[90:93], v134 offset:26624
	s_waitcnt lgkmcnt(4)
	v_mfma_f32_32x32x16_f16 v[18:33], v[170:173], v[126:129], v[18:33]
	ds_read_b128 v[170:173], v134 offset:30720
	s_waitcnt lgkmcnt(4)
	v_mfma_f32_32x32x16_f16 v[2:17], v[66:69], v[126:129], v[2:17]
	ds_read_b128 v[126:129], v134 offset:19456
	s_waitcnt vmcnt(11) lgkmcnt(4)
	v_mfma_f32_32x32x16_f16 v[50:65], v[110:113], v[130:133], v[50:65]
	global_load_dwordx4 v[70:73], v[178:179], off offset:2048
	ds_read_b128 v[110:113], v134 offset:23552
	s_waitcnt lgkmcnt(4)
	v_mfma_f32_32x32x16_f16 v[34:49], v[174:177], v[130:133], v[34:49]
	ds_read_b128 v[174:177], v134 offset:27648
	s_waitcnt lgkmcnt(4)
	v_mfma_f32_32x32x16_f16 v[18:33], v[90:93], v[130:133], v[18:33]
	ds_read_b128 v[90:93], v134 offset:31744
	s_waitcnt lgkmcnt(4)
	v_mfma_f32_32x32x16_f16 v[2:17], v[170:173], v[130:133], v[2:17]
	global_load_dwordx4 v[66:69], v[178:179], off offset:3072
	s_waitcnt vmcnt(12) lgkmcnt(3)
	v_mfma_f32_32x32x16_f16 v[50:65], v[126:129], v[106:109], v[50:65]
	s_waitcnt lgkmcnt(0)
	s_barrier
	ds_read_b128 v[126:129], v134
	ds_read_b128 v[130:133], v134 offset:4096
	v_mfma_f32_32x32x16_f16 v[34:49], v[110:113], v[106:109], v[34:49]
	ds_read_b128 v[110:113], v134 offset:8192
	v_mfma_f32_32x32x16_f16 v[18:33], v[174:177], v[106:109], v[18:33]
	ds_read_b128 v[170:173], v134 offset:12288
	v_mfma_f32_32x32x16_f16 v[2:17], v[90:93], v[106:109], v[2:17]
	ds_read_b128 v[106:109], v134 offset:1024
	s_waitcnt vmcnt(11) lgkmcnt(4)
	v_mfma_f32_32x32x16_f16 v[50:65], v[126:129], v[78:81], v[50:65]
	s_mov_b32 s9, 0xe000
	v_add_co_u32_e32 v178, vcc, s9, v168
	ds_read_b128 v[126:129], v134 offset:5120
	s_nop 0
	v_addc_co_u32_e32 v179, vcc, 0, v169, vcc
	global_load_dwordx4 v[90:93], v[178:179], off offset:-4096
	s_mov_b32 s9, 0xd000
	v_add_co_u32_e32 v180, vcc, s9, v168
	s_waitcnt lgkmcnt(4)
	v_mfma_f32_32x32x16_f16 v[34:49], v[130:133], v[78:81], v[34:49]
	v_addc_co_u32_e32 v181, vcc, 0, v169, vcc
	ds_read_b128 v[130:133], v134 offset:9216
	s_waitcnt lgkmcnt(4)
	v_mfma_f32_32x32x16_f16 v[18:33], v[110:113], v[78:81], v[18:33]
	ds_read_b128 v[110:113], v134 offset:13312
	s_waitcnt lgkmcnt(4)
	v_mfma_f32_32x32x16_f16 v[2:17], v[170:173], v[78:81], v[2:17]
	ds_read_b128 v[78:81], v134 offset:2048
	s_waitcnt vmcnt(11) lgkmcnt(4)
	v_mfma_f32_32x32x16_f16 v[50:65], v[106:109], v[82:85], v[50:65]
	global_load_dwordx4 v[106:109], v[180:181], off offset:1024
	ds_read_b128 v[170:173], v134 offset:6144
	s_waitcnt lgkmcnt(4)
	v_mfma_f32_32x32x16_f16 v[34:49], v[126:129], v[82:85], v[34:49]
	ds_read_b128 v[126:129], v134 offset:10240
	s_waitcnt lgkmcnt(4)
	v_mfma_f32_32x32x16_f16 v[18:33], v[130:133], v[82:85], v[18:33]
	ds_read_b128 v[130:133], v134 offset:14336
	s_waitcnt lgkmcnt(4)
	v_mfma_f32_32x32x16_f16 v[2:17], v[110:113], v[82:85], v[2:17]
	ds_read_b128 v[110:113], v134 offset:3072
	s_waitcnt vmcnt(11) lgkmcnt(4)
	v_mfma_f32_32x32x16_f16 v[50:65], v[78:81], v[98:101], v[50:65]
	global_load_dwordx4 v[82:85], v[180:181], off offset:2048
	ds_read_b128 v[174:177], v134 offset:7168
	s_waitcnt lgkmcnt(4)
	v_mfma_f32_32x32x16_f16 v[34:49], v[170:173], v[98:101], v[34:49]
	ds_read_b128 v[170:173], v134 offset:11264
	s_waitcnt lgkmcnt(4)
	v_mfma_f32_32x32x16_f16 v[18:33], v[126:129], v[98:101], v[18:33]
	ds_read_b128 v[126:129], v134 offset:15360
	s_waitcnt lgkmcnt(4)
	v_mfma_f32_32x32x16_f16 v[2:17], v[130:133], v[98:101], v[2:17]
	global_load_dwordx4 v[78:81], v[180:181], off offset:3072
	s_waitcnt vmcnt(12) lgkmcnt(3)
	v_mfma_f32_32x32x16_f16 v[50:65], v[110:113], v[74:77], v[50:65]
	s_waitcnt lgkmcnt(0)
	s_barrier
	ds_read_b128 v[98:101], v134 offset:16384
	ds_read_b128 v[110:113], v134 offset:20480
	v_mfma_f32_32x32x16_f16 v[34:49], v[174:177], v[74:77], v[34:49]
	ds_read_b128 v[130:133], v134 offset:24576
	v_mfma_f32_32x32x16_f16 v[18:33], v[170:173], v[74:77], v[18:33]
	ds_read_b128 v[170:173], v134 offset:28672
	v_mfma_f32_32x32x16_f16 v[2:17], v[126:129], v[74:77], v[2:17]
	ds_read_b128 v[74:77], v134 offset:17408
	s_waitcnt vmcnt(11) lgkmcnt(4)
	v_mfma_f32_32x32x16_f16 v[50:65], v[98:101], v[114:117], v[50:65]
	global_load_dwordx4 v[98:101], v[178:179], off
	ds_read_b128 v[126:129], v134 offset:21504
	s_waitcnt lgkmcnt(4)
	v_mfma_f32_32x32x16_f16 v[34:49], v[110:113], v[114:117], v[34:49]
	ds_read_b128 v[174:177], v134 offset:25600
	s_waitcnt lgkmcnt(4)
	v_mfma_f32_32x32x16_f16 v[18:33], v[130:133], v[114:117], v[18:33]
	ds_read_b128 v[130:133], v134 offset:29696
	s_waitcnt lgkmcnt(4)
	v_mfma_f32_32x32x16_f16 v[2:17], v[170:173], v[114:117], v[2:17]
	ds_read_b128 v[114:117], v134 offset:18432
	s_waitcnt vmcnt(11) lgkmcnt(4)
	v_mfma_f32_32x32x16_f16 v[50:65], v[74:77], v[118:121], v[50:65]
	global_load_dwordx4 v[110:113], v[178:179], off offset:1024
	ds_read_b128 v[74:77], v134 offset:22528
	s_waitcnt lgkmcnt(4)
	v_mfma_f32_32x32x16_f16 v[34:49], v[126:129], v[118:121], v[34:49]
	ds_read_b128 v[126:129], v134 offset:26624
	s_waitcnt lgkmcnt(4)
	v_mfma_f32_32x32x16_f16 v[18:33], v[174:177], v[118:121], v[18:33]
	ds_read_b128 v[170:173], v134 offset:30720
	s_waitcnt lgkmcnt(4)
	v_mfma_f32_32x32x16_f16 v[2:17], v[130:133], v[118:121], v[2:17]
	ds_read_b128 v[118:121], v134 offset:19456
	s_waitcnt vmcnt(11) lgkmcnt(4)
	v_mfma_f32_32x32x16_f16 v[50:65], v[114:117], v[122:125], v[50:65]
	global_load_dwordx4 v[114:117], v[178:179], off offset:2048
	ds_read_b128 v[130:133], v134 offset:23552
	s_waitcnt lgkmcnt(4)
	v_mfma_f32_32x32x16_f16 v[34:49], v[74:77], v[122:125], v[34:49]
	ds_read_b128 v[174:177], v134 offset:27648
	s_waitcnt lgkmcnt(4)
	v_mfma_f32_32x32x16_f16 v[18:33], v[126:129], v[122:125], v[18:33]
	ds_read_b128 v[126:129], v134 offset:31744
	s_waitcnt lgkmcnt(4)
	v_mfma_f32_32x32x16_f16 v[2:17], v[170:173], v[122:125], v[2:17]
	global_load_dwordx4 v[74:77], v[178:179], off offset:3072
	s_waitcnt vmcnt(12) lgkmcnt(3)
	v_mfma_f32_32x32x16_f16 v[50:65], v[118:121], v[94:97], v[50:65]
	s_waitcnt lgkmcnt(0)
	s_barrier
	ds_read_b128 v[118:121], v134
	ds_read_b128 v[122:125], v134 offset:4096
	v_mfma_f32_32x32x16_f16 v[34:49], v[130:133], v[94:97], v[34:49]
	ds_read_b128 v[130:133], v134 offset:8192
	v_mfma_f32_32x32x16_f16 v[18:33], v[174:177], v[94:97], v[18:33]
	v_mfma_f32_32x32x16_f16 v[2:17], v[126:129], v[94:97], v[2:17]
	ds_read_b128 v[126:129], v134 offset:12288
	ds_read_b128 v[170:173], v134 offset:1024
	s_waitcnt vmcnt(11) lgkmcnt(4)
	v_mfma_f32_32x32x16_f16 v[50:65], v[118:121], v[102:105], v[50:65]
	s_mov_b32 s9, 0xf000
	v_add_co_u32_e32 v174, vcc, s9, v168
	ds_read_b128 v[118:121], v134 offset:5120
	s_nop 0
	v_addc_co_u32_e32 v175, vcc, 0, v169, vcc
	global_load_dwordx4 v[94:97], v[174:175], off
	s_waitcnt lgkmcnt(4)
	v_mfma_f32_32x32x16_f16 v[34:49], v[122:125], v[102:105], v[34:49]
	ds_read_b128 v[122:125], v134 offset:9216
	s_waitcnt lgkmcnt(4)
	v_mfma_f32_32x32x16_f16 v[18:33], v[130:133], v[102:105], v[18:33]
	s_waitcnt lgkmcnt(3)
	v_mfma_f32_32x32x16_f16 v[2:17], v[126:129], v[102:105], v[2:17]
	ds_read_b128 v[126:129], v134 offset:13312
	ds_read_b128 v[130:133], v134 offset:2048
	s_waitcnt vmcnt(11) lgkmcnt(4)
	v_mfma_f32_32x32x16_f16 v[50:65], v[170:173], v[86:89], v[50:65]
	global_load_dwordx4 v[102:105], v[174:175], off offset:1024
	s_waitcnt lgkmcnt(3)
	v_mfma_f32_32x32x16_f16 v[34:49], v[118:121], v[86:89], v[34:49]
	ds_read_b128 v[118:121], v134 offset:6144
	s_waitcnt lgkmcnt(3)
	v_mfma_f32_32x32x16_f16 v[18:33], v[122:125], v[86:89], v[18:33]
	ds_read_b128 v[122:125], v134 offset:10240
	s_waitcnt lgkmcnt(3)
	v_mfma_f32_32x32x16_f16 v[2:17], v[126:129], v[86:89], v[2:17]
	ds_read_b128 v[126:129], v134 offset:14336
	ds_read_b128 v[168:171], v134 offset:3072
	s_waitcnt vmcnt(11) lgkmcnt(4)
	v_mfma_f32_32x32x16_f16 v[50:65], v[130:133], v[70:73], v[50:65]
	global_load_dwordx4 v[86:89], v[174:175], off offset:2048
	s_waitcnt lgkmcnt(3)
	v_mfma_f32_32x32x16_f16 v[34:49], v[118:121], v[70:73], v[34:49]
	ds_read_b128 v[118:121], v134 offset:7168
	s_waitcnt lgkmcnt(3)
	v_mfma_f32_32x32x16_f16 v[18:33], v[122:125], v[70:73], v[18:33]
	ds_read_b128 v[122:125], v134 offset:11264
	s_waitcnt lgkmcnt(3)
	v_mfma_f32_32x32x16_f16 v[2:17], v[126:129], v[70:73], v[2:17]
	ds_read_b128 v[126:129], v134 offset:15360
	global_load_dwordx4 v[70:73], v[174:175], off offset:3072
	s_waitcnt vmcnt(12) lgkmcnt(3)
	v_mfma_f32_32x32x16_f16 v[50:65], v[168:171], v[66:69], v[50:65]
	s_waitcnt lgkmcnt(0)
	s_barrier
	ds_read_b128 v[130:133], v134 offset:16384
	v_mfma_f32_32x32x16_f16 v[34:49], v[118:121], v[66:69], v[34:49]
	ds_read_b128 v[118:121], v134 offset:20480
	v_mfma_f32_32x32x16_f16 v[18:33], v[122:125], v[66:69], v[18:33]
	ds_read_b128 v[122:125], v134 offset:24576
	v_mfma_f32_32x32x16_f16 v[2:17], v[126:129], v[66:69], v[2:17]
	ds_read_b128 v[66:69], v134 offset:28672
	ds_read_b128 v[126:129], v134 offset:17408
	s_waitcnt vmcnt(11) lgkmcnt(4)
	v_mfma_f32_32x32x16_f16 v[50:65], v[130:133], v[90:93], v[50:65]
	ds_read_b128 v[130:133], v134 offset:21504
	s_waitcnt lgkmcnt(4)
	v_mfma_f32_32x32x16_f16 v[34:49], v[118:121], v[90:93], v[34:49]
	ds_read_b128 v[118:121], v134 offset:25600
	s_waitcnt lgkmcnt(4)
	v_mfma_f32_32x32x16_f16 v[18:33], v[122:125], v[90:93], v[18:33]
	ds_read_b128 v[122:125], v134 offset:29696
	s_waitcnt lgkmcnt(4)
	v_mfma_f32_32x32x16_f16 v[2:17], v[66:69], v[90:93], v[2:17]
	ds_read_b128 v[66:69], v134 offset:18432
	s_waitcnt vmcnt(10) lgkmcnt(4)
	v_mfma_f32_32x32x16_f16 v[50:65], v[126:129], v[106:109], v[50:65]
	ds_read_b128 v[90:93], v134 offset:22528
	s_waitcnt lgkmcnt(4)
	v_mfma_f32_32x32x16_f16 v[34:49], v[130:133], v[106:109], v[34:49]
	ds_read_b128 v[126:129], v134 offset:26624
	s_waitcnt lgkmcnt(4)
	v_mfma_f32_32x32x16_f16 v[18:33], v[118:121], v[106:109], v[18:33]
	ds_read_b128 v[118:121], v134 offset:30720
	s_waitcnt lgkmcnt(4)
	v_mfma_f32_32x32x16_f16 v[2:17], v[122:125], v[106:109], v[2:17]
	ds_read_b128 v[106:109], v134 offset:19456
	s_waitcnt vmcnt(9) lgkmcnt(4)
	v_mfma_f32_32x32x16_f16 v[50:65], v[66:69], v[82:85], v[50:65]
	ds_read_b128 v[66:69], v134 offset:23552
	s_waitcnt lgkmcnt(4)
	v_mfma_f32_32x32x16_f16 v[34:49], v[90:93], v[82:85], v[34:49]
	ds_read_b128 v[90:93], v134 offset:27648
	s_waitcnt lgkmcnt(4)
	v_mfma_f32_32x32x16_f16 v[18:33], v[126:129], v[82:85], v[18:33]
	ds_read_b128 v[122:125], v134 offset:31744
	s_waitcnt lgkmcnt(4)
	v_mfma_f32_32x32x16_f16 v[2:17], v[118:121], v[82:85], v[2:17]
	s_waitcnt vmcnt(8) lgkmcnt(3)
	v_mfma_f32_32x32x16_f16 v[50:65], v[106:109], v[78:81], v[50:65]
	s_waitcnt lgkmcnt(0)
	s_barrier
	ds_read_b128 v[82:85], v134
	ds_read_b128 v[106:109], v134 offset:4096
	v_mfma_f32_32x32x16_f16 v[34:49], v[66:69], v[78:81], v[34:49]
	ds_read_b128 v[66:69], v134 offset:8192
	v_mfma_f32_32x32x16_f16 v[18:33], v[90:93], v[78:81], v[18:33]
	ds_read_b128 v[90:93], v134 offset:12288
	v_mfma_f32_32x32x16_f16 v[2:17], v[122:125], v[78:81], v[2:17]
	ds_read_b128 v[78:81], v134 offset:1024
	s_waitcnt vmcnt(7) lgkmcnt(4)
	v_mfma_f32_32x32x16_f16 v[50:65], v[82:85], v[98:101], v[50:65]
	ds_read_b128 v[82:85], v134 offset:5120
	s_waitcnt lgkmcnt(4)
	v_mfma_f32_32x32x16_f16 v[34:49], v[106:109], v[98:101], v[34:49]
	ds_read_b128 v[106:109], v134 offset:9216
	s_waitcnt lgkmcnt(4)
	v_mfma_f32_32x32x16_f16 v[18:33], v[66:69], v[98:101], v[18:33]
	ds_read_b128 v[66:69], v134 offset:13312
	s_waitcnt lgkmcnt(4)
	v_mfma_f32_32x32x16_f16 v[2:17], v[90:93], v[98:101], v[2:17]
	ds_read_b128 v[90:93], v134 offset:2048
	s_waitcnt vmcnt(6) lgkmcnt(4)
	v_mfma_f32_32x32x16_f16 v[50:65], v[78:81], v[110:113], v[50:65]
	ds_read_b128 v[78:81], v134 offset:6144
	s_waitcnt lgkmcnt(4)
	v_mfma_f32_32x32x16_f16 v[34:49], v[82:85], v[110:113], v[34:49]
	ds_read_b128 v[82:85], v134 offset:10240
	s_waitcnt lgkmcnt(4)
	v_mfma_f32_32x32x16_f16 v[18:33], v[106:109], v[110:113], v[18:33]
	ds_read_b128 v[98:101], v134 offset:14336
	s_waitcnt lgkmcnt(4)
	v_mfma_f32_32x32x16_f16 v[2:17], v[66:69], v[110:113], v[2:17]
	ds_read_b128 v[66:69], v134 offset:3072
	s_waitcnt vmcnt(5) lgkmcnt(4)
	v_mfma_f32_32x32x16_f16 v[50:65], v[90:93], v[114:117], v[50:65]
	ds_read_b128 v[90:93], v134 offset:7168
	s_waitcnt lgkmcnt(4)
	v_mfma_f32_32x32x16_f16 v[34:49], v[78:81], v[114:117], v[34:49]
	ds_read_b128 v[78:81], v134 offset:11264
	s_waitcnt lgkmcnt(4)
	v_mfma_f32_32x32x16_f16 v[18:33], v[82:85], v[114:117], v[18:33]
	ds_read_b128 v[82:85], v134 offset:15360
	s_waitcnt lgkmcnt(4)
	v_mfma_f32_32x32x16_f16 v[2:17], v[98:101], v[114:117], v[2:17]
	s_waitcnt vmcnt(4) lgkmcnt(3)
	v_mfma_f32_32x32x16_f16 v[50:65], v[66:69], v[74:77], v[50:65]
	s_waitcnt lgkmcnt(0)
	s_barrier
	ds_read_b128 v[66:69], v134 offset:16384
	ds_read_b128 v[98:101], v134 offset:20480
	v_mfma_f32_32x32x16_f16 v[34:49], v[90:93], v[74:77], v[34:49]
	ds_read_b128 v[90:93], v134 offset:24576
	v_mfma_f32_32x32x16_f16 v[18:33], v[78:81], v[74:77], v[18:33]
	ds_read_b128 v[78:81], v134 offset:28672
	v_mfma_f32_32x32x16_f16 v[2:17], v[82:85], v[74:77], v[2:17]
	ds_read_b128 v[74:77], v134 offset:17408
	s_waitcnt vmcnt(3) lgkmcnt(4)
	v_mfma_f32_32x32x16_f16 v[50:65], v[66:69], v[94:97], v[50:65]
	ds_read_b128 v[66:69], v134 offset:21504
	s_waitcnt lgkmcnt(4)
	v_mfma_f32_32x32x16_f16 v[34:49], v[98:101], v[94:97], v[34:49]
	ds_read_b128 v[82:85], v134 offset:25600
	s_waitcnt lgkmcnt(4)
	v_mfma_f32_32x32x16_f16 v[18:33], v[90:93], v[94:97], v[18:33]
	ds_read_b128 v[90:93], v134 offset:29696
	s_waitcnt lgkmcnt(4)
	v_mfma_f32_32x32x16_f16 v[2:17], v[78:81], v[94:97], v[2:17]
	s_waitcnt vmcnt(2) lgkmcnt(3)
	v_mfma_f32_32x32x16_f16 v[50:65], v[74:77], v[102:105], v[50:65]
	ds_read_b128 v[74:77], v134 offset:18432
	s_waitcnt lgkmcnt(3)
	v_mfma_f32_32x32x16_f16 v[34:49], v[66:69], v[102:105], v[34:49]
	ds_read_b128 v[66:69], v134 offset:22528
	ds_read_b128 v[78:81], v134 offset:26624
	s_waitcnt lgkmcnt(4)
	v_mfma_f32_32x32x16_f16 v[18:33], v[82:85], v[102:105], v[18:33]
	ds_read_b128 v[82:85], v134 offset:30720
	s_waitcnt lgkmcnt(4)
	v_mfma_f32_32x32x16_f16 v[2:17], v[90:93], v[102:105], v[2:17]
	ds_read_b128 v[90:93], v134 offset:19456
	s_waitcnt vmcnt(1) lgkmcnt(4)
	v_mfma_f32_32x32x16_f16 v[50:65], v[74:77], v[86:89], v[50:65]
	ds_read_b128 v[74:77], v134 offset:23552
	s_waitcnt lgkmcnt(4)
	v_mfma_f32_32x32x16_f16 v[34:49], v[66:69], v[86:89], v[34:49]
	ds_read_b128 v[66:69], v134 offset:27648
	s_waitcnt lgkmcnt(4)
	v_mfma_f32_32x32x16_f16 v[18:33], v[78:81], v[86:89], v[18:33]
	ds_read_b128 v[78:81], v134 offset:31744
	s_waitcnt lgkmcnt(4)
	v_mfma_f32_32x32x16_f16 v[2:17], v[82:85], v[86:89], v[2:17]
	s_waitcnt vmcnt(0) lgkmcnt(3)
	v_mfma_f32_32x32x16_f16 v[50:65], v[90:93], v[70:73], v[50:65]
	s_waitcnt lgkmcnt(2)
	v_mfma_f32_32x32x16_f16 v[34:49], v[74:77], v[70:73], v[34:49]
	s_waitcnt lgkmcnt(1)
	v_mfma_f32_32x32x16_f16 v[18:33], v[66:69], v[70:73], v[18:33]
	s_waitcnt lgkmcnt(0)
	v_mfma_f32_32x32x16_f16 v[2:17], v[78:81], v[70:73], v[2:17]
	v_cvt_f32_f16_e32 v66, v166
	v_cvt_f32_f16_sdwa v67, v166 dst_sel:DWORD dst_unused:UNUSED_PAD src0_sel:WORD_1
	v_cvt_f32_f16_e32 v68, v167
	v_cvt_f32_f16_sdwa v69, v167 dst_sel:DWORD dst_unused:UNUSED_PAD src0_sel:WORD_1
	v_cvt_f32_f16_e32 v70, v164
	v_cvt_f32_f16_sdwa v71, v164 dst_sel:DWORD dst_unused:UNUSED_PAD src0_sel:WORD_1
	v_cvt_f32_f16_e32 v72, v165
	v_cvt_f32_f16_sdwa v73, v165 dst_sel:DWORD dst_unused:UNUSED_PAD src0_sel:WORD_1
	v_cvt_f32_f16_e32 v74, v162
	v_cvt_f32_f16_sdwa v75, v162 dst_sel:DWORD dst_unused:UNUSED_PAD src0_sel:WORD_1
	v_pk_fma_f32 v[66:67], v[66:67], v[66:67], 1.0 op_sel_hi:[1,1,0] neg_lo:[1,0,0] neg_hi:[1,0,0]
	v_cvt_f32_f16_e32 v76, v163
	v_cvt_f32_f16_sdwa v77, v163 dst_sel:DWORD dst_unused:UNUSED_PAD src0_sel:WORD_1
	v_pk_mul_f32 v[66:67], v[50:51], v[66:67]
	v_pk_fma_f32 v[50:51], v[68:69], v[68:69], 1.0 op_sel_hi:[1,1,0] neg_lo:[1,0,0] neg_hi:[1,0,0]
	s_nop 0
	v_pk_mul_f32 v[68:69], v[52:53], v[50:51]
	v_pk_fma_f32 v[50:51], v[70:71], v[70:71], 1.0 op_sel_hi:[1,1,0] neg_lo:[1,0,0] neg_hi:[1,0,0]
	s_barrier
	v_pk_mul_f32 v[54:55], v[54:55], v[50:51]
	v_pk_fma_f32 v[50:51], v[72:73], v[72:73], 1.0 op_sel_hi:[1,1,0] neg_lo:[1,0,0] neg_hi:[1,0,0]
	s_nop 0
	v_pk_mul_f32 v[56:57], v[56:57], v[50:51]
	v_pk_fma_f32 v[50:51], v[74:75], v[74:75], 1.0 op_sel_hi:[1,1,0] neg_lo:[1,0,0] neg_hi:[1,0,0]
	v_cvt_f32_f16_e32 v78, v160
	v_pk_mul_f32 v[90:91], v[58:59], v[50:51]
	v_pk_fma_f32 v[50:51], v[76:77], v[76:77], 1.0 op_sel_hi:[1,1,0] neg_lo:[1,0,0] neg_hi:[1,0,0]
	v_cvt_f32_f16_sdwa v79, v160 dst_sel:DWORD dst_unused:UNUSED_PAD src0_sel:WORD_1
	v_pk_mul_f32 v[92:93], v[60:61], v[50:51]
	ds_read_b128 v[50:53], v134 offset:33792
	v_cvt_f32_f16_e32 v86, v161
	v_cvt_f32_f16_sdwa v87, v161 dst_sel:DWORD dst_unused:UNUSED_PAD src0_sel:WORD_1
	v_cvt_pk_f16_f32 v57, v56, v57
	v_cvt_pk_f16_f32 v56, v54, v55
	v_cvt_pk_f16_f32 v55, v68, v69
	v_cvt_pk_f16_f32 v54, v66, v67
	v_pk_fma_f32 v[58:59], v[78:79], v[78:79], 1.0 op_sel_hi:[1,1,0] neg_lo:[1,0,0] neg_hi:[1,0,0]
	v_cvt_f32_f16_e32 v94, v152
	s_waitcnt lgkmcnt(0)
	v_mfma_f32_32x32x16_f16 v[66:81], v[50:53], v[54:57], 0
	v_fma_f32 v50, -v86, v86, 1.0
	v_fma_f32 v51, -v87, v87, 1.0
	v_mul_f32_e64 v62, v62, v58
	v_mul_f32_e64 v63, v63, v59
	ds_read_b128 v[58:61], v134 offset:34816
	ds_read_b128 v[82:85], v134 offset:35840
	v_pk_mul_f32 v[50:51], v[64:65], v[50:51]
	v_cvt_f32_f16_e32 v52, v159
	v_cvt_pk_f16_f32 v89, v50, v51
	v_cvt_f32_f16_e32 v50, v158
	v_cvt_f32_f16_sdwa v51, v158 dst_sel:DWORD dst_unused:UNUSED_PAD src0_sel:WORD_1
	v_cvt_f32_f16_sdwa v53, v159 dst_sel:DWORD dst_unused:UNUSED_PAD src0_sel:WORD_1
	v_cvt_pk_f16_f32 v88, v62, v63
	v_cvt_f32_f16_e32 v62, v156
	v_cvt_f32_f16_sdwa v63, v156 dst_sel:DWORD dst_unused:UNUSED_PAD src0_sel:WORD_1
	v_cvt_pk_f16_f32 v87, v92, v93
	v_cvt_pk_f16_f32 v86, v90, v91
	v_cvt_f32_f16_e32 v64, v157
	v_cvt_f32_f16_sdwa v65, v157 dst_sel:DWORD dst_unused:UNUSED_PAD src0_sel:WORD_1
	s_waitcnt lgkmcnt(0)
	v_mfma_f32_32x32x16_f16 v[66:81], v[82:85], v[86:89], v[66:81]
	v_cvt_f32_f16_e32 v82, v154
	v_cvt_f32_f16_sdwa v83, v154 dst_sel:DWORD dst_unused:UNUSED_PAD src0_sel:WORD_1
	v_fma_f32 v50, -v50, v50, 1.0
	v_fma_f32 v51, -v51, v51, 1.0
	v_cvt_f32_f16_e32 v84, v155
	v_cvt_f32_f16_sdwa v85, v155 dst_sel:DWORD dst_unused:UNUSED_PAD src0_sel:WORD_1
	v_pk_mul_f32 v[98:99], v[34:35], v[50:51]
	v_pk_fma_f32 v[34:35], v[52:53], v[52:53], 1.0 op_sel_hi:[1,1,0] neg_lo:[1,0,0] neg_hi:[1,0,0]
	v_cvt_f32_f16_sdwa v95, v152 dst_sel:DWORD dst_unused:UNUSED_PAD src0_sel:WORD_1
	v_pk_mul_f32 v[100:101], v[36:37], v[34:35]
	v_pk_fma_f32 v[34:35], v[62:63], v[62:63], 1.0 op_sel_hi:[1,1,0] neg_lo:[1,0,0] neg_hi:[1,0,0]
	ds_read_b128 v[90:93], v134 offset:36864
	v_pk_mul_f32 v[38:39], v[38:39], v[34:35]
	v_pk_fma_f32 v[34:35], v[64:65], v[64:65], 1.0 op_sel_hi:[1,1,0] neg_lo:[1,0,0] neg_hi:[1,0,0]
	v_mfma_f32_32x32x16_f16 v[50:65], v[58:61], v[54:57], 0
	v_mul_f32_e64 v40, v40, v34
	v_mul_f32_e64 v41, v41, v35
	v_fma_f32 v34, -v82, v82, 1.0
	v_fma_f32 v35, -v83, v83, 1.0
	v_cvt_pk_f16_f32 v41, v40, v41
	v_pk_mul_f32 v[82:83], v[42:43], v[34:35]
	v_pk_fma_f32 v[34:35], v[84:85], v[84:85], 1.0 op_sel_hi:[1,1,0] neg_lo:[1,0,0] neg_hi:[1,0,0]
	v_cvt_pk_f16_f32 v40, v38, v39
	v_pk_mul_f32 v[84:85], v[44:45], v[34:35]
	v_pk_fma_f32 v[34:35], v[94:95], v[94:95], 1.0 op_sel_hi:[1,1,0] neg_lo:[1,0,0] neg_hi:[1,0,0]
	v_cvt_pk_f16_f32 v39, v100, v101
	v_pk_mul_f32 v[46:47], v[46:47], v[34:35]
	ds_read_b128 v[34:37], v134 offset:37888
	v_cvt_pk_f16_f32 v38, v98, v99
	v_cvt_f32_f16_e32 v96, v153
	v_cvt_f32_f16_sdwa v97, v153 dst_sel:DWORD dst_unused:UNUSED_PAD src0_sel:WORD_1
	s_waitcnt lgkmcnt(0)
	v_mfma_f32_32x32x16_f16 v[66:81], v[34:37], v[38:41], v[66:81]
	v_cvt_f32_f16_e32 v34, v150
	v_cvt_f32_f16_sdwa v35, v150 dst_sel:DWORD dst_unused:UNUSED_PAD src0_sel:WORD_1
	v_cvt_f32_f16_e32 v36, v151
	v_cvt_f32_f16_sdwa v37, v151 dst_sel:DWORD dst_unused:UNUSED_PAD src0_sel:WORD_1
	v_fma_f32 v42, -v96, v96, 1.0
	v_fma_f32 v43, -v97, v97, 1.0
	v_pk_fma_f32 v[34:35], v[34:35], v[34:35], 1.0 op_sel_hi:[1,1,0] neg_lo:[1,0,0] neg_hi:[1,0,0]
	v_pk_mul_f32 v[48:49], v[48:49], v[42:43]
	v_mfma_f32_32x32x16_f16 v[50:65], v[90:93], v[86:89], v[50:65]
	v_cvt_f32_f16_e32 v86, v148
	v_cvt_f32_f16_sdwa v87, v148 dst_sel:DWORD dst_unused:UNUSED_PAD src0_sel:WORD_1
	v_cvt_f32_f16_e32 v88, v149
	v_cvt_f32_f16_sdwa v89, v149 dst_sel:DWORD dst_unused:UNUSED_PAD src0_sel:WORD_1
	v_cvt_f32_f16_e32 v90, v146
	v_cvt_f32_f16_sdwa v91, v146 dst_sel:DWORD dst_unused:UNUSED_PAD src0_sel:WORD_1
	ds_read_b128 v[42:45], v134 offset:38912
	v_cvt_f32_f16_e32 v92, v147
	v_cvt_f32_f16_sdwa v93, v147 dst_sel:DWORD dst_unused:UNUSED_PAD src0_sel:WORD_1
	v_pk_mul_f32 v[34:35], v[18:19], v[34:35]
	v_pk_fma_f32 v[18:19], v[36:37], v[36:37], 1.0 op_sel_hi:[1,1,0] neg_lo:[1,0,0] neg_hi:[1,0,0]
	v_cvt_f32_f16_e32 v94, v144
	v_cvt_f32_f16_sdwa v95, v144 dst_sel:DWORD dst_unused:UNUSED_PAD src0_sel:WORD_1
	v_pk_mul_f32 v[36:37], v[20:21], v[18:19]
	v_pk_fma_f32 v[18:19], v[86:87], v[86:87], 1.0 op_sel_hi:[1,1,0] neg_lo:[1,0,0] neg_hi:[1,0,0]
	v_cvt_f32_f16_e32 v96, v145
	v_pk_mul_f32 v[86:87], v[22:23], v[18:19]
	v_pk_fma_f32 v[18:19], v[88:89], v[88:89], 1.0 op_sel_hi:[1,1,0] neg_lo:[1,0,0] neg_hi:[1,0,0]
	v_cvt_f32_f16_sdwa v97, v145 dst_sel:DWORD dst_unused:UNUSED_PAD src0_sel:WORD_1
	v_pk_mul_f32 v[88:89], v[24:25], v[18:19]
	v_pk_fma_f32 v[18:19], v[90:91], v[90:91], 1.0 op_sel_hi:[1,1,0] neg_lo:[1,0,0] neg_hi:[1,0,0]
	v_cvt_pk_f16_f32 v25, v48, v49
	v_pk_mul_f32 v[90:91], v[26:27], v[18:19]
	v_pk_fma_f32 v[18:19], v[92:93], v[92:93], 1.0 op_sel_hi:[1,1,0] neg_lo:[1,0,0] neg_hi:[1,0,0]
	v_cvt_pk_f16_f32 v24, v46, v47
	v_pk_mul_f32 v[92:93], v[28:29], v[18:19]
	v_pk_fma_f32 v[18:19], v[94:95], v[94:95], 1.0 op_sel_hi:[1,1,0] neg_lo:[1,0,0] neg_hi:[1,0,0]
	ds_read_b128 v[26:29], v134 offset:40960
	v_pk_mul_f32 v[30:31], v[30:31], v[18:19]
	ds_read_b128 v[18:21], v134 offset:39936
	s_waitcnt lgkmcnt(2)
	v_mfma_f32_32x32x16_f16 v[50:65], v[42:45], v[38:41], v[50:65]
	v_cvt_f32_f16_e32 v40, v142
	v_cvt_f32_f16_sdwa v41, v142 dst_sel:DWORD dst_unused:UNUSED_PAD src0_sel:WORD_1
	v_fma_f32 v38, -v96, v96, 1.0
	v_fma_f32 v39, -v97, v97, 1.0
	v_cvt_pk_f16_f32 v23, v84, v85
	v_cvt_pk_f16_f32 v22, v82, v83
	v_pk_mul_f32 v[32:33], v[32:33], v[38:39]
	v_cvt_f32_f16_e32 v38, v143
	s_waitcnt lgkmcnt(0)
	v_mfma_f32_32x32x16_f16 v[66:81], v[18:21], v[22:25], v[66:81]
	v_cvt_f32_f16_sdwa v39, v143 dst_sel:DWORD dst_unused:UNUSED_PAD src0_sel:WORD_1
	v_fma_f32 v18, -v40, v40, 1.0
	v_fma_f32 v19, -v41, v41, 1.0
	s_or_b32 s6, s6, s7
	v_mul_f32_e64 v40, v2, v18
	v_mul_f32_e64 v41, v3, v19
	ds_read_b128 v[18:21], v134 offset:41984
	v_pk_fma_f32 v[2:3], v[38:39], v[38:39], 1.0 op_sel_hi:[1,1,0] neg_lo:[1,0,0] neg_hi:[1,0,0]
	v_cvt_f32_f16_e32 v38, v140
	v_mfma_f32_32x32x16_f16 v[50:65], v[26:29], v[22:25], v[50:65]
	ds_read_b128 v[26:29], v134 offset:43008
	v_cvt_f32_f16_sdwa v39, v140 dst_sel:DWORD dst_unused:UNUSED_PAD src0_sel:WORD_1
	v_cvt_pk_f16_f32 v22, v34, v35
	v_mul_f32_e64 v34, v4, v2
	v_mul_f32_e64 v35, v5, v3
	v_cvt_pk_f16_f32 v25, v88, v89
	v_pk_fma_f32 v[2:3], v[38:39], v[38:39], 1.0 op_sel_hi:[1,1,0] neg_lo:[1,0,0] neg_hi:[1,0,0]
	v_cvt_pk_f16_f32 v24, v86, v87
	v_cvt_pk_f16_f32 v23, v36, v37
	v_pk_mul_f32 v[6:7], v[6:7], v[2:3]
	ds_read_b128 v[2:5], v134 offset:44032
	s_waitcnt lgkmcnt(2)
	v_mfma_f32_32x32x16_f16 v[66:81], v[18:21], v[22:25], v[66:81]
	v_cvt_f32_f16_e32 v18, v141
	v_cvt_f32_f16_sdwa v19, v141 dst_sel:DWORD dst_unused:UNUSED_PAD src0_sel:WORD_1
	v_cvt_pk_f16_f32 v21, v32, v33
	v_cvt_pk_f16_f32 v20, v30, v31
	s_ashr_i32 s7, s6, 31
	s_lshl_b64 s[6:7], s[6:7], 12
	s_add_u32 s2, s2, s6
	s_waitcnt lgkmcnt(1)
	v_mfma_f32_32x32x16_f16 v[50:65], v[26:29], v[22:25], v[50:65]
	ds_read_b128 v[22:25], v134 offset:45056
	v_cvt_f32_f16_e32 v28, v138
	v_cvt_f32_f16_sdwa v29, v138 dst_sel:DWORD dst_unused:UNUSED_PAD src0_sel:WORD_1
	v_fma_f32 v26, -v18, v18, 1.0
	v_fma_f32 v27, -v19, v19, 1.0
	v_cvt_pk_f16_f32 v19, v92, v93
	v_cvt_pk_f16_f32 v18, v90, v91
	v_pk_mul_f32 v[8:9], v[8:9], v[26:27]
	v_cvt_f32_f16_e32 v26, v139
	s_waitcnt lgkmcnt(1)
	v_mfma_f32_32x32x16_f16 v[66:81], v[2:5], v[18:21], v[66:81]
	v_fma_f32 v2, -v28, v28, 1.0
	v_fma_f32 v3, -v29, v29, 1.0
	v_cvt_f32_f16_sdwa v27, v139 dst_sel:DWORD dst_unused:UNUSED_PAD src0_sel:WORD_1
	v_mul_f32_e64 v10, v10, v2
	v_mul_f32_e64 v11, v11, v3
	ds_read_b128 v[2:5], v134 offset:46080
	v_cvt_pk_f16_f32 v9, v8, v9
	v_cvt_pk_f16_f32 v8, v6, v7
	v_cvt_pk_f16_f32 v7, v34, v35
	s_waitcnt lgkmcnt(1)
	v_mfma_f32_32x32x16_f16 v[50:65], v[22:25], v[18:21], v[50:65]
	ds_read_b128 v[18:21], v134 offset:47104
	v_fma_f32 v22, -v26, v26, 1.0
	v_fma_f32 v23, -v27, v27, 1.0
	v_cvt_f32_f16_e32 v24, v136
	v_cvt_f32_f16_sdwa v25, v136 dst_sel:DWORD dst_unused:UNUSED_PAD src0_sel:WORD_1
	v_pk_mul_f32 v[12:13], v[12:13], v[22:23]
	v_cvt_f32_f16_e32 v22, v137
	v_cvt_f32_f16_sdwa v23, v137 dst_sel:DWORD dst_unused:UNUSED_PAD src0_sel:WORD_1
	v_cvt_pk_f16_f32 v6, v40, v41
	s_addc_u32 s3, s3, s7
	s_waitcnt lgkmcnt(1)
	v_mfma_f32_32x32x16_f16 v[66:81], v[2:5], v[6:9], v[66:81]
	v_fma_f32 v2, -v24, v24, 1.0
	v_fma_f32 v3, -v25, v25, 1.0
	v_mul_f32_e64 v14, v14, v2
	v_mul_f32_e64 v15, v15, v3
	ds_read_b128 v[2:5], v134 offset:48128
	s_waitcnt lgkmcnt(1)
	v_mfma_f32_32x32x16_f16 v[50:65], v[18:21], v[6:9], v[50:65]
	v_fma_f32 v6, -v22, v22, 1.0
	v_fma_f32 v7, -v23, v23, 1.0
	v_cvt_pk_f16_f32 v8, v14, v15
	v_mul_f32_e64 v6, v16, v6
	v_mul_f32_e64 v7, v17, v7
	v_cvt_pk_f16_f32 v9, v6, v7
	v_cvt_pk_f16_f32 v7, v12, v13
	v_cvt_pk_f16_f32 v6, v10, v11
	ds_read_b128 v[10:13], v134 offset:49152
	s_waitcnt lgkmcnt(1)
	v_mfma_f32_32x32x16_f16 v[66:81], v[2:5], v[6:9], v[66:81]
	s_waitcnt lgkmcnt(0)
	v_mfma_f32_32x32x16_f16 v[50:65], v[10:13], v[6:9], v[50:65]
	s_nop 9
	v_cvt_pk_f16_f32 v5, v72, v73
	v_cvt_pk_f16_f32 v4, v70, v71
	v_cvt_pk_f16_f32 v3, v68, v69
	v_cvt_pk_f16_f32 v2, v66, v67
	global_store_dwordx4 v134, v[2:5], s[2:3] sc1
	s_nop 1
	v_cvt_pk_f16_f32 v5, v80, v81
	v_cvt_pk_f16_f32 v4, v78, v79
	v_cvt_pk_f16_f32 v3, v76, v77
	v_cvt_pk_f16_f32 v2, v74, v75
	global_store_dwordx4 v134, v[2:5], s[2:3] offset:1024 sc1
	s_nop 1
	v_cvt_pk_f16_f32 v5, v56, v57
	v_cvt_pk_f16_f32 v4, v54, v55
	v_cvt_pk_f16_f32 v3, v52, v53
	v_cvt_pk_f16_f32 v2, v50, v51
	global_store_dwordx4 v134, v[2:5], s[2:3] offset:2048 sc1
	s_nop 1
	v_cvt_pk_f16_f32 v5, v64, v65
	v_cvt_pk_f16_f32 v4, v62, v63
	v_cvt_pk_f16_f32 v3, v60, v61
	v_cvt_pk_f16_f32 v2, v58, v59
	global_store_dwordx4 v134, v[2:5], s[2:3] offset:3072 sc1
	s_cbranch_execnz .LBB3_2
